# v91 + touch loads: P11 PSQ rows before the sort stages (dst v255, 256 VGPRs) and P12 prologue h1 rows of tokens 1..3 while token 0 is processed
# baseline (speedup 1.0000x reference)
; __device__ __forceinline__ void p11_route(Frame& F) {
;     ...
;     for (int item = F.gw; item < (S_ / 16) * PH; item += F.NGW) {
;         const int tile = item >> 3, h = item & 7, t0 = tile * 16;
; #pragma unroll
;         for (int c = 0; c < 2; ++c) {
;             f32x4 acc[8];
; #pragma unroll
;             for (int nt = 0; nt < 8; ++nt) acc[nt] = (f32x4){0.f, 0.f, 0.f, 0.f};
; #pragma unroll
;             for (int ks = 0; ks < 4; ++ks) { const gbf16x8 a = *(const gbf16x8*)(QRY + (size_t)(t0 + l15) * 2048 + h * 256 + c * 128 + 32 * ks + 8 * g);
; #pragma unroll
;                 for (int nt = 0; nt < 8; ++nt) acc[nt] = __builtin_amdgcn_mfma_f32_16x16x32_bf16(a, *(const gbf16x8*)(SK + ((size_t)(h * 2 + c) * PNK + 16 * nt + l15) * 128 + 32 * ks + 8 * g), acc[nt], 0, 0, 0); }
.LBB0_3214:
	s_lshl_b32 s4, s17, 1
	s_and_b32 s18, s4, -16
	s_waitcnt lgkmcnt(0)
	v_or_b32_e32 v126, s18, v150
	v_ashrrev_i32_e32 v127, 31, v126
	v_lshlrev_b64 v[126:127], 12, v[126:127]
	v_lshl_add_u64 v[126:127], v[2:3], 0, v[126:127]
	global_load_dwordx4 v[128:131], v[126:127], off
	global_load_dwordx4 v[132:135], v[4:5], off
	global_load_dwordx4 v[136:139], v[6:7], off
	global_load_dwordx4 v[140:143], v[8:9], off
	global_load_dwordx4 v[144:147], v[10:11], off
	global_load_dwordx4 v[160:163], v[12:13], off
	global_load_dwordx4 v[164:167], v[14:15], off
	global_load_dwordx4 v[168:171], v[16:17], off
	global_load_dwordx4 v[172:175], v[18:19], off
	global_load_dwordx4 v[176:179], v[126:127], off offset:64
	global_load_dwordx4 v[180:183], v[4:5], off offset:64
	global_load_dwordx4 v[184:187], v[20:21], off
	global_load_dwordx4 v[188:191], v[22:23], off
	global_load_dwordx4 v[192:195], v[24:25], off
	global_load_dwordx4 v[196:199], v[26:27], off
	global_load_dwordx4 v[200:203], v[28:29], off
	global_load_dwordx4 v[204:207], v[30:31], off
	global_load_dwordx4 v[208:211], v[32:33], off
	global_load_dwordx4 v[212:215], v[126:127], off offset:128
	global_load_dwordx4 v[216:219], v[4:5], off offset:128
	global_load_dwordx4 v[220:223], v[34:35], off
	global_load_dwordx4 v[224:227], v[36:37], off
	global_load_dwordx4 v[228:231], v[38:39], off
	global_load_dwordx4 v[232:235], v[40:41], off
	global_load_dwordx4 v[236:239], v[42:43], off
	global_load_dwordx4 v[240:243], v[44:45], off
	global_load_dwordx4 v[244:247], v[46:47], off
	s_mov_b32 s4, 0
	v_mov_b32_e32 v148, 0xff800000
	v_mov_b32_e32 v149, 0xff800000
	v_mov_b32_e32 v159, 0xff800000
	s_waitcnt vmcnt(25)
	v_mfma_f32_16x16x32_bf16 v[132:135], v[128:131], v[132:135], 0
	s_waitcnt vmcnt(24)
	v_mfma_f32_16x16x32_bf16 v[136:139], v[128:131], v[136:139], 0
	s_waitcnt vmcnt(23)
	v_mfma_f32_16x16x32_bf16 v[140:143], v[128:131], v[140:143], 0
	s_waitcnt vmcnt(22)
	v_mfma_f32_16x16x32_bf16 v[144:147], v[128:131], v[144:147], 0
	s_waitcnt vmcnt(21)
	v_mfma_f32_16x16x32_bf16 v[160:163], v[128:131], v[160:163], 0
	s_waitcnt vmcnt(20)
	v_mfma_f32_16x16x32_bf16 v[164:167], v[128:131], v[164:167], 0
	s_waitcnt vmcnt(19)
	v_mfma_f32_16x16x32_bf16 v[168:171], v[128:131], v[168:171], 0
	s_waitcnt vmcnt(18)
	v_mfma_f32_16x16x32_bf16 v[128:131], v[128:131], v[172:175], 0
	s_waitcnt vmcnt(16)
	v_mfma_f32_16x16x32_bf16 v[132:135], v[176:179], v[180:183], v[132:135]
	s_waitcnt vmcnt(15)
	v_mfma_f32_16x16x32_bf16 v[136:139], v[176:179], v[184:187], v[136:139]
	s_waitcnt vmcnt(14)
	v_mfma_f32_16x16x32_bf16 v[140:143], v[176:179], v[188:191], v[140:143]
	s_waitcnt vmcnt(13)
	v_mfma_f32_16x16x32_bf16 v[144:147], v[176:179], v[192:195], v[144:147]
	s_waitcnt vmcnt(12)
	v_mfma_f32_16x16x32_bf16 v[160:163], v[176:179], v[196:199], v[160:163]
	s_waitcnt vmcnt(11)
	v_mfma_f32_16x16x32_bf16 v[164:167], v[176:179], v[200:203], v[164:167]
	s_waitcnt vmcnt(10)
	v_mfma_f32_16x16x32_bf16 v[168:171], v[176:179], v[204:207], v[168:171]
	s_waitcnt vmcnt(9)
	v_mfma_f32_16x16x32_bf16 v[128:131], v[176:179], v[208:211], v[128:131]
	global_load_dwordx4 v[176:179], v[126:127], off offset:192
	global_load_dwordx4 v[180:183], v[4:5], off offset:192
	global_load_dwordx4 v[184:187], v[48:49], off
	global_load_dwordx4 v[188:191], v[50:51], off
	global_load_dwordx4 v[192:195], v[52:53], off
	global_load_dwordx4 v[196:199], v[54:55], off
	global_load_dwordx4 v[200:203], v[56:57], off
	global_load_dwordx4 v[204:207], v[58:59], off
	global_load_dwordx4 v[208:211], v[60:61], off
	s_waitcnt vmcnt(16)
	v_mfma_f32_16x16x32_bf16 v[132:135], v[212:215], v[216:219], v[132:135]
	s_waitcnt vmcnt(15)
	v_mfma_f32_16x16x32_bf16 v[136:139], v[212:215], v[220:223], v[136:139]
	s_waitcnt vmcnt(14)
	v_mfma_f32_16x16x32_bf16 v[140:143], v[212:215], v[224:227], v[140:143]
	s_waitcnt vmcnt(13)
	v_mfma_f32_16x16x32_bf16 v[144:147], v[212:215], v[228:231], v[144:147]
	s_waitcnt vmcnt(12)
	v_mfma_f32_16x16x32_bf16 v[160:163], v[212:215], v[232:235], v[160:163]
	s_waitcnt vmcnt(11)
	v_mfma_f32_16x16x32_bf16 v[164:167], v[212:215], v[236:239], v[164:167]
	s_waitcnt vmcnt(10)
	v_mfma_f32_16x16x32_bf16 v[168:171], v[212:215], v[240:243], v[168:171]
	s_waitcnt vmcnt(9)
	v_mfma_f32_16x16x32_bf16 v[128:131], v[212:215], v[244:247], v[128:131]
	s_waitcnt vmcnt(7)
	v_mfma_f32_16x16x32_bf16 v[132:135], v[176:179], v[180:183], v[132:135]
	s_waitcnt vmcnt(6)
	v_mfma_f32_16x16x32_bf16 v[136:139], v[176:179], v[184:187], v[136:139]
	s_waitcnt vmcnt(5)
	v_mfma_f32_16x16x32_bf16 v[140:143], v[176:179], v[188:191], v[140:143]
	s_waitcnt vmcnt(4)
	v_mfma_f32_16x16x32_bf16 v[144:147], v[176:179], v[192:195], v[144:147]
	s_waitcnt vmcnt(3)
	v_mfma_f32_16x16x32_bf16 v[160:163], v[176:179], v[196:199], v[160:163]
	s_waitcnt vmcnt(2)
	v_mfma_f32_16x16x32_bf16 v[164:167], v[176:179], v[200:203], v[164:167]
	s_waitcnt vmcnt(1)
	v_mfma_f32_16x16x32_bf16 v[168:171], v[176:179], v[204:207], v[168:171]
	s_waitcnt vmcnt(0)
; __device__ __forceinline__ void p11_route(Frame& F) {
;     ...
;         for (int c = 0; c < 2; ++c) {
;             f32x4 acc[8];
; #pragma unroll
;             for (int nt = 0; nt < 8; ++nt) acc[nt] = (f32x4){0.f, 0.f, 0.f, 0.f};
; #pragma unroll
;             for (int ks = 0; ks < 4; ++ks) { const gbf16x8 a = *(const gbf16x8*)(QRY + (size_t)(t0 + l15) * 2048 + h * 256 + c * 128 + 32 * ks + 8 * g);
; #pragma unroll
;                 for (int nt = 0; nt < 8; ++nt) acc[nt] = __builtin_amdgcn_mfma_f32_16x16x32_bf16(a, *(const gbf16x8*)(SK + ((size_t)(h * 2 + c) * PNK + 16 * nt + l15) * 128 + 32 * ks + 8 * g), acc[nt], 0, 0, 0); }
; #pragma unroll
;             for (int nt = 0; nt < 8; ++nt)
; #pragma unroll
;                 for (int r = 0; r < 4; ++r) sc[(c * 16 + 4 * g + r) * 129 + 16 * nt + l15] = acc[nt][r];
	v_mfma_f32_16x16x32_bf16 v[128:131], v[176:179], v[208:211], v[128:131]
	s_nop 3
	ds_write2_b32 v151, v132, v136 offset1:16
	ds_write2_b32 v151, v133, v137 offset0:129 offset1:145
	v_add_u32_e32 v132, 0x400, v151
	ds_write2_b32 v132, v134, v138 offset0:2 offset1:18
	ds_write2_b32 v132, v135, v139 offset0:131 offset1:147
	ds_write2_b32 v151, v140, v144 offset0:32 offset1:48
	ds_write2_b32 v151, v141, v145 offset0:161 offset1:177
	ds_write2_b32 v132, v142, v146 offset0:34 offset1:50
	ds_write2_b32 v132, v143, v147 offset0:163 offset1:179
	ds_write2_b32 v151, v160, v164 offset0:64 offset1:80
	ds_write2_b32 v151, v161, v165 offset0:193 offset1:209
	ds_write2_b32 v132, v162, v166 offset0:66 offset1:82
	ds_write2_b32 v132, v163, v167 offset0:195 offset1:211
	ds_write2_b32 v151, v168, v128 offset0:96 offset1:112
	ds_write2_b32 v151, v169, v129 offset0:225 offset1:241
	ds_write2_b32 v132, v170, v130 offset0:98 offset1:114
	ds_write2_b32 v132, v171, v131 offset0:227 offset1:243
	global_load_dwordx4 v[128:131], v[126:127], off offset:256
	global_load_dwordx4 v[132:135], v[62:63], off
	global_load_dwordx4 v[136:139], v[64:65], off
	global_load_dwordx4 v[140:143], v[66:67], off
	global_load_dwordx4 v[144:147], v[68:69], off
	global_load_dwordx4 v[160:163], v[70:71], off
	global_load_dwordx4 v[164:167], v[72:73], off
	global_load_dwordx4 v[168:171], v[74:75], off
	global_load_dwordx4 v[172:175], v[76:77], off
	global_load_dwordx4 v[176:179], v[126:127], off offset:320
	global_load_dwordx4 v[180:183], v[78:79], off
	global_load_dwordx4 v[184:187], v[80:81], off
	global_load_dwordx4 v[188:191], v[82:83], off
	global_load_dwordx4 v[192:195], v[84:85], off
	global_load_dwordx4 v[196:199], v[86:87], off
	global_load_dwordx4 v[200:203], v[88:89], off
	global_load_dwordx4 v[204:207], v[90:91], off
	global_load_dwordx4 v[208:211], v[92:93], off
	global_load_dwordx4 v[212:215], v[126:127], off offset:384
	global_load_dwordx4 v[216:219], v[94:95], off
	global_load_dwordx4 v[220:223], v[96:97], off
	global_load_dwordx4 v[224:227], v[98:99], off
	global_load_dwordx4 v[228:231], v[100:101], off
	global_load_dwordx4 v[232:235], v[102:103], off
	global_load_dwordx4 v[236:239], v[104:105], off
	global_load_dwordx4 v[240:243], v[106:107], off
	global_load_dwordx4 v[244:247], v[108:109], off
	s_waitcnt vmcnt(25)
	v_mfma_f32_16x16x32_bf16 v[132:135], v[128:131], v[132:135], 0
	s_waitcnt vmcnt(24)
	v_mfma_f32_16x16x32_bf16 v[136:139], v[128:131], v[136:139], 0
	s_waitcnt vmcnt(23)
	v_mfma_f32_16x16x32_bf16 v[140:143], v[128:131], v[140:143], 0
	s_waitcnt vmcnt(22)
	v_mfma_f32_16x16x32_bf16 v[144:147], v[128:131], v[144:147], 0
	s_waitcnt vmcnt(21)
	v_mfma_f32_16x16x32_bf16 v[160:163], v[128:131], v[160:163], 0
	s_waitcnt vmcnt(20)
	v_mfma_f32_16x16x32_bf16 v[164:167], v[128:131], v[164:167], 0
	s_waitcnt vmcnt(19)
	v_mfma_f32_16x16x32_bf16 v[168:171], v[128:131], v[168:171], 0
	s_waitcnt vmcnt(18)
	v_mfma_f32_16x16x32_bf16 v[128:131], v[128:131], v[172:175], 0
	s_waitcnt vmcnt(16)
	v_mfma_f32_16x16x32_bf16 v[132:135], v[176:179], v[180:183], v[132:135]
	s_waitcnt vmcnt(15)
	v_mfma_f32_16x16x32_bf16 v[136:139], v[176:179], v[184:187], v[136:139]
	s_waitcnt vmcnt(14)
	v_mfma_f32_16x16x32_bf16 v[140:143], v[176:179], v[188:191], v[140:143]
	s_waitcnt vmcnt(13)
	v_mfma_f32_16x16x32_bf16 v[144:147], v[176:179], v[192:195], v[144:147]
	s_waitcnt vmcnt(12)
	v_mfma_f32_16x16x32_bf16 v[160:163], v[176:179], v[196:199], v[160:163]
	s_waitcnt vmcnt(11)
	v_mfma_f32_16x16x32_bf16 v[164:167], v[176:179], v[200:203], v[164:167]
	s_waitcnt vmcnt(10)
	v_mfma_f32_16x16x32_bf16 v[168:171], v[176:179], v[204:207], v[168:171]
	s_waitcnt vmcnt(9)
	v_mfma_f32_16x16x32_bf16 v[128:131], v[176:179], v[208:211], v[128:131]
	global_load_dwordx4 v[176:179], v[126:127], off offset:448
	global_load_dwordx4 v[180:183], v[110:111], off
	global_load_dwordx4 v[184:187], v[112:113], off
	global_load_dwordx4 v[188:191], v[114:115], off
	global_load_dwordx4 v[192:195], v[116:117], off
	global_load_dwordx4 v[196:199], v[118:119], off
	global_load_dwordx4 v[200:203], v[120:121], off
	global_load_dwordx4 v[204:207], v[122:123], off
	global_load_dwordx4 v[208:211], v[124:125], off
	s_waitcnt vmcnt(16)
	v_mfma_f32_16x16x32_bf16 v[132:135], v[212:215], v[216:219], v[132:135]
	s_waitcnt vmcnt(15)
	v_mfma_f32_16x16x32_bf16 v[136:139], v[212:215], v[220:223], v[136:139]
	s_waitcnt vmcnt(14)
	v_mfma_f32_16x16x32_bf16 v[140:143], v[212:215], v[224:227], v[140:143]
	s_waitcnt vmcnt(13)
	v_mfma_f32_16x16x32_bf16 v[144:147], v[212:215], v[228:231], v[144:147]
	s_waitcnt vmcnt(12)
	v_mfma_f32_16x16x32_bf16 v[160:163], v[212:215], v[232:235], v[160:163]
	s_waitcnt vmcnt(11)
	v_mfma_f32_16x16x32_bf16 v[164:167], v[212:215], v[236:239], v[164:167]
	s_waitcnt vmcnt(10)
	v_mfma_f32_16x16x32_bf16 v[168:171], v[212:215], v[240:243], v[168:171]
	s_waitcnt vmcnt(9)
	v_mfma_f32_16x16x32_bf16 v[128:131], v[212:215], v[244:247], v[128:131]
	s_waitcnt vmcnt(7)
	v_mfma_f32_16x16x32_bf16 v[132:135], v[176:179], v[180:183], v[132:135]
	s_waitcnt vmcnt(6)
	v_mfma_f32_16x16x32_bf16 v[136:139], v[176:179], v[184:187], v[136:139]
	s_waitcnt vmcnt(5)
	v_mfma_f32_16x16x32_bf16 v[140:143], v[176:179], v[188:191], v[140:143]
	s_waitcnt vmcnt(4)
	v_mfma_f32_16x16x32_bf16 v[144:147], v[176:179], v[192:195], v[144:147]
	s_waitcnt vmcnt(3)
	v_mfma_f32_16x16x32_bf16 v[160:163], v[176:179], v[196:199], v[160:163]
	s_waitcnt vmcnt(2)
	v_mfma_f32_16x16x32_bf16 v[164:167], v[176:179], v[200:203], v[164:167]
	s_waitcnt vmcnt(1)
	v_mfma_f32_16x16x32_bf16 v[168:171], v[176:179], v[204:207], v[168:171]
	s_waitcnt vmcnt(0)
; #define LAS __attribute__((address_space(3)))
; __device__ __forceinline__ float uniq_key(float s, int n) { return __uint_as_float((__float_as_uint(s) & ~0xffu) | (unsigned)(255 - n)); }
; #define INS16(A_, X_) do { float x_ = (X_); _Pragma("unroll") for (int i_ = 0; i_ < 16; ++i_) { const float hi_ = fmaxf(A_[i_], x_); x_ = fminf(A_[i_], x_); A_[i_] = hi_; } } while (0)
; __device__ __forceinline__ void p11_route(Frame& F) {
;     ...
;                 for (int r = 0; r < 4; ++r) sc[(c * 16 + 4 * g + r) * 129 + 16 * nt + l15] = acc[nt][r];
;         }
;         { LAS float* row = sc + (F.lane & 31) * 129; float a[16]; const int nb = (F.lane >> 5) * (PNK / 2);
; #pragma unroll
;             for (int i = 0; i < 16; ++i) a[i] = -INFINITY;
; #pragma unroll 4
;             for (int n = 0; n < PNK / 2; ++n) INS16(a, uniq_key(row[nb + n], nb + n));
;     ...
;             float rsn; { const f32x4* pp = (const f32x4*)((const float*)(F.ws + WS_PSQ) + (size_t)t * 64); float q = 0.f;
	v_mfma_f32_16x16x32_bf16 v[126:129], v[176:179], v[208:211], v[128:131]
	s_nop 2
	v_add_u32_e32 v130, 0x2000, v151
	v_add_u32_e32 v131, 0x2400, v151
	ds_write2_b32 v130, v132, v136 offset0:16 offset1:32
	ds_write2_b32 v130, v133, v137 offset0:145 offset1:161
	ds_write2_b32 v131, v134, v138 offset0:18 offset1:34
	ds_write2_b32 v131, v135, v139 offset0:147 offset1:163
	ds_write2_b32 v130, v140, v144 offset0:48 offset1:64
	ds_write2_b32 v130, v141, v145 offset0:177 offset1:193
	ds_write2_b32 v131, v142, v146 offset0:50 offset1:66
	ds_write2_b32 v131, v143, v147 offset0:179 offset1:195
	ds_write2_b32 v130, v160, v164 offset0:80 offset1:96
	ds_write2_b32 v130, v161, v165 offset0:209 offset1:225
	ds_write2_b32 v131, v162, v166 offset0:82 offset1:98
	ds_write2_b32 v131, v163, v167 offset0:211 offset1:227
	ds_write2_b32 v130, v168, v126 offset0:112 offset1:128
	v_add_u32_e32 v126, 0x2200, v151
	ds_write2_b32 v126, v169, v127 offset0:113 offset1:129
	ds_write2_b32 v131, v170, v128 offset0:114 offset1:130
	v_add_u32_e32 v126, 0x2600, v151
	ds_write2_b32 v126, v171, v129 offset0:115 offset1:131
	s_lshl_b32 s46, s18, 8
	s_add_u32 s46, s6, s46
	s_addc_u32 s47, s7, 0
	v_and_b32_e32 v255, 16, v1
	v_lshlrev_b32_e32 v255, 3, v255
	v_lshl_or_b32 v255, v150, 8, v255
	global_load_dword v255, v255, s[46:47]
	ds_read2_b32 v[222:223], v155 offset0:0 offset1:1
	ds_read2_b32 v[224:225], v155 offset0:2 offset1:3
	ds_read2_b32 v[226:227], v155 offset0:4 offset1:5
	ds_read2_b32 v[228:229], v155 offset0:6 offset1:7
	ds_read2_b32 v[230:231], v155 offset0:8 offset1:9
	ds_read2_b32 v[232:233], v155 offset0:10 offset1:11
	ds_read2_b32 v[234:235], v155 offset0:12 offset1:13
	ds_read2_b32 v[236:237], v155 offset0:14 offset1:15
	s_waitcnt lgkmcnt(0)
	ds_read2_b32 v[238:239], v155 offset0:16 offset1:17
	ds_read2_b32 v[240:241], v155 offset0:18 offset1:19
	ds_read2_b32 v[242:243], v155 offset0:20 offset1:21
	ds_read2_b32 v[244:245], v155 offset0:22 offset1:23
	ds_read2_b32 v[246:247], v155 offset0:24 offset1:25
	ds_read2_b32 v[248:249], v155 offset0:26 offset1:27
	ds_read2_b32 v[250:251], v155 offset0:28 offset1:29
	ds_read2_b32 v[252:253], v155 offset0:30 offset1:31
	v_add_u32_e32 v127, 3, v156
	v_and_or_b32 v222, v222, s14, v127
	v_add_u32_e32 v130, 2, v156
	v_and_or_b32 v223, v223, s14, v130
	v_add_u32_e32 v127, 1, v156
	v_and_or_b32 v224, v224, s14, v127
	v_add_u32_e32 v130, 0, v156
	v_and_or_b32 v225, v225, s14, v130
	v_add_u32_e32 v127, -1, v156
	v_and_or_b32 v226, v226, s14, v127
	v_add_u32_e32 v130, -2, v156
	v_and_or_b32 v227, v227, s14, v130
	v_add_u32_e32 v127, -3, v156
	v_and_or_b32 v228, v228, s14, v127
	v_add_u32_e32 v130, -4, v156
	v_and_or_b32 v229, v229, s14, v130
	v_add_u32_e32 v127, -5, v156
	v_and_or_b32 v230, v230, s14, v127
	v_add_u32_e32 v130, -6, v156
	v_and_or_b32 v231, v231, s14, v130
	v_add_u32_e32 v127, -7, v156
	v_and_or_b32 v232, v232, s14, v127
	v_add_u32_e32 v130, -8, v156
	v_and_or_b32 v233, v233, s14, v130
	v_add_u32_e32 v127, -9, v156
	v_and_or_b32 v234, v234, s14, v127
	v_add_u32_e32 v130, -10, v156
	v_and_or_b32 v235, v235, s14, v130
	v_add_u32_e32 v127, -11, v156
	v_and_or_b32 v236, v236, s14, v127
	v_add_u32_e32 v130, -12, v156
	v_and_or_b32 v237, v237, s14, v130
	v_max_f32_e32 v220, v222, v223
	v_min_f32_e32 v223, v222, v223
	v_max_f32_e32 v222, v224, v225
	v_min_f32_e32 v225, v224, v225
	v_max_f32_e32 v224, v220, v222
	v_min_f32_e32 v222, v220, v222
	v_max_f32_e32 v220, v223, v225
	v_min_f32_e32 v225, v223, v225
	v_max_f32_e32 v223, v220, v222
	v_min_f32_e32 v222, v220, v222
	v_max_f32_e32 v220, v226, v227
	v_min_f32_e32 v227, v226, v227
	v_max_f32_e32 v226, v228, v229
	v_min_f32_e32 v229, v228, v229
	v_max_f32_e32 v228, v220, v226
	v_min_f32_e32 v226, v220, v226
	v_max_f32_e32 v220, v227, v229
	v_min_f32_e32 v229, v227, v229
	v_max_f32_e32 v227, v220, v226
	v_min_f32_e32 v226, v220, v226
	v_max_f32_e32 v220, v224, v228
	v_min_f32_e32 v228, v224, v228
	v_max_f32_e32 v224, v222, v226
	v_min_f32_e32 v226, v222, v226
	v_max_f32_e32 v222, v224, v228
	v_min_f32_e32 v228, v224, v228
	v_max_f32_e32 v224, v223, v227
	v_min_f32_e32 v227, v223, v227
	v_max_f32_e32 v223, v225, v229
	v_min_f32_e32 v229, v225, v229
	v_max_f32_e32 v225, v223, v227
	v_min_f32_e32 v227, v223, v227
	v_max_f32_e32 v223, v224, v222
	v_min_f32_e32 v222, v224, v222
	v_max_f32_e32 v224, v225, v228
	v_min_f32_e32 v228, v225, v228
	v_max_f32_e32 v225, v227, v226
	v_min_f32_e32 v226, v227, v226
	v_max_f32_e32 v227, v230, v231
	v_min_f32_e32 v231, v230, v231
	v_max_f32_e32 v230, v232, v233
	v_min_f32_e32 v233, v232, v233
	v_max_f32_e32 v232, v227, v230
	v_min_f32_e32 v230, v227, v230
	v_max_f32_e32 v227, v231, v233
	v_min_f32_e32 v233, v231, v233
	v_max_f32_e32 v231, v227, v230
	v_min_f32_e32 v230, v227, v230
	v_max_f32_e32 v227, v234, v235
	v_min_f32_e32 v235, v234, v235
	v_max_f32_e32 v234, v236, v237
	v_min_f32_e32 v237, v236, v237
	v_max_f32_e32 v236, v227, v234
	v_min_f32_e32 v234, v227, v234
	v_max_f32_e32 v227, v235, v237
	v_min_f32_e32 v237, v235, v237
	v_max_f32_e32 v235, v227, v234
	v_min_f32_e32 v234, v227, v234
	v_max_f32_e32 v227, v232, v236
	v_min_f32_e32 v236, v232, v236
	v_max_f32_e32 v232, v230, v234
	v_min_f32_e32 v234, v230, v234
	v_max_f32_e32 v230, v232, v236
	v_min_f32_e32 v236, v232, v236
	v_max_f32_e32 v232, v231, v235
	v_min_f32_e32 v235, v231, v235
	v_max_f32_e32 v231, v233, v237
	v_min_f32_e32 v237, v233, v237
	v_max_f32_e32 v233, v231, v235
	v_min_f32_e32 v235, v231, v235
	v_max_f32_e32 v231, v232, v230
	v_min_f32_e32 v230, v232, v230
	v_max_f32_e32 v232, v233, v236
	v_min_f32_e32 v236, v233, v236
	v_max_f32_e32 v233, v235, v234
; __device__ __forceinline__ float uniq_key(float s, int n) { return __uint_as_float((__float_as_uint(s) & ~0xffu) | (unsigned)(255 - n)); }
; #define INS16(A_, X_) do { float x_ = (X_); _Pragma("unroll") for (int i_ = 0; i_ < 16; ++i_) { const float hi_ = fmaxf(A_[i_], x_); x_ = fminf(A_[i_], x_); A_[i_] = hi_; } } while (0)
; __device__ __forceinline__ void p11_route(Frame& F) {
;     ...
; #pragma unroll 4
;             for (int n = 0; n < PNK / 2; ++n) INS16(a, uniq_key(row[nb + n], nb + n));
	v_min_f32_e32 v234, v235, v234
	v_max_f32_e32 v235, v220, v227
	v_min_f32_e32 v227, v220, v227
	v_max_f32_e32 v220, v228, v236
	v_min_f32_e32 v236, v228, v236
	v_max_f32_e32 v228, v220, v227
	v_min_f32_e32 v227, v220, v227
	v_max_f32_e32 v220, v222, v230
	v_min_f32_e32 v230, v222, v230
	v_max_f32_e32 v222, v226, v234
	v_min_f32_e32 v234, v226, v234
	v_max_f32_e32 v226, v222, v230
	v_min_f32_e32 v230, v222, v230
	v_max_f32_e32 v222, v220, v228
	v_min_f32_e32 v228, v220, v228
	v_max_f32_e32 v220, v226, v227
	v_min_f32_e32 v227, v226, v227
	v_max_f32_e32 v226, v230, v236
	v_min_f32_e32 v236, v230, v236
	v_max_f32_e32 v230, v223, v231
	v_min_f32_e32 v231, v223, v231
	v_max_f32_e32 v223, v225, v233
	v_min_f32_e32 v233, v225, v233
	v_max_f32_e32 v225, v223, v231
	v_min_f32_e32 v231, v223, v231
	v_max_f32_e32 v223, v224, v232
	v_min_f32_e32 v232, v224, v232
	v_max_f32_e32 v224, v229, v237
	v_min_f32_e32 v237, v229, v237
	v_max_f32_e32 v229, v224, v232
	v_min_f32_e32 v232, v224, v232
	v_max_f32_e32 v224, v223, v225
	v_min_f32_e32 v225, v223, v225
	v_max_f32_e32 v223, v229, v231
	v_min_f32_e32 v231, v229, v231
	v_max_f32_e32 v229, v232, v233
	v_min_f32_e32 v233, v232, v233
	v_max_f32_e32 v232, v230, v222
	v_min_f32_e32 v222, v230, v222
	v_max_f32_e32 v230, v224, v228
	v_min_f32_e32 v228, v224, v228
	v_max_f32_e32 v224, v225, v220
	v_min_f32_e32 v220, v225, v220
	v_max_f32_e32 v225, v223, v227
	v_min_f32_e32 v227, v223, v227
	v_max_f32_e32 v223, v231, v226
	v_min_f32_e32 v226, v231, v226
	v_max_f32_e32 v231, v229, v236
	v_min_f32_e32 v236, v229, v236
	v_max_f32_e32 v229, v233, v234
	v_min_f32_e32 v234, v233, v234
	s_waitcnt lgkmcnt(0)
	v_add_u32_e32 v127, -13, v156
	v_and_or_b32 v238, v238, s14, v127
	v_add_u32_e32 v130, -14, v156
	v_and_or_b32 v239, v239, s14, v130
	v_add_u32_e32 v127, -15, v156
	v_and_or_b32 v240, v240, s14, v127
	v_add_u32_e32 v130, -16, v156
	v_and_or_b32 v241, v241, s14, v130
	v_add_u32_e32 v127, 0xffffffef, v156
	v_and_or_b32 v242, v242, s14, v127
	v_add_u32_e32 v130, 0xffffffee, v156
	v_and_or_b32 v243, v243, s14, v130
	v_add_u32_e32 v127, 0xffffffed, v156
	v_and_or_b32 v244, v244, s14, v127
	v_add_u32_e32 v130, 0xffffffec, v156
	v_and_or_b32 v245, v245, s14, v130
	v_add_u32_e32 v127, 0xffffffeb, v156
	v_and_or_b32 v246, v246, s14, v127
	v_add_u32_e32 v130, 0xffffffea, v156
	v_and_or_b32 v247, v247, s14, v130
	v_add_u32_e32 v127, 0xffffffe9, v156
	v_and_or_b32 v248, v248, s14, v127
	v_add_u32_e32 v130, 0xffffffe8, v156
	v_and_or_b32 v249, v249, s14, v130
	v_add_u32_e32 v127, 0xffffffe7, v156
	v_and_or_b32 v250, v250, s14, v127
	v_add_u32_e32 v130, 0xffffffe6, v156
	v_and_or_b32 v251, v251, s14, v130
	v_add_u32_e32 v127, 0xffffffe5, v156
	v_and_or_b32 v252, v252, s14, v127
	v_add_u32_e32 v130, 0xffffffe4, v156
	v_and_or_b32 v253, v253, s14, v130
	v_max_f32_e32 v128, v238, v239
	v_min_f32_e32 v239, v238, v239
	v_max_f32_e32 v238, v240, v241
	v_min_f32_e32 v241, v240, v241
	v_max_f32_e32 v240, v128, v238
	v_min_f32_e32 v238, v128, v238
	v_max_f32_e32 v128, v239, v241
	v_min_f32_e32 v241, v239, v241
	v_max_f32_e32 v239, v128, v238
	v_min_f32_e32 v238, v128, v238
	v_max_f32_e32 v128, v242, v243
	v_min_f32_e32 v243, v242, v243
	v_max_f32_e32 v242, v244, v245
	v_min_f32_e32 v245, v244, v245
	v_max_f32_e32 v244, v128, v242
	v_min_f32_e32 v242, v128, v242
	v_max_f32_e32 v128, v243, v245
	v_min_f32_e32 v245, v243, v245
	v_max_f32_e32 v243, v128, v242
	v_min_f32_e32 v242, v128, v242
	v_max_f32_e32 v128, v240, v244
	v_min_f32_e32 v244, v240, v244
	v_max_f32_e32 v240, v238, v242
	v_min_f32_e32 v242, v238, v242
	v_max_f32_e32 v238, v240, v244
	v_min_f32_e32 v244, v240, v244
	v_max_f32_e32 v240, v239, v243
	v_min_f32_e32 v243, v239, v243
	v_max_f32_e32 v239, v241, v245
	v_min_f32_e32 v245, v241, v245
	v_max_f32_e32 v241, v239, v243
	v_min_f32_e32 v243, v239, v243
	v_max_f32_e32 v239, v240, v238
	v_min_f32_e32 v238, v240, v238
	v_max_f32_e32 v240, v241, v244
	v_min_f32_e32 v244, v241, v244
	v_max_f32_e32 v241, v243, v242
	v_min_f32_e32 v242, v243, v242
	v_max_f32_e32 v243, v246, v247
	v_min_f32_e32 v247, v246, v247
	v_max_f32_e32 v246, v248, v249
	v_min_f32_e32 v249, v248, v249
	v_max_f32_e32 v248, v243, v246
	v_min_f32_e32 v246, v243, v246
	v_max_f32_e32 v243, v247, v249
	v_min_f32_e32 v249, v247, v249
	v_max_f32_e32 v247, v243, v246
	v_min_f32_e32 v246, v243, v246
	v_max_f32_e32 v243, v250, v251
	v_min_f32_e32 v251, v250, v251
	v_max_f32_e32 v250, v252, v253
	v_min_f32_e32 v253, v252, v253
	v_max_f32_e32 v252, v243, v250
	v_min_f32_e32 v250, v243, v250
	v_max_f32_e32 v243, v251, v253
	v_min_f32_e32 v253, v251, v253
	v_max_f32_e32 v251, v243, v250
	v_min_f32_e32 v250, v243, v250
	v_max_f32_e32 v243, v248, v252
	v_min_f32_e32 v252, v248, v252
	v_max_f32_e32 v248, v246, v250
	v_min_f32_e32 v250, v246, v250
	v_max_f32_e32 v246, v248, v252
	v_min_f32_e32 v252, v248, v252
	v_max_f32_e32 v248, v247, v251
	v_min_f32_e32 v251, v247, v251
	v_max_f32_e32 v247, v249, v253
	v_min_f32_e32 v253, v249, v253
	v_max_f32_e32 v249, v247, v251
	v_min_f32_e32 v251, v247, v251
	v_max_f32_e32 v247, v248, v246
	v_min_f32_e32 v246, v248, v246
	v_max_f32_e32 v248, v249, v252
	v_min_f32_e32 v252, v249, v252
	v_max_f32_e32 v249, v251, v250
	v_min_f32_e32 v250, v251, v250
	v_max_f32_e32 v251, v128, v243
	v_min_f32_e32 v243, v128, v243
	v_max_f32_e32 v128, v244, v252
	v_min_f32_e32 v252, v244, v252
	v_max_f32_e32 v244, v128, v243
	v_min_f32_e32 v243, v128, v243
	v_max_f32_e32 v128, v238, v246
	v_min_f32_e32 v246, v238, v246
	v_max_f32_e32 v238, v242, v250
	v_min_f32_e32 v250, v242, v250
	v_max_f32_e32 v242, v238, v246
	v_min_f32_e32 v246, v238, v246
; __device__ __forceinline__ float uniq_key(float s, int n) { return __uint_as_float((__float_as_uint(s) & ~0xffu) | (unsigned)(255 - n)); }
; #define INS16(A_, X_) do { float x_ = (X_); _Pragma("unroll") for (int i_ = 0; i_ < 16; ++i_) { const float hi_ = fmaxf(A_[i_], x_); x_ = fminf(A_[i_], x_); A_[i_] = hi_; } } while (0)
; __device__ __forceinline__ void p11_route(Frame& F) {
;     ...
; #pragma unroll 4
;             for (int n = 0; n < PNK / 2; ++n) INS16(a, uniq_key(row[nb + n], nb + n));
	v_max_f32_e32 v238, v128, v244
	v_min_f32_e32 v244, v128, v244
	v_max_f32_e32 v128, v242, v243
	v_min_f32_e32 v243, v242, v243
	v_max_f32_e32 v242, v246, v252
	v_min_f32_e32 v252, v246, v252
	v_max_f32_e32 v246, v239, v247
	v_min_f32_e32 v247, v239, v247
	v_max_f32_e32 v239, v241, v249
	v_min_f32_e32 v249, v241, v249
	v_max_f32_e32 v241, v239, v247
	v_min_f32_e32 v247, v239, v247
	v_max_f32_e32 v239, v240, v248
	v_min_f32_e32 v248, v240, v248
	v_max_f32_e32 v240, v245, v253
	v_min_f32_e32 v253, v245, v253
	v_max_f32_e32 v245, v240, v248
	v_min_f32_e32 v248, v240, v248
	v_max_f32_e32 v240, v239, v241
	v_min_f32_e32 v241, v239, v241
	v_max_f32_e32 v239, v245, v247
	v_min_f32_e32 v247, v245, v247
	v_max_f32_e32 v245, v248, v249
	v_min_f32_e32 v249, v248, v249
	v_max_f32_e32 v248, v246, v238
	v_min_f32_e32 v238, v246, v238
	v_max_f32_e32 v246, v240, v244
	v_min_f32_e32 v244, v240, v244
	v_max_f32_e32 v240, v241, v128
	v_min_f32_e32 v128, v241, v128
	v_max_f32_e32 v241, v239, v243
	v_min_f32_e32 v243, v239, v243
	v_max_f32_e32 v239, v247, v242
	v_min_f32_e32 v242, v247, v242
	v_max_f32_e32 v247, v245, v252
	v_min_f32_e32 v252, v245, v252
	v_max_f32_e32 v245, v249, v250
	v_min_f32_e32 v250, v249, v250
	v_max_f32_e32 v235, v235, v253
	v_max_f32_e32 v232, v232, v250
	v_max_f32_e32 v222, v222, v245
	v_max_f32_e32 v230, v230, v252
	v_max_f32_e32 v228, v228, v247
	v_max_f32_e32 v224, v224, v242
	v_max_f32_e32 v220, v220, v239
	v_max_f32_e32 v225, v225, v243
	v_max_f32_e32 v227, v227, v241
	v_max_f32_e32 v223, v223, v128
	v_max_f32_e32 v226, v226, v240
	v_max_f32_e32 v231, v231, v244
	v_max_f32_e32 v236, v236, v246
	v_max_f32_e32 v229, v229, v238
	v_max_f32_e32 v234, v234, v248
	v_max_f32_e32 v237, v237, v251
	ds_read2_b32 v[238:239], v155 offset0:32 offset1:33
	ds_read2_b32 v[240:241], v155 offset0:34 offset1:35
	ds_read2_b32 v[242:243], v155 offset0:36 offset1:37
	ds_read2_b32 v[244:245], v155 offset0:38 offset1:39
	ds_read2_b32 v[246:247], v155 offset0:40 offset1:41
	ds_read2_b32 v[248:249], v155 offset0:42 offset1:43
	ds_read2_b32 v[250:251], v155 offset0:44 offset1:45
	ds_read2_b32 v[252:253], v155 offset0:46 offset1:47
	v_max_f32_e32 v233, v235, v227
	v_min_f32_e32 v227, v235, v227
	v_max_f32_e32 v235, v232, v223
	v_min_f32_e32 v223, v232, v223
	v_max_f32_e32 v232, v222, v226
	v_min_f32_e32 v226, v222, v226
	v_max_f32_e32 v222, v230, v231
	v_min_f32_e32 v231, v230, v231
	v_max_f32_e32 v230, v228, v236
	v_min_f32_e32 v236, v228, v236
	v_max_f32_e32 v228, v224, v229
	v_min_f32_e32 v229, v224, v229
	v_max_f32_e32 v224, v220, v234
	v_min_f32_e32 v234, v220, v234
	v_max_f32_e32 v220, v225, v237
	v_min_f32_e32 v237, v225, v237
	v_max_f32_e32 v225, v233, v230
	v_min_f32_e32 v230, v233, v230
	v_max_f32_e32 v233, v235, v228
	v_min_f32_e32 v228, v235, v228
	v_max_f32_e32 v235, v232, v224
	v_min_f32_e32 v224, v232, v224
	v_max_f32_e32 v232, v222, v220
	v_min_f32_e32 v220, v222, v220
	v_max_f32_e32 v222, v227, v236
	v_min_f32_e32 v236, v227, v236
	v_max_f32_e32 v227, v223, v229
	v_min_f32_e32 v229, v223, v229
	v_max_f32_e32 v223, v226, v234
	v_min_f32_e32 v234, v226, v234
	v_max_f32_e32 v226, v231, v237
	v_min_f32_e32 v237, v231, v237
	v_max_f32_e32 v231, v225, v235
	v_min_f32_e32 v235, v225, v235
	v_max_f32_e32 v225, v233, v232
	v_min_f32_e32 v232, v233, v232
	v_max_f32_e32 v233, v230, v224
	v_min_f32_e32 v224, v230, v224
	v_max_f32_e32 v230, v228, v220
	v_min_f32_e32 v220, v228, v220
	v_max_f32_e32 v228, v222, v223
	v_min_f32_e32 v223, v222, v223
	v_max_f32_e32 v222, v227, v226
	v_min_f32_e32 v226, v227, v226
	v_max_f32_e32 v227, v236, v234
	v_min_f32_e32 v234, v236, v234
	v_max_f32_e32 v236, v229, v237
	v_min_f32_e32 v237, v229, v237
	v_max_f32_e32 v229, v231, v225
	v_min_f32_e32 v225, v231, v225
	v_max_f32_e32 v231, v235, v232
	v_min_f32_e32 v232, v235, v232
	v_max_f32_e32 v235, v233, v230
	v_min_f32_e32 v230, v233, v230
	v_max_f32_e32 v233, v224, v220
	v_min_f32_e32 v220, v224, v220
	v_max_f32_e32 v224, v228, v222
	v_min_f32_e32 v222, v228, v222
	v_max_f32_e32 v228, v223, v226
	v_min_f32_e32 v226, v223, v226
	v_max_f32_e32 v223, v227, v236
	v_min_f32_e32 v236, v227, v236
	v_max_f32_e32 v227, v234, v237
	v_min_f32_e32 v237, v234, v237
	s_waitcnt lgkmcnt(0)
	v_add_u32_e32 v127, 0xffffffe3, v156
	v_and_or_b32 v238, v238, s14, v127
	v_add_u32_e32 v130, 0xffffffe2, v156
	v_and_or_b32 v239, v239, s14, v130
	v_add_u32_e32 v127, 0xffffffe1, v156
	v_and_or_b32 v240, v240, s14, v127
	v_add_u32_e32 v130, 0xffffffe0, v156
	v_and_or_b32 v241, v241, s14, v130
	v_add_u32_e32 v127, 0xffffffdf, v156
	v_and_or_b32 v242, v242, s14, v127
	v_add_u32_e32 v130, 0xffffffde, v156
	v_and_or_b32 v243, v243, s14, v130
	v_add_u32_e32 v127, 0xffffffdd, v156
	v_and_or_b32 v244, v244, s14, v127
	v_add_u32_e32 v130, 0xffffffdc, v156
	v_and_or_b32 v245, v245, s14, v130
	v_add_u32_e32 v127, 0xffffffdb, v156
	v_and_or_b32 v246, v246, s14, v127
	v_add_u32_e32 v130, 0xffffffda, v156
	v_and_or_b32 v247, v247, s14, v130
	v_add_u32_e32 v127, 0xffffffd9, v156
	v_and_or_b32 v248, v248, s14, v127
	v_add_u32_e32 v130, 0xffffffd8, v156
	v_and_or_b32 v249, v249, s14, v130
	v_add_u32_e32 v127, 0xffffffd7, v156
	v_and_or_b32 v250, v250, s14, v127
	v_add_u32_e32 v130, 0xffffffd6, v156
	v_and_or_b32 v251, v251, s14, v130
	v_add_u32_e32 v127, 0xffffffd5, v156
	v_and_or_b32 v252, v252, s14, v127
	v_add_u32_e32 v130, 0xffffffd4, v156
	v_and_or_b32 v253, v253, s14, v130
	v_max_f32_e32 v128, v238, v239
	v_min_f32_e32 v239, v238, v239
	v_max_f32_e32 v238, v240, v241
	v_min_f32_e32 v241, v240, v241
	v_max_f32_e32 v240, v128, v238
	v_min_f32_e32 v238, v128, v238
	v_max_f32_e32 v128, v239, v241
; __device__ __forceinline__ float uniq_key(float s, int n) { return __uint_as_float((__float_as_uint(s) & ~0xffu) | (unsigned)(255 - n)); }
; #define INS16(A_, X_) do { float x_ = (X_); _Pragma("unroll") for (int i_ = 0; i_ < 16; ++i_) { const float hi_ = fmaxf(A_[i_], x_); x_ = fminf(A_[i_], x_); A_[i_] = hi_; } } while (0)
; __device__ __forceinline__ void p11_route(Frame& F) {
;     ...
; #pragma unroll 4
;             for (int n = 0; n < PNK / 2; ++n) INS16(a, uniq_key(row[nb + n], nb + n));
	v_min_f32_e32 v241, v239, v241
	v_max_f32_e32 v239, v128, v238
	v_min_f32_e32 v238, v128, v238
	v_max_f32_e32 v128, v242, v243
	v_min_f32_e32 v243, v242, v243
	v_max_f32_e32 v242, v244, v245
	v_min_f32_e32 v245, v244, v245
	v_max_f32_e32 v244, v128, v242
	v_min_f32_e32 v242, v128, v242
	v_max_f32_e32 v128, v243, v245
	v_min_f32_e32 v245, v243, v245
	v_max_f32_e32 v243, v128, v242
	v_min_f32_e32 v242, v128, v242
	v_max_f32_e32 v128, v240, v244
	v_min_f32_e32 v244, v240, v244
	v_max_f32_e32 v240, v238, v242
	v_min_f32_e32 v242, v238, v242
	v_max_f32_e32 v238, v240, v244
	v_min_f32_e32 v244, v240, v244
	v_max_f32_e32 v240, v239, v243
	v_min_f32_e32 v243, v239, v243
	v_max_f32_e32 v239, v241, v245
	v_min_f32_e32 v245, v241, v245
	v_max_f32_e32 v241, v239, v243
	v_min_f32_e32 v243, v239, v243
	v_max_f32_e32 v239, v240, v238
	v_min_f32_e32 v238, v240, v238
	v_max_f32_e32 v240, v241, v244
	v_min_f32_e32 v244, v241, v244
	v_max_f32_e32 v241, v243, v242
	v_min_f32_e32 v242, v243, v242
	v_max_f32_e32 v243, v246, v247
	v_min_f32_e32 v247, v246, v247
	v_max_f32_e32 v246, v248, v249
	v_min_f32_e32 v249, v248, v249
	v_max_f32_e32 v248, v243, v246
	v_min_f32_e32 v246, v243, v246
	v_max_f32_e32 v243, v247, v249
	v_min_f32_e32 v249, v247, v249
	v_max_f32_e32 v247, v243, v246
	v_min_f32_e32 v246, v243, v246
	v_max_f32_e32 v243, v250, v251
	v_min_f32_e32 v251, v250, v251
	v_max_f32_e32 v250, v252, v253
	v_min_f32_e32 v253, v252, v253
	v_max_f32_e32 v252, v243, v250
	v_min_f32_e32 v250, v243, v250
	v_max_f32_e32 v243, v251, v253
	v_min_f32_e32 v253, v251, v253
	v_max_f32_e32 v251, v243, v250
	v_min_f32_e32 v250, v243, v250
	v_max_f32_e32 v243, v248, v252
	v_min_f32_e32 v252, v248, v252
	v_max_f32_e32 v248, v246, v250
	v_min_f32_e32 v250, v246, v250
	v_max_f32_e32 v246, v248, v252
	v_min_f32_e32 v252, v248, v252
	v_max_f32_e32 v248, v247, v251
	v_min_f32_e32 v251, v247, v251
	v_max_f32_e32 v247, v249, v253
	v_min_f32_e32 v253, v249, v253
	v_max_f32_e32 v249, v247, v251
	v_min_f32_e32 v251, v247, v251
	v_max_f32_e32 v247, v248, v246
	v_min_f32_e32 v246, v248, v246
	v_max_f32_e32 v248, v249, v252
	v_min_f32_e32 v252, v249, v252
	v_max_f32_e32 v249, v251, v250
	v_min_f32_e32 v250, v251, v250
	v_max_f32_e32 v251, v128, v243
	v_min_f32_e32 v243, v128, v243
	v_max_f32_e32 v128, v244, v252
	v_min_f32_e32 v252, v244, v252
	v_max_f32_e32 v244, v128, v243
	v_min_f32_e32 v243, v128, v243
	v_max_f32_e32 v128, v238, v246
	v_min_f32_e32 v246, v238, v246
	v_max_f32_e32 v238, v242, v250
	v_min_f32_e32 v250, v242, v250
	v_max_f32_e32 v242, v238, v246
	v_min_f32_e32 v246, v238, v246
	v_max_f32_e32 v238, v128, v244
	v_min_f32_e32 v244, v128, v244
	v_max_f32_e32 v128, v242, v243
	v_min_f32_e32 v243, v242, v243
	v_max_f32_e32 v242, v246, v252
	v_min_f32_e32 v252, v246, v252
	v_max_f32_e32 v246, v239, v247
	v_min_f32_e32 v247, v239, v247
	v_max_f32_e32 v239, v241, v249
	v_min_f32_e32 v249, v241, v249
	v_max_f32_e32 v241, v239, v247
	v_min_f32_e32 v247, v239, v247
	v_max_f32_e32 v239, v240, v248
	v_min_f32_e32 v248, v240, v248
	v_max_f32_e32 v240, v245, v253
	v_min_f32_e32 v253, v245, v253
	v_max_f32_e32 v245, v240, v248
	v_min_f32_e32 v248, v240, v248
	v_max_f32_e32 v240, v239, v241
	v_min_f32_e32 v241, v239, v241
	v_max_f32_e32 v239, v245, v247
	v_min_f32_e32 v247, v245, v247
	v_max_f32_e32 v245, v248, v249
	v_min_f32_e32 v249, v248, v249
	v_max_f32_e32 v248, v246, v238
	v_min_f32_e32 v238, v246, v238
	v_max_f32_e32 v246, v240, v244
	v_min_f32_e32 v244, v240, v244
	v_max_f32_e32 v240, v241, v128
	v_min_f32_e32 v128, v241, v128
	v_max_f32_e32 v241, v239, v243
	v_min_f32_e32 v243, v239, v243
	v_max_f32_e32 v239, v247, v242
	v_min_f32_e32 v242, v247, v242
	v_max_f32_e32 v247, v245, v252
	v_min_f32_e32 v252, v245, v252
	v_max_f32_e32 v245, v249, v250
	v_min_f32_e32 v250, v249, v250
	v_max_f32_e32 v229, v229, v253
	v_max_f32_e32 v225, v225, v250
	v_max_f32_e32 v231, v231, v245
	v_max_f32_e32 v232, v232, v252
	v_max_f32_e32 v235, v235, v247
	v_max_f32_e32 v230, v230, v242
	v_max_f32_e32 v233, v233, v239
	v_max_f32_e32 v220, v220, v243
	v_max_f32_e32 v224, v224, v241
	v_max_f32_e32 v222, v222, v128
	v_max_f32_e32 v228, v228, v240
	v_max_f32_e32 v226, v226, v244
	v_max_f32_e32 v223, v223, v246
	v_max_f32_e32 v236, v236, v238
	v_max_f32_e32 v227, v227, v248
	v_max_f32_e32 v237, v237, v251
	ds_read2_b32 v[238:239], v155 offset0:48 offset1:49
	ds_read2_b32 v[240:241], v155 offset0:50 offset1:51
	ds_read2_b32 v[242:243], v155 offset0:52 offset1:53
	ds_read2_b32 v[244:245], v155 offset0:54 offset1:55
	ds_read2_b32 v[246:247], v155 offset0:56 offset1:57
	ds_read2_b32 v[248:249], v155 offset0:58 offset1:59
	ds_read2_b32 v[250:251], v155 offset0:60 offset1:61
	ds_read2_b32 v[252:253], v155 offset0:62 offset1:63
	v_max_f32_e32 v234, v229, v224
	v_min_f32_e32 v224, v229, v224
	v_max_f32_e32 v229, v225, v222
	v_min_f32_e32 v222, v225, v222
	v_max_f32_e32 v225, v231, v228
	v_min_f32_e32 v228, v231, v228
	v_max_f32_e32 v231, v232, v226
	v_min_f32_e32 v226, v232, v226
	v_max_f32_e32 v232, v235, v223
	v_min_f32_e32 v223, v235, v223
	v_max_f32_e32 v235, v230, v236
	v_min_f32_e32 v236, v230, v236
	v_max_f32_e32 v230, v233, v227
	v_min_f32_e32 v227, v233, v227
	v_max_f32_e32 v233, v220, v237
	v_min_f32_e32 v237, v220, v237
	v_max_f32_e32 v220, v234, v232
	v_min_f32_e32 v232, v234, v232
	v_max_f32_e32 v234, v229, v235
	v_min_f32_e32 v235, v229, v235
	v_max_f32_e32 v229, v225, v230
	v_min_f32_e32 v230, v225, v230
	v_max_f32_e32 v225, v231, v233
	v_min_f32_e32 v233, v231, v233
	v_max_f32_e32 v231, v224, v223
	v_min_f32_e32 v223, v224, v223
	v_max_f32_e32 v224, v222, v236
	v_min_f32_e32 v236, v222, v236
	v_max_f32_e32 v222, v228, v227
	v_min_f32_e32 v227, v228, v227
	v_max_f32_e32 v228, v226, v237
	v_min_f32_e32 v237, v226, v237
	v_max_f32_e32 v226, v220, v229
	v_min_f32_e32 v229, v220, v229
	v_max_f32_e32 v220, v234, v225
	v_min_f32_e32 v225, v234, v225
	v_max_f32_e32 v234, v232, v230
	v_min_f32_e32 v230, v232, v230
	v_max_f32_e32 v232, v235, v233
	v_min_f32_e32 v233, v235, v233
	v_max_f32_e32 v235, v231, v222
	v_min_f32_e32 v222, v231, v222
	v_max_f32_e32 v231, v224, v228
	v_min_f32_e32 v228, v224, v228
	v_max_f32_e32 v224, v223, v227
	v_min_f32_e32 v227, v223, v227
	v_max_f32_e32 v223, v236, v237
	v_min_f32_e32 v237, v236, v237
	v_max_f32_e32 v236, v226, v220
	v_min_f32_e32 v220, v226, v220
	v_max_f32_e32 v226, v229, v225
	v_min_f32_e32 v225, v229, v225
	v_max_f32_e32 v229, v234, v232
	v_min_f32_e32 v232, v234, v232
	v_max_f32_e32 v234, v230, v233
	v_min_f32_e32 v233, v230, v233
	v_max_f32_e32 v230, v235, v231
	v_min_f32_e32 v231, v235, v231
	v_max_f32_e32 v235, v222, v228
	v_min_f32_e32 v228, v222, v228
	v_max_f32_e32 v222, v224, v223
	v_min_f32_e32 v223, v224, v223
	v_max_f32_e32 v224, v227, v237
	v_min_f32_e32 v237, v227, v237
	s_waitcnt lgkmcnt(0)
; __device__ __forceinline__ float uniq_key(float s, int n) { return __uint_as_float((__float_as_uint(s) & ~0xffu) | (unsigned)(255 - n)); }
; #define INS16(A_, X_) do { float x_ = (X_); _Pragma("unroll") for (int i_ = 0; i_ < 16; ++i_) { const float hi_ = fmaxf(A_[i_], x_); x_ = fminf(A_[i_], x_); A_[i_] = hi_; } } while (0)
; __device__ __forceinline__ void p11_route(Frame& F) {
;     ...
; #pragma unroll 4
;             for (int n = 0; n < PNK / 2; ++n) INS16(a, uniq_key(row[nb + n], nb + n));
	v_add_u32_e32 v127, 0xffffffd3, v156
	v_and_or_b32 v238, v238, s14, v127
	v_add_u32_e32 v130, 0xffffffd2, v156
	v_and_or_b32 v239, v239, s14, v130
	v_add_u32_e32 v127, 0xffffffd1, v156
	v_and_or_b32 v240, v240, s14, v127
	v_add_u32_e32 v130, 0xffffffd0, v156
	v_and_or_b32 v241, v241, s14, v130
	v_add_u32_e32 v127, 0xffffffcf, v156
	v_and_or_b32 v242, v242, s14, v127
	v_add_u32_e32 v130, 0xffffffce, v156
	v_and_or_b32 v243, v243, s14, v130
	v_add_u32_e32 v127, 0xffffffcd, v156
	v_and_or_b32 v244, v244, s14, v127
	v_add_u32_e32 v130, 0xffffffcc, v156
	v_and_or_b32 v245, v245, s14, v130
	v_add_u32_e32 v127, 0xffffffcb, v156
	v_and_or_b32 v246, v246, s14, v127
	v_add_u32_e32 v130, 0xffffffca, v156
	v_and_or_b32 v247, v247, s14, v130
	v_add_u32_e32 v127, 0xffffffc9, v156
	v_and_or_b32 v248, v248, s14, v127
	v_add_u32_e32 v130, 0xffffffc8, v156
	v_and_or_b32 v249, v249, s14, v130
	v_add_u32_e32 v127, 0xffffffc7, v156
	v_and_or_b32 v250, v250, s14, v127
	v_add_u32_e32 v130, 0xffffffc6, v156
	v_and_or_b32 v251, v251, s14, v130
	v_add_u32_e32 v127, 0xffffffc5, v156
	v_and_or_b32 v252, v252, s14, v127
	v_add_u32_e32 v130, 0xffffffc4, v156
	v_and_or_b32 v253, v253, s14, v130
	v_max_f32_e32 v128, v238, v239
	v_min_f32_e32 v239, v238, v239
	v_max_f32_e32 v238, v240, v241
	v_min_f32_e32 v241, v240, v241
	v_max_f32_e32 v240, v128, v238
	v_min_f32_e32 v238, v128, v238
	v_max_f32_e32 v128, v239, v241
	v_min_f32_e32 v241, v239, v241
	v_max_f32_e32 v239, v128, v238
	v_min_f32_e32 v238, v128, v238
	v_max_f32_e32 v128, v242, v243
	v_min_f32_e32 v243, v242, v243
	v_max_f32_e32 v242, v244, v245
	v_min_f32_e32 v245, v244, v245
	v_max_f32_e32 v244, v128, v242
	v_min_f32_e32 v242, v128, v242
	v_max_f32_e32 v128, v243, v245
	v_min_f32_e32 v245, v243, v245
	v_max_f32_e32 v243, v128, v242
	v_min_f32_e32 v242, v128, v242
	v_max_f32_e32 v128, v240, v244
	v_min_f32_e32 v244, v240, v244
	v_max_f32_e32 v240, v238, v242
	v_min_f32_e32 v242, v238, v242
	v_max_f32_e32 v238, v240, v244
	v_min_f32_e32 v244, v240, v244
	v_max_f32_e32 v240, v239, v243
	v_min_f32_e32 v243, v239, v243
	v_max_f32_e32 v239, v241, v245
	v_min_f32_e32 v245, v241, v245
	v_max_f32_e32 v241, v239, v243
	v_min_f32_e32 v243, v239, v243
	v_max_f32_e32 v239, v240, v238
	v_min_f32_e32 v238, v240, v238
	v_max_f32_e32 v240, v241, v244
	v_min_f32_e32 v244, v241, v244
	v_max_f32_e32 v241, v243, v242
	v_min_f32_e32 v242, v243, v242
	v_max_f32_e32 v243, v246, v247
	v_min_f32_e32 v247, v246, v247
	v_max_f32_e32 v246, v248, v249
	v_min_f32_e32 v249, v248, v249
	v_max_f32_e32 v248, v243, v246
	v_min_f32_e32 v246, v243, v246
	v_max_f32_e32 v243, v247, v249
	v_min_f32_e32 v249, v247, v249
	v_max_f32_e32 v247, v243, v246
	v_min_f32_e32 v246, v243, v246
	v_max_f32_e32 v243, v250, v251
	v_min_f32_e32 v251, v250, v251
	v_max_f32_e32 v250, v252, v253
	v_min_f32_e32 v253, v252, v253
	v_max_f32_e32 v252, v243, v250
	v_min_f32_e32 v250, v243, v250
	v_max_f32_e32 v243, v251, v253
	v_min_f32_e32 v253, v251, v253
	v_max_f32_e32 v251, v243, v250
	v_min_f32_e32 v250, v243, v250
	v_max_f32_e32 v243, v248, v252
	v_min_f32_e32 v252, v248, v252
	v_max_f32_e32 v248, v246, v250
	v_min_f32_e32 v250, v246, v250
	v_max_f32_e32 v246, v248, v252
	v_min_f32_e32 v252, v248, v252
	v_max_f32_e32 v248, v247, v251
	v_min_f32_e32 v251, v247, v251
	v_max_f32_e32 v247, v249, v253
	v_min_f32_e32 v253, v249, v253
	v_max_f32_e32 v249, v247, v251
	v_min_f32_e32 v251, v247, v251
	v_max_f32_e32 v247, v248, v246
	v_min_f32_e32 v246, v248, v246
	v_max_f32_e32 v248, v249, v252
	v_min_f32_e32 v252, v249, v252
	v_max_f32_e32 v249, v251, v250
	v_min_f32_e32 v250, v251, v250
	v_max_f32_e32 v251, v128, v243
	v_min_f32_e32 v243, v128, v243
	v_max_f32_e32 v128, v244, v252
	v_min_f32_e32 v252, v244, v252
	v_max_f32_e32 v244, v128, v243
	v_min_f32_e32 v243, v128, v243
	v_max_f32_e32 v128, v238, v246
	v_min_f32_e32 v246, v238, v246
	v_max_f32_e32 v238, v242, v250
	v_min_f32_e32 v250, v242, v250
	v_max_f32_e32 v242, v238, v246
	v_min_f32_e32 v246, v238, v246
	v_max_f32_e32 v238, v128, v244
	v_min_f32_e32 v244, v128, v244
	v_max_f32_e32 v128, v242, v243
	v_min_f32_e32 v243, v242, v243
	v_max_f32_e32 v242, v246, v252
	v_min_f32_e32 v252, v246, v252
	v_max_f32_e32 v246, v239, v247
	v_min_f32_e32 v247, v239, v247
	v_max_f32_e32 v239, v241, v249
	v_min_f32_e32 v249, v241, v249
	v_max_f32_e32 v241, v239, v247
	v_min_f32_e32 v247, v239, v247
	v_max_f32_e32 v239, v240, v248
	v_min_f32_e32 v248, v240, v248
	v_max_f32_e32 v240, v245, v253
	v_min_f32_e32 v253, v245, v253
	v_max_f32_e32 v245, v240, v248
	v_min_f32_e32 v248, v240, v248
	v_max_f32_e32 v240, v239, v241
	v_min_f32_e32 v241, v239, v241
	v_max_f32_e32 v239, v245, v247
	v_min_f32_e32 v247, v245, v247
	v_max_f32_e32 v245, v248, v249
	v_min_f32_e32 v249, v248, v249
	v_max_f32_e32 v248, v246, v238
	v_min_f32_e32 v238, v246, v238
	v_max_f32_e32 v246, v240, v244
	v_min_f32_e32 v244, v240, v244
	v_max_f32_e32 v240, v241, v128
	v_min_f32_e32 v128, v241, v128
	v_max_f32_e32 v241, v239, v243
	v_min_f32_e32 v243, v239, v243
	v_max_f32_e32 v239, v247, v242
	v_min_f32_e32 v242, v247, v242
	v_max_f32_e32 v247, v245, v252
	v_min_f32_e32 v252, v245, v252
	v_max_f32_e32 v245, v249, v250
	v_min_f32_e32 v250, v249, v250
	v_max_f32_e32 v236, v236, v253
	v_max_f32_e32 v220, v220, v250
	v_max_f32_e32 v226, v226, v245
	v_max_f32_e32 v225, v225, v252
	v_max_f32_e32 v229, v229, v247
	v_max_f32_e32 v232, v232, v242
	v_max_f32_e32 v234, v234, v239
	v_max_f32_e32 v233, v233, v243
	v_max_f32_e32 v230, v230, v241
	v_max_f32_e32 v231, v231, v128
	v_max_f32_e32 v235, v235, v240
	v_max_f32_e32 v228, v228, v244
	v_max_f32_e32 v222, v222, v246
; __device__ __forceinline__ float uniq_key(float s, int n) { return __uint_as_float((__float_as_uint(s) & ~0xffu) | (unsigned)(255 - n)); }
; #define INS16(A_, X_) do { float x_ = (X_); _Pragma("unroll") for (int i_ = 0; i_ < 16; ++i_) { const float hi_ = fmaxf(A_[i_], x_); x_ = fminf(A_[i_], x_); A_[i_] = hi_; } } while (0)
; __device__ __forceinline__ void p11_route(Frame& F) {
;     ...
;             for (int n = 0; n < PNK / 2; ++n) INS16(a, uniq_key(row[nb + n], nb + n));
;             float o[16];
; #pragma unroll
;             for (int i = 0; i < 16; ++i) o[i] = __builtin_bit_cast(float, __builtin_amdgcn_ds_bpermute(((F.lane + 32) & 63) << 2, __builtin_bit_cast(int, a[i])));
	v_max_f32_e32 v223, v223, v238
	v_max_f32_e32 v224, v224, v248
	v_max_f32_e32 v237, v237, v251
	v_max_f32_e32 v227, v236, v230
	v_min_f32_e32 v230, v236, v230
	v_max_f32_e32 v236, v220, v231
	v_min_f32_e32 v231, v220, v231
	v_max_f32_e32 v220, v226, v235
	v_min_f32_e32 v235, v226, v235
	v_max_f32_e32 v226, v225, v228
	v_min_f32_e32 v228, v225, v228
	v_max_f32_e32 v225, v229, v222
	v_min_f32_e32 v222, v229, v222
	v_max_f32_e32 v229, v232, v223
	v_min_f32_e32 v223, v232, v223
	v_max_f32_e32 v232, v234, v224
	v_min_f32_e32 v224, v234, v224
	v_max_f32_e32 v234, v233, v237
	v_min_f32_e32 v237, v233, v237
	v_max_f32_e32 v233, v227, v225
	v_min_f32_e32 v225, v227, v225
	v_max_f32_e32 v227, v236, v229
	v_min_f32_e32 v229, v236, v229
	v_max_f32_e32 v236, v220, v232
	v_min_f32_e32 v232, v220, v232
	v_max_f32_e32 v220, v226, v234
	v_min_f32_e32 v234, v226, v234
	v_max_f32_e32 v226, v230, v222
	v_min_f32_e32 v222, v230, v222
	v_max_f32_e32 v230, v231, v223
	v_min_f32_e32 v223, v231, v223
	v_max_f32_e32 v231, v235, v224
	v_min_f32_e32 v224, v235, v224
	v_max_f32_e32 v235, v228, v237
	v_min_f32_e32 v237, v228, v237
	v_max_f32_e32 v228, v233, v236
	v_min_f32_e32 v236, v233, v236
	v_max_f32_e32 v233, v227, v220
	v_min_f32_e32 v220, v227, v220
	v_max_f32_e32 v227, v225, v232
	v_min_f32_e32 v232, v225, v232
	v_max_f32_e32 v225, v229, v234
	v_min_f32_e32 v234, v229, v234
	v_max_f32_e32 v229, v226, v231
	v_min_f32_e32 v231, v226, v231
	v_max_f32_e32 v226, v230, v235
	v_min_f32_e32 v235, v230, v235
	v_max_f32_e32 v230, v222, v224
	v_min_f32_e32 v224, v222, v224
	v_max_f32_e32 v222, v223, v237
	v_min_f32_e32 v237, v223, v237
	v_max_f32_e32 v223, v228, v233
	v_min_f32_e32 v233, v228, v233
	v_max_f32_e32 v228, v236, v220
	v_min_f32_e32 v220, v236, v220
	v_max_f32_e32 v236, v227, v225
	v_min_f32_e32 v225, v227, v225
	v_max_f32_e32 v227, v232, v234
	v_min_f32_e32 v234, v232, v234
	v_max_f32_e32 v232, v229, v226
	v_min_f32_e32 v226, v229, v226
	v_max_f32_e32 v229, v231, v235
	v_min_f32_e32 v235, v231, v235
	v_max_f32_e32 v231, v230, v222
	v_min_f32_e32 v222, v230, v222
	v_max_f32_e32 v230, v224, v237
	v_min_f32_e32 v237, v224, v237
	v_mov_b32_e32 v137, v223
	v_mov_b32_e32 v139, v233
	v_mov_b32_e32 v140, v228
	v_mov_b32_e32 v141, v220
	v_mov_b32_e32 v142, v236
	v_mov_b32_e32 v143, v225
	v_mov_b32_e32 v144, v227
	v_mov_b32_e32 v145, v234
	v_mov_b32_e32 v147, v232
	v_mov_b32_e32 v148, v226
	v_mov_b32_e32 v149, v229
	v_mov_b32_e32 v159, v235
	v_mov_b32_e32 v161, v231
	v_mov_b32_e32 v162, v222
	v_mov_b32_e32 v160, v230
	v_mov_b32_e32 v129, v237
	ds_bpermute_b32 v166, v153, v137
	ds_bpermute_b32 v165, v153, v139
	ds_bpermute_b32 v164, v153, v140
	ds_bpermute_b32 v163, v153, v141
	ds_bpermute_b32 v146, v153, v142
	ds_bpermute_b32 v138, v153, v143
	ds_bpermute_b32 v136, v153, v144
	ds_bpermute_b32 v135, v153, v145
	ds_bpermute_b32 v134, v153, v147
	ds_bpermute_b32 v133, v153, v148
	ds_bpermute_b32 v132, v153, v149
	ds_bpermute_b32 v131, v153, v159
	ds_bpermute_b32 v130, v153, v161
	ds_bpermute_b32 v128, v153, v162
	ds_bpermute_b32 v127, v153, v160
	ds_bpermute_b32 v126, v153, v129
	s_and_saveexec_b64 s[4:5], s[0:1]
	s_cbranch_execz .LBB0_3218
; #define INS16(A_, X_) do { float x_ = (X_); _Pragma("unroll") for (int i_ = 0; i_ < 16; ++i_) { const float hi_ = fmaxf(A_[i_], x_); x_ = fminf(A_[i_], x_); A_[i_] = hi_; } } while (0)
; __device__ __forceinline__ void p11_route(Frame& F) {
;     ...
;             for (int i = 0; i < 16; ++i) INS16(a, o[i]);
;           if (F.lane < 32) {
;             float tv[16]; int ti[16];
; #pragma unroll
;             for (int i = 0; i < 16; ++i) { ti[i] = 255 - (int)(__float_as_uint(a[i]) & 255u); tv[i] = row[ti[i]]; }
; #pragma unroll
;             for (int i = 0; i < 16; ++i) { row[i] = tv[i]; row[16 + i] = __int_as_float(ti[i]); }
	s_waitcnt lgkmcnt(0)
	v_max_f32_e32 v222, v137, v126
	v_max_f32_e32 v223, v139, v127
	v_max_f32_e32 v224, v140, v128
	v_max_f32_e32 v225, v141, v130
	v_max_f32_e32 v226, v142, v131
	v_max_f32_e32 v227, v143, v132
	v_max_f32_e32 v228, v144, v133
	v_max_f32_e32 v229, v145, v134
	v_max_f32_e32 v230, v147, v135
	v_max_f32_e32 v231, v148, v136
	v_max_f32_e32 v232, v149, v138
	v_max_f32_e32 v233, v159, v146
	v_max_f32_e32 v234, v161, v163
	v_max_f32_e32 v235, v162, v164
	v_max_f32_e32 v236, v160, v165
	v_max_f32_e32 v237, v129, v166
	v_max_f32_e32 v238, v222, v230
	v_min_f32_e32 v230, v222, v230
	v_max_f32_e32 v222, v223, v231
	v_min_f32_e32 v231, v223, v231
	v_max_f32_e32 v223, v224, v232
	v_min_f32_e32 v232, v224, v232
	v_max_f32_e32 v224, v225, v233
	v_min_f32_e32 v233, v225, v233
	v_max_f32_e32 v225, v226, v234
	v_min_f32_e32 v234, v226, v234
	v_max_f32_e32 v226, v227, v235
	v_min_f32_e32 v235, v227, v235
	v_max_f32_e32 v227, v228, v236
	v_min_f32_e32 v236, v228, v236
	v_max_f32_e32 v228, v229, v237
	v_min_f32_e32 v237, v229, v237
	v_max_f32_e32 v229, v238, v225
	v_min_f32_e32 v225, v238, v225
	v_max_f32_e32 v238, v222, v226
	v_min_f32_e32 v226, v222, v226
	v_max_f32_e32 v222, v223, v227
	v_min_f32_e32 v227, v223, v227
	v_max_f32_e32 v223, v224, v228
	v_min_f32_e32 v228, v224, v228
	v_max_f32_e32 v224, v230, v234
	v_min_f32_e32 v234, v230, v234
	v_max_f32_e32 v230, v231, v235
	v_min_f32_e32 v235, v231, v235
	v_max_f32_e32 v231, v232, v236
	v_min_f32_e32 v236, v232, v236
	v_max_f32_e32 v232, v233, v237
	v_min_f32_e32 v237, v233, v237
	v_max_f32_e32 v233, v229, v222
	v_min_f32_e32 v222, v229, v222
	v_max_f32_e32 v229, v238, v223
	v_min_f32_e32 v223, v238, v223
	v_max_f32_e32 v238, v225, v227
	v_min_f32_e32 v227, v225, v227
	v_max_f32_e32 v225, v226, v228
	v_min_f32_e32 v228, v226, v228
	v_max_f32_e32 v226, v224, v231
	v_min_f32_e32 v231, v224, v231
	v_max_f32_e32 v224, v230, v232
	v_min_f32_e32 v232, v230, v232
	v_max_f32_e32 v230, v234, v236
	v_min_f32_e32 v236, v234, v236
	v_max_f32_e32 v234, v235, v237
	v_min_f32_e32 v237, v235, v237
	v_max_f32_e32 v235, v233, v229
	v_min_f32_e32 v229, v233, v229
	v_max_f32_e32 v233, v222, v223
	v_min_f32_e32 v223, v222, v223
	v_max_f32_e32 v222, v238, v225
	v_min_f32_e32 v225, v238, v225
	v_max_f32_e32 v238, v227, v228
	v_min_f32_e32 v228, v227, v228
	v_max_f32_e32 v227, v226, v224
	v_min_f32_e32 v224, v226, v224
	v_max_f32_e32 v226, v231, v232
	v_min_f32_e32 v232, v231, v232
	v_max_f32_e32 v231, v230, v234
	v_min_f32_e32 v234, v230, v234
	v_max_f32_e32 v230, v236, v237
	v_min_f32_e32 v237, v236, v237
	v_mov_b32_e32 v126, v235
	v_mov_b32_e32 v127, v229
	v_mov_b32_e32 v128, v233
	v_mov_b32_e32 v130, v223
	v_mov_b32_e32 v131, v222
	v_mov_b32_e32 v132, v225
	v_mov_b32_e32 v133, v238
	v_mov_b32_e32 v134, v228
	v_mov_b32_e32 v135, v227
	v_mov_b32_e32 v136, v224
	v_mov_b32_e32 v137, v226
	v_mov_b32_e32 v138, v232
	v_mov_b32_e32 v139, v231
	v_mov_b32_e32 v140, v234
	v_mov_b32_e32 v141, v230
	v_mov_b32_e32 v129, v237
	v_xor_b32_e32 v127, -1, v127
	v_xor_b32_e32 v126, -1, v126
	v_xor_b32_e32 v130, -1, v130
	v_xor_b32_e32 v128, -1, v128
	v_xor_b32_e32 v132, -1, v132
	v_xor_b32_e32 v131, -1, v131
	v_xor_b32_e32 v134, -1, v134
	v_xor_b32_e32 v133, -1, v133
	v_xor_b32_e32 v136, -1, v136
	v_xor_b32_e32 v135, -1, v135
	v_xor_b32_e32 v138, -1, v138
	v_xor_b32_e32 v137, -1, v137
	v_xor_b32_e32 v140, -1, v140
	v_xor_b32_e32 v139, -1, v139
	v_xor_b32_e32 v129, -1, v129
	v_xor_b32_e32 v141, -1, v141
	v_and_b32_e32 v127, 0xff, v127
	v_and_b32_e32 v126, 0xff, v126
	v_and_b32_e32 v130, 0xff, v130
	v_and_b32_e32 v128, 0xff, v128
	v_and_b32_e32 v132, 0xff, v132
	v_and_b32_e32 v131, 0xff, v131
	v_and_b32_e32 v134, 0xff, v134
	v_and_b32_e32 v133, 0xff, v133
	v_and_b32_e32 v136, 0xff, v136
	v_and_b32_e32 v135, 0xff, v135
	v_and_b32_e32 v138, 0xff, v138
	v_and_b32_e32 v137, 0xff, v137
	v_and_b32_e32 v140, 0xff, v140
	v_and_b32_e32 v139, 0xff, v139
	v_and_b32_e32 v129, 0xff, v129
	v_and_b32_e32 v141, 0xff, v141
	v_lshl_add_u32 v142, v126, 2, v152
	v_lshl_add_u32 v143, v127, 2, v152
	v_lshl_add_u32 v144, v128, 2, v152
	v_lshl_add_u32 v145, v130, 2, v152
	v_lshl_add_u32 v146, v131, 2, v152
	v_lshl_add_u32 v147, v132, 2, v152
	v_lshl_add_u32 v148, v133, 2, v152
	v_lshl_add_u32 v149, v134, 2, v152
	v_lshl_add_u32 v159, v135, 2, v152
	v_lshl_add_u32 v160, v136, 2, v152
	v_lshl_add_u32 v161, v137, 2, v152
	v_lshl_add_u32 v162, v138, 2, v152
	v_lshl_add_u32 v163, v139, 2, v152
	v_lshl_add_u32 v164, v140, 2, v152
	v_lshl_add_u32 v165, v141, 2, v152
	v_lshl_add_u32 v166, v129, 2, v152
	ds_read_b32 v142, v142
	ds_read_b32 v143, v143
	ds_read_b32 v144, v144
	ds_read_b32 v145, v145
	ds_read_b32 v146, v146
	ds_read_b32 v147, v147
	ds_read_b32 v148, v148
	ds_read_b32 v149, v149
	ds_read_b32 v159, v159
	ds_read_b32 v160, v160
	ds_read_b32 v161, v161
	ds_read_b32 v162, v162
	ds_read_b32 v163, v163
	ds_read_b32 v164, v164
	ds_read_b32 v165, v165
	ds_read_b32 v166, v166
	s_waitcnt lgkmcnt(14)
	ds_write2_b32 v152, v142, v143 offset1:1
	ds_write2_b32 v152, v126, v127 offset0:16 offset1:17
	s_waitcnt lgkmcnt(14)
	ds_write2_b32 v152, v144, v145 offset0:2 offset1:3
	ds_write2_b32 v152, v128, v130 offset0:18 offset1:19
	s_waitcnt lgkmcnt(14)
	ds_write2_b32 v152, v146, v147 offset0:4 offset1:5
	ds_write2_b32 v152, v131, v132 offset0:20 offset1:21
	s_waitcnt lgkmcnt(14)
	ds_write2_b32 v152, v148, v149 offset0:6 offset1:7
	ds_write2_b32 v152, v133, v134 offset0:22 offset1:23
	s_waitcnt lgkmcnt(14)
	ds_write2_b32 v152, v159, v160 offset0:8 offset1:9
	ds_write2_b32 v152, v135, v136 offset0:24 offset1:25
	s_waitcnt lgkmcnt(14)
	ds_write2_b32 v152, v161, v162 offset0:10 offset1:11
	ds_write2_b32 v152, v137, v138 offset0:26 offset1:27
	s_waitcnt lgkmcnt(14)
	ds_write2_b32 v152, v163, v164 offset0:12 offset1:13
	ds_write2_b32 v152, v139, v140 offset0:28 offset1:29
	s_waitcnt lgkmcnt(14)
	ds_write2_b32 v152, v165, v166 offset0:14 offset1:15
	ds_write2_b32 v152, v141, v129 offset0:30 offset1:31
	s_or_b64 exec, exec, s[4:5]
	s_and_saveexec_b64 s[12:13], s[2:3]
	s_cbranch_execz .LBB0_3213
	s_branch .LBB0_3219

; __device__ __forceinline__ float bflo(unsigned w) { return __uint_as_float(w << 16); }
; __device__ __forceinline__ float bfhi(unsigned w) { return __uint_as_float(w & 0xffff0000u); }
; __device__ __forceinline__ float wave_max(float v) { v = dpp_max16(v); return fmaxf(fmaxf(rdlane(v, 0), rdlane(v, 16)), fmaxf(rdlane(v, 32), rdlane(v, 48))); }
; __device__ __forceinline__ void p12_peer(Frame& F) {
;     ...
;     const int g8 = F.lane >> 3, k8 = F.lane & 7;
;     float sx[4];
; #pragma unroll
;     for (int i = 0; i < 4; ++i) {
;         const int t = F.gw + i * F.NGW; v4u xp[8]; float mxa = 0.f;
; #pragma unroll
;         for (int j = 0; j < 8; ++j) { xp[j] = ((const v4u*)(HN + (size_t)t * D_))[F.lane + 64 * j];
;             mxa = fmaxf(fmaxf(fmaxf(mxa, fmaxf(fabsf(bflo(xp[j].x)), fabsf(bfhi(xp[j].x)))), fmaxf(fabsf(bflo(xp[j].y)), fabsf(bfhi(xp[j].y)))), fmaxf(fmaxf(fabsf(bflo(xp[j].z)), fabsf(bfhi(xp[j].z))), fmaxf(fabsf(bflo(xp[j].w)), fabsf(bfhi(xp[j].w))))); }
;         mxa = wave_max(mxa); const float inv = mxa > 0.f ? 127.0f / mxa : 0.f;
.LBB0_3270:
	s_cmp_gt_i32 s84, 12
	s_cselect_b64 s[0:1], -1, 0
	s_cmp_lt_i32 s85, 13
	s_cselect_b64 s[2:3], -1, 0
	s_or_b64 s[0:1], s[0:1], s[2:3]
	s_and_b64 vcc, exec, s[0:1]
	s_cbranch_vccnz .LBB0_3413
	s_add_u32 s6, s68, 0x23400000
	s_addc_u32 s7, s69, 0
	s_add_u32 s0, s68, 0x7000000
	s_addc_u32 s1, s69, 0
	s_waitcnt lgkmcnt(0)
	s_add_u32 s18, s68, 0xe00000
	s_addc_u32 s19, s69, 0
	s_add_u32 s22, s68, 0x800000
	s_addc_u32 s23, s69, 0
	s_mul_i32 s2, s66, 0x4400
	s_ashr_i32 s95, s94, 31
	s_add_i32 s20, s2, 0
	s_lshl_b64 s[2:3], s[94:95], 13
	v_mbcnt_lo_u32_b32 v92, -1, 0
	v_mbcnt_hi_u32_b32 v92, -1, v92
	s_add_u32 s2, s6, s2
	v_ashrrev_i32_e32 v93, 31, v92
	s_addc_u32 s3, s7, s3
	s_waitcnt vmcnt(7)
	v_lshlrev_b64 v[18:19], 4, v[92:93]
	v_lshl_add_u64 v[0:1], s[2:3], 0, v[18:19]
	global_load_dwordx4 v[12:15], v[0:1], off
	global_load_dwordx4 v[26:29], v[0:1], off offset:1024
	global_load_dwordx4 v[60:63], v[0:1], off offset:2048
	global_load_dwordx4 v[64:67], v[0:1], off offset:3072
	s_movk_i32 s28, 0x1000
	s_waitcnt vmcnt(4)
	v_add_co_u32_e32 v46, vcc, s28, v0
	s_lshl_b64 s[2:3], s[94:95], 8
	s_nop 0
	v_addc_co_u32_e32 v47, vcc, 0, v1, vcc
	global_load_dwordx4 v[0:3], v[46:47], off
	global_load_dwordx4 v[4:7], v[46:47], off offset:1024
	global_load_dwordx4 v[8:11], v[46:47], off offset:2048
	s_add_u32 s4, s22, s2
	s_addc_u32 s5, s23, s3
	s_lshl_b64 s[2:3], s[94:95], 9
	v_lshlrev_b64 v[16:17], 2, v[92:93]
	s_add_u32 s8, s18, s2
	v_lshl_add_u64 v[20:21], s[4:5], 0, v[16:17]
	s_addc_u32 s9, s19, s3
	v_lshl_add_u64 v[22:23], s[8:9], 0, v[16:17]
	s_mov_b32 s29, 0x42fe0000
	s_mov_b32 s21, 0x40c0c00
	v_lshl_add_u32 v25, v92, 3, s20
	s_add_i32 s4, s34, s94
	s_ashr_i32 s5, s4, 31
	s_lshl_b64 s[8:9], s[4:5], 13
	s_add_u32 s8, s6, s8
	v_lshl_add_u32 v24, v92, 1, s20
	s_addc_u32 s9, s7, s9
	v_ashrrev_i32_e32 v94, 3, v92
	v_lshl_add_u32 v93, v94, 1, s20
	v_and_b32_e32 v164, 7, v92
	v_lshlrev_b32_e32 v95, 1, v164
	v_lshlrev_b32_e32 v165, 4, v164
	v_mov_b32_e32 v109, 0
	s_mov_b32 s43, 0x5040100
	v_lshl_add_u32 v166, v164, 5, s20
	s_mov_b32 s44, 0
	v_mov_b32_e32 v108, 0
	v_mov_b32_e32 v110, 0
	v_mov_b32_e32 v111, v109
	v_mov_b32_e32 v112, 0
	v_mov_b32_e32 v113, v109
	v_mov_b32_e32 v114, 0
	v_mov_b32_e32 v115, v109
	v_mov_b32_e32 v116, 0
	v_mov_b32_e32 v117, v109
	v_mov_b32_e32 v118, 0
	v_mov_b32_e32 v119, v109
	v_mov_b32_e32 v120, 0
	v_mov_b32_e32 v121, v109
	v_mov_b32_e32 v122, 0
	v_mov_b32_e32 v123, v109
	v_mov_b32_e32 v124, 0
	v_mov_b32_e32 v125, v109
	v_mov_b32_e32 v126, 0
	v_mov_b32_e32 v127, v109
	v_mov_b32_e32 v128, 0
	v_mov_b32_e32 v129, v109
	v_mov_b32_e32 v130, 0
	v_mov_b32_e32 v131, v109
	v_mov_b32_e32 v132, 0
	v_mov_b32_e32 v133, v109
	v_mov_b32_e32 v134, 0
	v_mov_b32_e32 v135, v109
	v_mov_b32_e32 v136, 0
	v_mov_b32_e32 v137, v109
	v_mov_b32_e32 v138, 0
	v_mov_b32_e32 v139, v109
	v_mov_b32_e32 v140, 0
	v_mov_b32_e32 v141, v109
	v_mov_b32_e32 v142, 0
	v_mov_b32_e32 v143, v109
	v_mov_b32_e32 v144, 0
	v_mov_b32_e32 v145, v109
	v_mov_b32_e32 v146, 0
	v_mov_b32_e32 v147, v109
	v_mov_b32_e32 v148, 0
	v_mov_b32_e32 v149, v109
	v_mov_b32_e32 v150, 0
	v_mov_b32_e32 v151, v109
	s_waitcnt vmcnt(6)
	v_lshlrev_b32_e32 v58, 16, v12
	v_and_b32_e32 v57, 0xffff0000, v12
	v_lshlrev_b32_e32 v56, 16, v13
	v_and_b32_e32 v55, 0xffff0000, v13
	v_lshlrev_b32_e32 v52, 16, v15
	v_and_b32_e32 v51, 0xffff0000, v15
	v_lshlrev_b32_e32 v54, 16, v14
	v_and_b32_e32 v53, 0xffff0000, v14
	s_waitcnt vmcnt(5)
	v_lshlrev_b32_e32 v48, 16, v26
	v_and_b32_e32 v45, 0xffff0000, v26
	v_lshlrev_b32_e32 v38, 16, v29
	v_and_b32_e32 v37, 0xffff0000, v29
	v_max_f32_e64 v12, |v57|, |v57|
	v_max_f32_e64 v13, |v58|, |v58|
	v_max_f32_e64 v14, |v55|, |v55|
	v_max_f32_e64 v15, |v56|, |v56|
	v_max_f32_e64 v32, |v51|, |v51|
	v_max_f32_e64 v35, |v52|, |v52|
	v_lshlrev_b32_e32 v43, 16, v27
	v_and_b32_e32 v41, 0xffff0000, v27
	v_max_f32_e64 v36, |v45|, |v45|
	v_max_f32_e64 v42, |v48|, |v48|
	v_max_f32_e64 v50, |v37|, |v37|
	v_max_f32_e64 v59, |v38|, |v38|
	v_max_f32_e32 v12, v13, v12
	v_max_f32_e32 v13, v15, v14
	v_max_f32_e32 v14, v35, v32
	v_lshlrev_b32_e32 v40, 16, v28
	v_and_b32_e32 v39, 0xffff0000, v28
	s_waitcnt vmcnt(4)
	v_lshlrev_b32_e32 v34, 16, v60
	v_and_b32_e32 v33, 0xffff0000, v60
	v_lshlrev_b32_e32 v31, 16, v61
	v_and_b32_e32 v30, 0xffff0000, v61
	v_max_f32_e64 v44, |v41|, |v41|
	v_max_f32_e64 v49, |v43|, |v43|
	v_max_f32_e32 v15, v42, v36
	v_max_f32_e32 v35, v59, v50
	v_max3_f32 v12, v12, 0, v13
	v_max3_f32 v13, |v54|, |v53|, v14
	v_lshlrev_b32_e32 v29, 16, v62
	v_and_b32_e32 v28, 0xffff0000, v62
	v_lshlrev_b32_e32 v27, 16, v63
	v_and_b32_e32 v26, 0xffff0000, v63
	v_max_f32_e64 v60, |v33|, |v33|
	v_max_f32_e64 v61, |v34|, |v34|
	v_max_f32_e64 v62, |v30|, |v30|
	v_max_f32_e64 v63, |v31|, |v31|
	v_max_f32_e32 v32, v49, v44
	v_max3_f32 v14, |v40|, |v39|, v35
	v_max3_f32 v12, v12, v13, v15
	v_max_f32_e32 v36, v61, v60
	v_max_f32_e32 v42, v63, v62
	v_max3_f32 v12, v12, v32, v14
	v_max_f32_e64 v68, |v26|, |v26|
	v_max3_f32 v32, v12, v36, v42
	v_max_f32_e64 v12, |v27|, |v27|
	v_max_f32_e32 v12, v12, v68
	v_max3_f32 v42, |v29|, |v28|, v12
	global_load_dwordx4 v[12:15], v[46:47], off offset:3072
	s_waitcnt vmcnt(4)
; __device__ __forceinline__ float bflo(unsigned w) { return __uint_as_float(w << 16); }
; __device__ __forceinline__ float bfhi(unsigned w) { return __uint_as_float(w & 0xffff0000u); }
; __device__ __forceinline__ float wave_sum(float v) { v = dpp_add16(v); return (rdlane(v, 0) + rdlane(v, 16)) + (rdlane(v, 32) + rdlane(v, 48)); }
; __device__ __forceinline__ float wave_max(float v) { v = dpp_max16(v); return fmaxf(fmaxf(rdlane(v, 0), rdlane(v, 16)), fmaxf(rdlane(v, 32), rdlane(v, 48))); }
; __device__ __forceinline__ void p12_peer(Frame& F) {
;     ...
;         const int t = F.gw + i * F.NGW; v4u xp[8]; float mxa = 0.f;
; #pragma unroll
;         for (int j = 0; j < 8; ++j) { xp[j] = ((const v4u*)(HN + (size_t)t * D_))[F.lane + 64 * j];
;             mxa = fmaxf(fmaxf(fmaxf(mxa, fmaxf(fabsf(bflo(xp[j].x)), fabsf(bfhi(xp[j].x)))), fmaxf(fabsf(bflo(xp[j].y)), fabsf(bfhi(xp[j].y)))), fmaxf(fmaxf(fabsf(bflo(xp[j].z)), fabsf(bfhi(xp[j].z))), fmaxf(fabsf(bflo(xp[j].w)), fabsf(bfhi(xp[j].w))))); }
;         mxa = wave_max(mxa); const float inv = mxa > 0.f ? 127.0f / mxa : 0.f;
;         const float rsn = 1.0f / sqrtf(wave_sum(PSQ[(size_t)t * 64 + F.lane]) * (1.f / D_) + 1e-6f);
;         sx[i] = mxa * rsn * (1.0f / 127.0f);
	v_lshlrev_b32_e32 v36, 16, v64
	v_and_b32_e32 v35, 0xffff0000, v64
	v_max_f32_e64 v44, |v35|, |v35|
	v_max_f32_e64 v46, |v36|, |v36|
	v_max_f32_e32 v44, v46, v44
	v_lshlrev_b32_e32 v50, 16, v65
	v_and_b32_e32 v47, 0xffff0000, v65
	v_max3_f32 v32, v32, v42, v44
	v_max_f32_e64 v42, |v47|, |v47|
	v_max_f32_e64 v44, |v50|, |v50|
	v_max_f32_e32 v59, v44, v42
	v_lshlrev_b32_e32 v44, 16, v67
	v_and_b32_e32 v42, 0xffff0000, v67
	v_max_f32_e64 v60, |v42|, |v42|
	v_max_f32_e64 v61, |v44|, |v44|
	v_lshlrev_b32_e32 v49, 16, v66
	v_and_b32_e32 v46, 0xffff0000, v66
	v_max_f32_e32 v60, v61, v60
	v_max3_f32 v60, |v49|, |v46|, v60
	v_max3_f32 v59, v32, v59, v60
	global_load_dword v32, v[20:21], off
	global_load_dword v60, v[22:23], off
	global_load_dword v61, v[22:23], off offset:256
	v_lshlrev_b32_e32 v250, 7, v92
	s_add_u32 s48, s68, 0x23400000
	s_addc_u32 s49, s69, 0
	s_mov_b32 s46, s94
	s_add_i32 s46, s46, s34
	s_lshl_b32 s47, s46, 13
	s_add_u32 s50, s48, s47
	s_addc_u32 s51, s49, 0
	global_load_dword v251, v250, s[50:51]
	s_add_i32 s46, s46, s34
	s_lshl_b32 s47, s46, 13
	s_add_u32 s50, s48, s47
	s_addc_u32 s51, s49, 0
	global_load_dword v252, v250, s[50:51]
	s_add_i32 s46, s46, s34
	s_lshl_b32 s47, s46, 13
	s_add_u32 s50, s48, s47
	s_addc_u32 s51, s49, 0
	global_load_dword v253, v250, s[50:51]
	s_waitcnt vmcnt(9)
	v_lshlrev_b32_e32 v20, 16, v0
	v_and_b32_e32 v21, 0xffff0000, v0
	v_max_f32_e64 v0, |v21|, |v21|
	v_max_f32_e64 v22, |v20|, |v20|
	v_max_f32_e32 v0, v22, v0
	v_lshlrev_b32_e32 v22, 16, v1
	v_and_b32_e32 v23, 0xffff0000, v1
	v_max_f32_e64 v1, |v23|, |v23|
	v_max_f32_e64 v62, |v22|, |v22|
	v_max_f32_e32 v1, v62, v1
	v_lshlrev_b32_e32 v63, 16, v3
	v_and_b32_e32 v64, 0xffff0000, v3
	v_max3_f32 v0, v59, v0, v1
	v_lshlrev_b32_e32 v59, 16, v2
	v_and_b32_e32 v62, 0xffff0000, v2
	v_max_f32_e64 v1, |v64|, |v64|
	v_max_f32_e64 v2, |v63|, |v63|
	s_waitcnt vmcnt(8)
	v_lshlrev_b32_e32 v65, 16, v4
	v_and_b32_e32 v66, 0xffff0000, v4
	v_max_f32_e32 v1, v2, v1
	v_max_f32_e64 v2, |v66|, |v66|
	v_max_f32_e64 v3, |v65|, |v65|
	v_max3_f32 v1, |v59|, |v62|, v1
	v_max_f32_e32 v2, v3, v2
	v_lshlrev_b32_e32 v67, 16, v5
	v_and_b32_e32 v68, 0xffff0000, v5
	v_max3_f32 v0, v0, v1, v2
	v_max_f32_e64 v1, |v68|, |v68|
	v_max_f32_e64 v2, |v67|, |v67|
	v_lshlrev_b32_e32 v70, 16, v7
	v_and_b32_e32 v7, 0xffff0000, v7
	v_max_f32_e32 v1, v2, v1
	v_max_f32_e64 v2, |v7|, |v7|
	v_max_f32_e64 v3, |v70|, |v70|
	v_lshlrev_b32_e32 v69, 16, v6
	v_and_b32_e32 v6, 0xffff0000, v6
	v_max_f32_e32 v2, v3, v2
	v_max3_f32 v2, |v69|, |v6|, v2
	s_waitcnt vmcnt(7)
	v_lshlrev_b32_e32 v71, 16, v8
	v_and_b32_e32 v8, 0xffff0000, v8
	v_max3_f32 v0, v0, v1, v2
	v_max_f32_e64 v1, |v8|, |v8|
	v_max_f32_e64 v2, |v71|, |v71|
	v_lshlrev_b32_e32 v72, 16, v9
	v_and_b32_e32 v9, 0xffff0000, v9
	v_max_f32_e32 v1, v2, v1
	v_max_f32_e64 v2, |v9|, |v9|
	v_max_f32_e64 v3, |v72|, |v72|
	v_max_f32_e32 v2, v3, v2
	v_lshlrev_b32_e32 v74, 16, v11
	v_and_b32_e32 v11, 0xffff0000, v11
	v_max3_f32 v0, v0, v1, v2
	v_max_f32_e64 v1, |v11|, |v11|
	v_max_f32_e64 v2, |v74|, |v74|
	v_lshlrev_b32_e32 v73, 16, v10
	v_and_b32_e32 v10, 0xffff0000, v10
	v_max_f32_e32 v1, v2, v1
	v_max3_f32 v1, |v73|, |v10|, v1
	s_waitcnt vmcnt(6)
	v_lshlrev_b32_e32 v75, 16, v12
	v_and_b32_e32 v12, 0xffff0000, v12
	v_max_f32_e64 v2, |v12|, |v12|
	v_max_f32_e64 v3, |v75|, |v75|
	v_max_f32_e32 v2, v3, v2
	v_lshlrev_b32_e32 v76, 16, v13
	v_and_b32_e32 v13, 0xffff0000, v13
	v_max3_f32 v0, v0, v1, v2
	v_max_f32_e64 v1, |v13|, |v13|
	v_max_f32_e64 v2, |v76|, |v76|
	v_lshlrev_b32_e32 v78, 16, v15
	v_and_b32_e32 v15, 0xffff0000, v15
	v_max_f32_e32 v1, v2, v1
	v_max_f32_e64 v2, |v15|, |v15|
	v_max_f32_e64 v3, |v78|, |v78|
	v_lshlrev_b32_e32 v77, 16, v14
	v_and_b32_e32 v14, 0xffff0000, v14
	v_max_f32_e32 v2, v3, v2
	v_max3_f32 v2, |v77|, |v14|, v2
	v_max3_f32 v0, v0, v1, v2
	v_mov_b32_e32 v1, 0
	s_waitcnt vmcnt(5)
	v_add_f32_dpp v32, v32, v32 quad_perm:[1,0,3,2] row_mask:0xf bank_mask:0xf bound_ctrl:1
	v_mov_b32_e32 v152, 0
	v_mov_b32_dpp v1, v0 quad_perm:[1,0,3,2] row_mask:0xf bank_mask:0xf
	v_max_f32_e32 v1, v1, v1
	v_max_f32_e32 v0, v0, v1
	v_mov_b32_e32 v1, 0
	v_add_f32_dpp v32, v32, v32 quad_perm:[2,3,0,1] row_mask:0xf bank_mask:0xf bound_ctrl:1
	v_mov_b32_e32 v153, v109
	v_mov_b32_dpp v1, v0 quad_perm:[2,3,0,1] row_mask:0xf bank_mask:0xf
	v_max_f32_e32 v1, v1, v1
	v_max_f32_e32 v0, v0, v1
	v_mov_b32_e32 v1, 0
	v_add_f32_dpp v32, v32, v32 row_half_mirror row_mask:0xf bank_mask:0xf bound_ctrl:1
	v_mov_b32_e32 v154, 0
	v_mov_b32_dpp v1, v0 row_half_mirror row_mask:0xf bank_mask:0xf
	v_max_f32_e32 v1, v1, v1
	v_max_f32_e32 v0, v0, v1
	v_mov_b32_e32 v1, 0
	v_add_f32_dpp v32, v32, v32 row_mirror row_mask:0xf bank_mask:0xf bound_ctrl:1
	v_mov_b32_e32 v155, v109
	v_mov_b32_dpp v1, v0 row_mirror row_mask:0xf bank_mask:0xf
	v_max_f32_e32 v1, v1, v1
	v_max_f32_e32 v0, v0, v1
	v_readlane_b32 s39, v32, 0
	v_readlane_b32 s12, v0, 32
	v_readlane_b32 s13, v0, 48
	v_readlane_b32 s10, v0, 0
	v_readlane_b32 s11, v0, 16
	v_max_f32_e64 v0, s13, s13
	v_max_f32_e64 v1, s12, s12
	v_max_f32_e32 v0, v1, v0
	v_mov_b32_e32 v1, s11
	v_max3_f32 v163, s10, v1, v0
	v_div_scale_f32 v2, s[10:11], v163, v163, s29
	v_rcp_f32_e32 v3, v2
	v_lshl_add_u64 v[0:1], s[8:9], 0, v[18:19]
	s_lshl_b64 s[8:9], s[4:5], 8
	s_add_u32 s8, s22, s8
	v_fma_f32 v4, -v2, v3, 1.0
	v_fmac_f32_e32 v3, v4, v3
	v_div_scale_f32 v4, vcc, s29, v163, s29
	v_mul_f32_e32 v5, v4, v3
	v_fma_f32 v79, -v2, v5, v4
	v_fmac_f32_e32 v5, v79, v3
	v_fma_f32 v2, -v2, v5, v4
	v_div_fmas_f32 v2, v2, v3, v5
	v_div_fixup_f32 v2, v2, v163, s29
	v_cmp_lt_f32_e32 vcc, 0, v163
	s_addc_u32 s9, s23, s9
	s_lshl_b64 s[16:17], s[4:5], 9
; #define LAS __attribute__((address_space(3)))
; __device__ __forceinline__ float bflo(unsigned w) { return __uint_as_float(w << 16); }
; __device__ __forceinline__ float bfhi(unsigned w) { return __uint_as_float(w & 0xffff0000u); }
; __device__ __forceinline__ void p12_peer(Frame& F) {
;     ...
; #pragma unroll
;         for (int j = 0; j < 8; ++j) {
;             const int q0 = (int)rintf(bflo(xp[j].x) * inv), q1 = (int)rintf(bfhi(xp[j].x) * inv), q2 = (int)rintf(bflo(xp[j].y) * inv), q3 = (int)rintf(bfhi(xp[j].y) * inv);
;             const int q4 = (int)rintf(bflo(xp[j].z) * inv), q5 = (int)rintf(bfhi(xp[j].z) * inv), q6 = (int)rintf(bflo(xp[j].w) * inv), q7 = (int)rintf(bfhi(xp[j].w) * inv);
;             *(LAS v2u*)(XQ + i * 4096 + 8 * (F.lane + 64 * j)) = (v2u){(unsigned)((q0 & 0xff) | ((q1 & 0xff) << 8) | ((q2 & 0xff) << 16) | (q3 << 24)), (unsigned)((q4 & 0xff) | ((q5 & 0xff) << 8) | ((q6 & 0xff) << 16) | (q7 << 24))}; }
	v_cndmask_b32_e32 v79, 0, v2, vcc
	v_mul_f32_e32 v3, v79, v57
	v_mul_f32_e32 v2, v79, v58
	v_rndne_f32_e32 v3, v3
	v_mul_f32_e32 v4, v79, v56
	v_mul_f32_e32 v5, v79, v55
	v_rndne_f32_e32 v2, v2
	v_cvt_i32_f32_e32 v3, v3
	v_rndne_f32_e32 v4, v4
	v_rndne_f32_e32 v5, v5
	v_mul_f32_e32 v53, v79, v53
	v_cvt_i32_f32_e32 v2, v2
	v_cvt_i32_f32_sdwa v4, v4 dst_sel:WORD_1 dst_unused:UNUSED_PAD src0_sel:DWORD
	v_cvt_i32_f32_e32 v5, v5
	v_mul_f32_e32 v54, v79, v54
	v_rndne_f32_e32 v53, v53
	v_mul_f32_e32 v52, v79, v52
	v_mul_f32_e32 v51, v79, v51
	v_rndne_f32_e32 v54, v54
	v_cvt_i32_f32_e32 v53, v53
	v_rndne_f32_e32 v52, v52
	v_rndne_f32_e32 v51, v51
	v_cvt_i32_f32_e32 v54, v54
	v_cvt_i32_f32_sdwa v52, v52 dst_sel:WORD_1 dst_unused:UNUSED_PAD src0_sel:DWORD
	v_cvt_i32_f32_e32 v51, v51
	v_lshlrev_b32_e32 v3, 8, v3
	v_and_b32_e32 v3, 0xff00, v3
	v_and_b32_e32 v4, 0xff0000, v4
	v_perm_b32 v2, v5, v2, s21
	v_or3_b32 v2, v2, v3, v4
	v_lshlrev_b32_e32 v3, 8, v53
	v_and_b32_e32 v3, 0xff00, v3
	v_and_b32_e32 v4, 0xff0000, v52
	v_perm_b32 v5, v51, v54, s21
	v_or3_b32 v3, v5, v3, v4
	v_mul_f32_e32 v5, v79, v45
	v_mul_f32_e32 v4, v79, v48
	v_rndne_f32_e32 v5, v5
	v_mul_f32_e32 v43, v79, v43
	v_mul_f32_e32 v41, v79, v41
	v_rndne_f32_e32 v4, v4
	v_cvt_i32_f32_e32 v5, v5
	v_rndne_f32_e32 v43, v43
	v_rndne_f32_e32 v41, v41
	v_mul_f32_e32 v39, v79, v39
	v_cvt_i32_f32_e32 v4, v4
	v_cvt_i32_f32_sdwa v43, v43 dst_sel:WORD_1 dst_unused:UNUSED_PAD src0_sel:DWORD
	v_cvt_i32_f32_e32 v41, v41
	v_mul_f32_e32 v40, v79, v40
	v_rndne_f32_e32 v39, v39
	v_mul_f32_e32 v38, v79, v38
	v_mul_f32_e32 v37, v79, v37
	v_rndne_f32_e32 v40, v40
	v_cvt_i32_f32_e32 v39, v39
	v_rndne_f32_e32 v38, v38
	v_rndne_f32_e32 v37, v37
	v_cvt_i32_f32_e32 v40, v40
	v_cvt_i32_f32_sdwa v38, v38 dst_sel:WORD_1 dst_unused:UNUSED_PAD src0_sel:DWORD
	v_cvt_i32_f32_e32 v37, v37
	v_lshlrev_b32_e32 v5, 8, v5
	v_and_b32_e32 v5, 0xff00, v5
	v_and_b32_e32 v43, 0xff0000, v43
	v_perm_b32 v4, v41, v4, s21
	v_or3_b32 v4, v4, v5, v43
	v_lshlrev_b32_e32 v5, 8, v39
	v_and_b32_e32 v5, 0xff00, v5
	v_and_b32_e32 v38, 0xff0000, v38
	v_perm_b32 v37, v37, v40, s21
	v_or3_b32 v5, v37, v5, v38
	ds_write2st64_b64 v25, v[2:3], v[4:5] offset1:1
	v_mul_f32_e32 v3, v79, v33
	v_mul_f32_e32 v2, v79, v34
	v_rndne_f32_e32 v3, v3
	v_mul_f32_e32 v4, v79, v31
	v_mul_f32_e32 v5, v79, v30
	v_rndne_f32_e32 v2, v2
	v_cvt_i32_f32_e32 v3, v3
	v_rndne_f32_e32 v4, v4
	v_rndne_f32_e32 v5, v5
	v_mul_f32_e32 v28, v79, v28
	v_cvt_i32_f32_e32 v2, v2
	v_cvt_i32_f32_sdwa v4, v4 dst_sel:WORD_1 dst_unused:UNUSED_PAD src0_sel:DWORD
	v_cvt_i32_f32_e32 v5, v5
	v_mul_f32_e32 v29, v79, v29
	v_rndne_f32_e32 v28, v28
	v_mul_f32_e32 v27, v79, v27
	v_mul_f32_e32 v26, v79, v26
	v_rndne_f32_e32 v29, v29
	v_cvt_i32_f32_e32 v28, v28
	v_rndne_f32_e32 v27, v27
	v_rndne_f32_e32 v26, v26
	v_cvt_i32_f32_e32 v29, v29
	v_cvt_i32_f32_sdwa v27, v27 dst_sel:WORD_1 dst_unused:UNUSED_PAD src0_sel:DWORD
	v_cvt_i32_f32_e32 v26, v26
	v_lshlrev_b32_e32 v3, 8, v3
	v_and_b32_e32 v3, 0xff00, v3
	v_and_b32_e32 v4, 0xff0000, v4
	v_perm_b32 v2, v5, v2, s21
	v_or3_b32 v2, v2, v3, v4
	v_lshlrev_b32_e32 v3, 8, v28
	v_and_b32_e32 v3, 0xff00, v3
	v_and_b32_e32 v4, 0xff0000, v27
	v_perm_b32 v5, v26, v29, s21
	v_or3_b32 v3, v5, v3, v4
	v_mul_f32_e32 v5, v79, v35
	v_mul_f32_e32 v4, v79, v36
	v_rndne_f32_e32 v5, v5
	v_mul_f32_e32 v26, v79, v50
	v_mul_f32_e32 v27, v79, v47
	v_rndne_f32_e32 v4, v4
	v_cvt_i32_f32_e32 v5, v5
	v_rndne_f32_e32 v26, v26
	v_rndne_f32_e32 v27, v27
	v_mul_f32_e32 v29, v79, v46
	v_cvt_i32_f32_e32 v4, v4
	v_cvt_i32_f32_sdwa v26, v26 dst_sel:WORD_1 dst_unused:UNUSED_PAD src0_sel:DWORD
	v_cvt_i32_f32_e32 v27, v27
	v_mul_f32_e32 v28, v79, v49
	v_rndne_f32_e32 v29, v29
	v_mul_f32_e32 v30, v79, v44
	v_mul_f32_e32 v31, v79, v42
	v_rndne_f32_e32 v28, v28
	v_cvt_i32_f32_e32 v29, v29
	v_rndne_f32_e32 v30, v30
	v_rndne_f32_e32 v31, v31
	v_cvt_i32_f32_e32 v28, v28
	v_cvt_i32_f32_sdwa v30, v30 dst_sel:WORD_1 dst_unused:UNUSED_PAD src0_sel:DWORD
	v_cvt_i32_f32_e32 v31, v31
	v_lshlrev_b32_e32 v5, 8, v5
	v_and_b32_e32 v5, 0xff00, v5
	v_and_b32_e32 v26, 0xff0000, v26
	v_perm_b32 v4, v27, v4, s21
	v_or3_b32 v4, v4, v5, v26
	v_lshlrev_b32_e32 v5, 8, v29
	v_and_b32_e32 v5, 0xff00, v5
	v_and_b32_e32 v26, 0xff0000, v30
	v_perm_b32 v27, v31, v28, s21
	v_or3_b32 v5, v27, v5, v26
	ds_write2st64_b64 v25, v[2:3], v[4:5] offset0:2 offset1:3
	v_mul_f32_e32 v3, v79, v21
	v_mul_f32_e32 v2, v79, v20
	v_rndne_f32_e32 v3, v3
	v_mul_f32_e32 v4, v79, v22
	v_mul_f32_e32 v5, v79, v23
	v_rndne_f32_e32 v2, v2
	v_cvt_i32_f32_e32 v3, v3
	v_rndne_f32_e32 v4, v4
	v_rndne_f32_e32 v5, v5
	v_mul_f32_e32 v21, v79, v62
	v_cvt_i32_f32_e32 v2, v2
	v_cvt_i32_f32_sdwa v4, v4 dst_sel:WORD_1 dst_unused:UNUSED_PAD src0_sel:DWORD
	v_cvt_i32_f32_e32 v5, v5
	v_mul_f32_e32 v20, v79, v59
	v_rndne_f32_e32 v21, v21
	v_mul_f32_e32 v22, v79, v63
	v_mul_f32_e32 v23, v79, v64
	v_rndne_f32_e32 v20, v20
	v_cvt_i32_f32_e32 v21, v21
	v_rndne_f32_e32 v22, v22
	v_rndne_f32_e32 v23, v23
	v_cvt_i32_f32_e32 v20, v20
	v_cvt_i32_f32_sdwa v22, v22 dst_sel:WORD_1 dst_unused:UNUSED_PAD src0_sel:DWORD
	v_cvt_i32_f32_e32 v23, v23
	v_lshlrev_b32_e32 v3, 8, v3
	v_and_b32_e32 v3, 0xff00, v3
	v_and_b32_e32 v4, 0xff0000, v4
	v_perm_b32 v2, v5, v2, s21
	v_or3_b32 v2, v2, v3, v4
	v_lshlrev_b32_e32 v3, 8, v21
	v_and_b32_e32 v3, 0xff00, v3
	v_and_b32_e32 v4, 0xff0000, v22
	v_perm_b32 v5, v23, v20, s21
	v_or3_b32 v3, v5, v3, v4
	v_mul_f32_e32 v5, v79, v66
	v_mul_f32_e32 v4, v79, v65
	v_rndne_f32_e32 v5, v5
	v_mul_f32_e32 v20, v79, v67
	v_mul_f32_e32 v21, v79, v68
	v_rndne_f32_e32 v4, v4
	v_cvt_i32_f32_e32 v5, v5
	v_rndne_f32_e32 v20, v20
	v_rndne_f32_e32 v21, v21
; #define LAS __attribute__((address_space(3)))
; __device__ __forceinline__ float bflo(unsigned w) { return __uint_as_float(w << 16); }
; __device__ __forceinline__ float bfhi(unsigned w) { return __uint_as_float(w & 0xffff0000u); }
; __device__ __forceinline__ float wave_sum(float v) { v = dpp_add16(v); return (rdlane(v, 0) + rdlane(v, 16)) + (rdlane(v, 32) + rdlane(v, 48)); }
; __device__ __forceinline__ float wave_max(float v) { v = dpp_max16(v); return fmaxf(fmaxf(rdlane(v, 0), rdlane(v, 16)), fmaxf(rdlane(v, 32), rdlane(v, 48))); }
; __device__ __forceinline__ void p12_peer(Frame& F) {
;     ...
;     for (int i = 0; i < 4; ++i) {
;         const int t = F.gw + i * F.NGW; v4u xp[8]; float mxa = 0.f;
; #pragma unroll
;         for (int j = 0; j < 8; ++j) { xp[j] = ((const v4u*)(HN + (size_t)t * D_))[F.lane + 64 * j];
;             mxa = fmaxf(fmaxf(fmaxf(mxa, fmaxf(fabsf(bflo(xp[j].x)), fabsf(bfhi(xp[j].x)))), fmaxf(fabsf(bflo(xp[j].y)), fabsf(bfhi(xp[j].y)))), fmaxf(fmaxf(fabsf(bflo(xp[j].z)), fabsf(bfhi(xp[j].z))), fmaxf(fabsf(bflo(xp[j].w)), fabsf(bfhi(xp[j].w))))); }
;         mxa = wave_max(mxa); const float inv = mxa > 0.f ? 127.0f / mxa : 0.f;
;         const float rsn = 1.0f / sqrtf(wave_sum(PSQ[(size_t)t * 64 + F.lane]) * (1.f / D_) + 1e-6f);
;         sx[i] = mxa * rsn * (1.0f / 127.0f);
; #pragma unroll
;         for (int j = 0; j < 8; ++j) {
;             const int q0 = (int)rintf(bflo(xp[j].x) * inv), q1 = (int)rintf(bfhi(xp[j].x) * inv), q2 = (int)rintf(bflo(xp[j].y) * inv), q3 = (int)rintf(bfhi(xp[j].y) * inv);
;             const int q4 = (int)rintf(bflo(xp[j].z) * inv), q5 = (int)rintf(bfhi(xp[j].z) * inv), q6 = (int)rintf(bflo(xp[j].w) * inv), q7 = (int)rintf(bfhi(xp[j].w) * inv);
;             *(LAS v2u*)(XQ + i * 4096 + 8 * (F.lane + 64 * j)) = (v2u){(unsigned)((q0 & 0xff) | ((q1 & 0xff) << 8) | ((q2 & 0xff) << 16) | (q3 << 24)), (unsigned)((q4 & 0xff) | ((q5 & 0xff) << 8) | ((q6 & 0xff) << 16) | (q7 << 24))}; }
;         EL[i * 128 + F.lane] = (unsigned short)PIDX[(size_t)t * 128 + F.lane]; EL[i * 128 + 64 + F.lane] = (unsigned short)PIDX[(size_t)t * 128 + 64 + F.lane];
	v_mul_f32_e32 v6, v79, v6
	v_cvt_i32_f32_e32 v4, v4
	v_cvt_i32_f32_sdwa v20, v20 dst_sel:WORD_1 dst_unused:UNUSED_PAD src0_sel:DWORD
	v_cvt_i32_f32_e32 v21, v21
	v_mul_f32_e32 v22, v79, v69
	v_rndne_f32_e32 v6, v6
	v_mul_f32_e32 v23, v79, v70
	v_mul_f32_e32 v7, v79, v7
	v_rndne_f32_e32 v22, v22
	v_cvt_i32_f32_e32 v6, v6
	v_rndne_f32_e32 v23, v23
	v_rndne_f32_e32 v7, v7
	v_cvt_i32_f32_e32 v22, v22
	v_cvt_i32_f32_sdwa v23, v23 dst_sel:WORD_1 dst_unused:UNUSED_PAD src0_sel:DWORD
	v_cvt_i32_f32_e32 v7, v7
	v_lshlrev_b32_e32 v5, 8, v5
	v_and_b32_e32 v5, 0xff00, v5
	v_and_b32_e32 v20, 0xff0000, v20
	v_perm_b32 v4, v21, v4, s21
	v_or3_b32 v4, v4, v5, v20
	v_lshlrev_b32_e32 v5, 8, v6
	v_and_b32_e32 v5, 0xff00, v5
	v_and_b32_e32 v6, 0xff0000, v23
	v_perm_b32 v7, v7, v22, s21
	v_or3_b32 v5, v7, v5, v6
	ds_write2st64_b64 v25, v[2:3], v[4:5] offset0:4 offset1:5
	v_mul_f32_e32 v3, v79, v8
	v_mul_f32_e32 v2, v79, v71
	v_rndne_f32_e32 v3, v3
	v_mul_f32_e32 v4, v79, v72
	v_mul_f32_e32 v5, v79, v9
	v_rndne_f32_e32 v2, v2
	v_cvt_i32_f32_e32 v3, v3
	v_rndne_f32_e32 v4, v4
	v_rndne_f32_e32 v5, v5
	v_mul_f32_e32 v7, v79, v10
	v_cvt_i32_f32_e32 v2, v2
	v_cvt_i32_f32_sdwa v4, v4 dst_sel:WORD_1 dst_unused:UNUSED_PAD src0_sel:DWORD
	v_cvt_i32_f32_e32 v5, v5
	v_mul_f32_e32 v6, v79, v73
	v_rndne_f32_e32 v7, v7
	v_mul_f32_e32 v8, v79, v74
	v_mul_f32_e32 v9, v79, v11
	v_rndne_f32_e32 v6, v6
	v_cvt_i32_f32_e32 v7, v7
	v_rndne_f32_e32 v8, v8
	v_rndne_f32_e32 v9, v9
	v_cvt_i32_f32_e32 v6, v6
	v_cvt_i32_f32_sdwa v8, v8 dst_sel:WORD_1 dst_unused:UNUSED_PAD src0_sel:DWORD
	v_cvt_i32_f32_e32 v9, v9
	v_lshlrev_b32_e32 v3, 8, v3
	v_and_b32_e32 v3, 0xff00, v3
	v_and_b32_e32 v4, 0xff0000, v4
	v_perm_b32 v2, v5, v2, s21
	v_or3_b32 v2, v2, v3, v4
	v_lshlrev_b32_e32 v3, 8, v7
	v_and_b32_e32 v3, 0xff00, v3
	v_and_b32_e32 v4, 0xff0000, v8
	v_perm_b32 v5, v9, v6, s21
	v_or3_b32 v3, v5, v3, v4
	v_mul_f32_e32 v5, v79, v12
	v_mul_f32_e32 v4, v79, v75
	v_rndne_f32_e32 v5, v5
	v_mul_f32_e32 v6, v79, v76
	v_mul_f32_e32 v7, v79, v13
	v_rndne_f32_e32 v4, v4
	v_cvt_i32_f32_e32 v5, v5
	v_rndne_f32_e32 v6, v6
	v_rndne_f32_e32 v7, v7
	v_mul_f32_e32 v9, v79, v14
	v_cvt_i32_f32_e32 v4, v4
	v_cvt_i32_f32_sdwa v6, v6 dst_sel:WORD_1 dst_unused:UNUSED_PAD src0_sel:DWORD
	v_cvt_i32_f32_e32 v7, v7
	v_mul_f32_e32 v8, v79, v77
	v_rndne_f32_e32 v9, v9
	v_mul_f32_e32 v10, v79, v78
	v_mul_f32_e32 v11, v79, v15
	v_rndne_f32_e32 v8, v8
	v_cvt_i32_f32_e32 v9, v9
	v_rndne_f32_e32 v10, v10
	v_rndne_f32_e32 v11, v11
	v_cvt_i32_f32_e32 v8, v8
	v_cvt_i32_f32_sdwa v10, v10 dst_sel:WORD_1 dst_unused:UNUSED_PAD src0_sel:DWORD
	v_cvt_i32_f32_e32 v11, v11
	v_lshlrev_b32_e32 v5, 8, v5
	v_and_b32_e32 v5, 0xff00, v5
	v_and_b32_e32 v6, 0xff0000, v6
	v_perm_b32 v4, v7, v4, s21
	v_or3_b32 v4, v4, v5, v6
	v_lshlrev_b32_e32 v5, 8, v9
	v_and_b32_e32 v5, 0xff00, v5
	v_and_b32_e32 v6, 0xff0000, v10
	v_perm_b32 v7, v11, v8, s21
	v_or3_b32 v5, v7, v5, v6
	ds_write2st64_b64 v25, v[2:3], v[4:5] offset0:6 offset1:7
	s_waitcnt vmcnt(4)
	ds_write_b16 v24, v60 offset:16384
	s_waitcnt vmcnt(0)
	ds_write_b16 v24, v61 offset:16512
	global_load_dwordx4 v[4:7], v[0:1], off
	global_load_dwordx4 v[8:11], v[0:1], off offset:1024
	global_load_dwordx4 v[12:15], v[0:1], off offset:2048
	global_load_dwordx4 v[60:63], v[0:1], off offset:3072
	v_add_co_u32_e32 v56, vcc, s28, v0
	v_lshl_add_u64 v[20:21], s[8:9], 0, v[16:17]
	s_nop 0
	v_addc_co_u32_e32 v57, vcc, 0, v1, vcc
	s_add_u32 s8, s18, s16
	s_addc_u32 s9, s19, s17
	v_lshl_add_u64 v[22:23], s[8:9], 0, v[16:17]
	s_add_i32 s8, s4, s34
	s_ashr_i32 s9, s8, 31
	s_lshl_b64 s[10:11], s[8:9], 13
	s_add_u32 s10, s6, s10
	s_addc_u32 s11, s7, s11
	v_readlane_b32 s41, v32, 16
	v_readlane_b32 s40, v32, 32
	v_readlane_b32 s42, v32, 48
	v_mov_b32_e32 v156, 0
	v_mov_b32_e32 v157, v109
	v_mov_b32_e32 v158, 0
	v_mov_b32_e32 v159, v109
	v_mov_b32_e32 v106, 0
	v_mov_b32_e32 v107, v109
	v_mov_b32_e32 v104, 0
	v_mov_b32_e32 v105, v109
	v_mov_b32_e32 v102, 0
	v_mov_b32_e32 v103, v109
	v_mov_b32_e32 v100, 0
	v_mov_b32_e32 v101, v109
	v_mov_b32_e32 v98, 0
	v_mov_b32_e32 v99, v109
	v_mov_b32_e32 v96, 0
	v_mov_b32_e32 v97, v109
	s_waitcnt vmcnt(3)
	v_lshlrev_b32_e32 v27, 16, v4
	v_and_b32_e32 v26, 0xffff0000, v4
	v_max_f32_e64 v2, |v26|, |v26|
	v_max_f32_e64 v3, |v27|, |v27|
	v_max_f32_e32 v4, v3, v2
	global_load_dwordx4 v[0:3], v[56:57], off
	v_lshlrev_b32_e32 v41, 16, v5
	v_and_b32_e32 v38, 0xffff0000, v5
	v_max_f32_e64 v5, |v38|, |v38|
	v_max_f32_e64 v28, |v41|, |v41|
	v_max_f32_e32 v5, v28, v5
	v_lshlrev_b32_e32 v36, 16, v7
	v_and_b32_e32 v34, 0xffff0000, v7
	v_max3_f32 v30, v4, 0, v5
	v_max_f32_e64 v4, |v34|, |v34|
	v_max_f32_e64 v5, |v36|, |v36|
	v_lshlrev_b32_e32 v42, 16, v6
	v_and_b32_e32 v39, 0xffff0000, v6
	v_max_f32_e32 v4, v5, v4
	v_max3_f32 v31, |v42|, |v39|, v4
	s_waitcnt vmcnt(3)
	v_lshlrev_b32_e32 v29, 16, v8
	v_and_b32_e32 v28, 0xffff0000, v8
	global_load_dwordx4 v[4:7], v[56:57], off offset:1024
	v_max_f32_e64 v8, |v28|, |v28|
	v_max_f32_e64 v33, |v29|, |v29|
	v_max_f32_e32 v8, v33, v8
	v_lshlrev_b32_e32 v48, 16, v9
	v_and_b32_e32 v45, 0xffff0000, v9
	v_lshlrev_b32_e32 v43, 16, v11
	v_and_b32_e32 v40, 0xffff0000, v11
	v_max3_f32 v8, v30, v31, v8
	v_max_f32_e64 v9, |v45|, |v45|
	v_max_f32_e64 v30, |v48|, |v48|
	v_lshlrev_b32_e32 v46, 16, v10
	v_and_b32_e32 v44, 0xffff0000, v10
	v_max_f32_e64 v10, |v40|, |v40|
	v_max_f32_e64 v11, |v43|, |v43|
	v_max_f32_e32 v9, v30, v9
	v_max_f32_e32 v10, v11, v10
	s_waitcnt vmcnt(3)
; #define LAS __attribute__((address_space(3)))
; __device__ __forceinline__ float bflo(unsigned w) { return __uint_as_float(w << 16); }
; __device__ __forceinline__ float bfhi(unsigned w) { return __uint_as_float(w & 0xffff0000u); }
; __device__ __forceinline__ float wave_sum(float v) { v = dpp_add16(v); return (rdlane(v, 0) + rdlane(v, 16)) + (rdlane(v, 32) + rdlane(v, 48)); }
; __device__ __forceinline__ float wave_max(float v) { v = dpp_max16(v); return fmaxf(fmaxf(rdlane(v, 0), rdlane(v, 16)), fmaxf(rdlane(v, 32), rdlane(v, 48))); }
; __device__ __forceinline__ void p12_peer(Frame& F) {
;     ...
;     for (int i = 0; i < 4; ++i) {
;         const int t = F.gw + i * F.NGW; v4u xp[8]; float mxa = 0.f;
; #pragma unroll
;         for (int j = 0; j < 8; ++j) { xp[j] = ((const v4u*)(HN + (size_t)t * D_))[F.lane + 64 * j];
;             mxa = fmaxf(fmaxf(fmaxf(mxa, fmaxf(fabsf(bflo(xp[j].x)), fabsf(bfhi(xp[j].x)))), fmaxf(fabsf(bflo(xp[j].y)), fabsf(bfhi(xp[j].y)))), fmaxf(fmaxf(fabsf(bflo(xp[j].z)), fabsf(bfhi(xp[j].z))), fmaxf(fabsf(bflo(xp[j].w)), fabsf(bfhi(xp[j].w))))); }
;         mxa = wave_max(mxa); const float inv = mxa > 0.f ? 127.0f / mxa : 0.f;
;         const float rsn = 1.0f / sqrtf(wave_sum(PSQ[(size_t)t * 64 + F.lane]) * (1.f / D_) + 1e-6f);
;         sx[i] = mxa * rsn * (1.0f / 127.0f);
; #pragma unroll
;         for (int j = 0; j < 8; ++j) {
;             const int q0 = (int)rintf(bflo(xp[j].x) * inv), q1 = (int)rintf(bfhi(xp[j].x) * inv), q2 = (int)rintf(bflo(xp[j].y) * inv), q3 = (int)rintf(bfhi(xp[j].y) * inv);
;             const int q4 = (int)rintf(bflo(xp[j].z) * inv), q5 = (int)rintf(bfhi(xp[j].z) * inv), q6 = (int)rintf(bflo(xp[j].w) * inv), q7 = (int)rintf(bfhi(xp[j].w) * inv);
;             *(LAS v2u*)(XQ + i * 4096 + 8 * (F.lane + 64 * j)) = (v2u){(unsigned)((q0 & 0xff) | ((q1 & 0xff) << 8) | ((q2 & 0xff) << 16) | (q3 << 24)), (unsigned)((q4 & 0xff) | ((q5 & 0xff) << 8) | ((q6 & 0xff) << 16) | (q7 << 24))}; }
;         EL[i * 128 + F.lane] = (unsigned short)PIDX[(size_t)t * 128 + F.lane]; EL[i * 128 + 64 + F.lane] = (unsigned short)PIDX[(size_t)t * 128 + 64 + F.lane];
	v_lshlrev_b32_e32 v31, 16, v12
	v_and_b32_e32 v30, 0xffff0000, v12
	v_max3_f32 v10, |v46|, |v44|, v10
	v_max_f32_e64 v12, |v30|, |v30|
	v_max_f32_e64 v35, |v31|, |v31|
	v_lshlrev_b32_e32 v53, 16, v13
	v_and_b32_e32 v50, 0xffff0000, v13
	v_max3_f32 v33, v8, v9, v10
	global_load_dwordx4 v[8:11], v[56:57], off offset:2048
	v_max_f32_e32 v12, v35, v12
	v_max_f32_e64 v13, |v50|, |v50|
	v_max_f32_e64 v35, |v53|, |v53|
	v_max_f32_e32 v13, v35, v13
	v_lshlrev_b32_e32 v49, 16, v15
	v_and_b32_e32 v47, 0xffff0000, v15
	v_max3_f32 v33, v33, v12, v13
	v_max_f32_e64 v12, |v47|, |v47|
	v_max_f32_e64 v13, |v49|, |v49|
	v_lshlrev_b32_e32 v54, 16, v14
	v_and_b32_e32 v51, 0xffff0000, v14
	v_max_f32_e32 v12, v13, v12
	v_max3_f32 v52, |v54|, |v51|, v12
	global_load_dwordx4 v[12:15], v[56:57], off offset:3072
	s_waitcnt vmcnt(4)
	v_lshlrev_b32_e32 v37, 16, v60
	v_and_b32_e32 v35, 0xffff0000, v60
	v_max_f32_e64 v55, |v35|, |v35|
	v_max_f32_e64 v56, |v37|, |v37|
	v_max_f32_e32 v55, v56, v55
	v_lshlrev_b32_e32 v59, 16, v61
	v_and_b32_e32 v57, 0xffff0000, v61
	v_max3_f32 v33, v33, v52, v55
	v_max_f32_e64 v52, |v57|, |v57|
	v_max_f32_e64 v55, |v59|, |v59|
	v_max_f32_e32 v60, v55, v52
	v_lshlrev_b32_e32 v55, 16, v63
	v_and_b32_e32 v52, 0xffff0000, v63
	v_lshlrev_b32_e32 v58, 16, v62
	v_and_b32_e32 v56, 0xffff0000, v62
	v_max_f32_e64 v61, |v52|, |v52|
	v_max_f32_e64 v62, |v55|, |v55|
	v_max_f32_e32 v61, v62, v61
	v_max3_f32 v61, |v58|, |v56|, v61
	v_max3_f32 v60, v33, v60, v61
	global_load_dword v33, v[20:21], off
	global_load_dword v61, v[22:23], off
	global_load_dword v62, v[22:23], off offset:256
	s_waitcnt vmcnt(6)
	v_lshlrev_b32_e32 v20, 16, v0
	v_and_b32_e32 v21, 0xffff0000, v0
	v_max_f32_e64 v0, |v21|, |v21|
	v_max_f32_e64 v22, |v20|, |v20|
	v_max_f32_e32 v0, v22, v0
	v_lshlrev_b32_e32 v22, 16, v1
	v_and_b32_e32 v23, 0xffff0000, v1
	v_max_f32_e64 v1, |v23|, |v23|
	v_max_f32_e64 v63, |v22|, |v22|
	v_max_f32_e32 v1, v63, v1
	v_lshlrev_b32_e32 v64, 16, v3
	v_and_b32_e32 v65, 0xffff0000, v3
	v_max3_f32 v0, v60, v0, v1
	v_lshlrev_b32_e32 v60, 16, v2
	v_and_b32_e32 v63, 0xffff0000, v2
	v_max_f32_e64 v1, |v65|, |v65|
	v_max_f32_e64 v2, |v64|, |v64|
	s_waitcnt vmcnt(5)
	v_lshlrev_b32_e32 v66, 16, v4
	v_and_b32_e32 v67, 0xffff0000, v4
	v_max_f32_e32 v1, v2, v1
	v_max_f32_e64 v2, |v67|, |v67|
	v_max_f32_e64 v3, |v66|, |v66|
	v_max3_f32 v1, |v60|, |v63|, v1
	v_max_f32_e32 v2, v3, v2
	v_lshlrev_b32_e32 v68, 16, v5
	v_and_b32_e32 v69, 0xffff0000, v5
	v_max3_f32 v0, v0, v1, v2
	v_max_f32_e64 v1, |v69|, |v69|
	v_max_f32_e64 v2, |v68|, |v68|
	v_lshlrev_b32_e32 v71, 16, v7
	v_and_b32_e32 v7, 0xffff0000, v7
	v_max_f32_e32 v1, v2, v1
	v_max_f32_e64 v2, |v7|, |v7|
	v_max_f32_e64 v3, |v71|, |v71|
	v_lshlrev_b32_e32 v70, 16, v6
	v_and_b32_e32 v6, 0xffff0000, v6
	v_max_f32_e32 v2, v3, v2
	v_max3_f32 v2, |v70|, |v6|, v2
	v_max3_f32 v0, v0, v1, v2
	s_waitcnt vmcnt(4)
	v_lshlrev_b32_e32 v72, 16, v8
	v_and_b32_e32 v8, 0xffff0000, v8
	v_max_f32_e64 v1, |v8|, |v8|
	v_max_f32_e64 v2, |v72|, |v72|
	v_lshlrev_b32_e32 v73, 16, v9
	v_and_b32_e32 v9, 0xffff0000, v9
	v_max_f32_e32 v1, v2, v1
	v_max_f32_e64 v2, |v9|, |v9|
	v_max_f32_e64 v3, |v73|, |v73|
	v_max_f32_e32 v2, v3, v2
	v_lshlrev_b32_e32 v75, 16, v11
	v_and_b32_e32 v11, 0xffff0000, v11
	v_max3_f32 v0, v0, v1, v2
	v_max_f32_e64 v1, |v11|, |v11|
	v_max_f32_e64 v2, |v75|, |v75|
	s_waitcnt vmcnt(3)
	v_lshlrev_b32_e32 v76, 16, v12
	v_and_b32_e32 v12, 0xffff0000, v12
	v_lshlrev_b32_e32 v74, 16, v10
	v_and_b32_e32 v10, 0xffff0000, v10
	v_max_f32_e32 v1, v2, v1
	v_max_f32_e64 v2, |v12|, |v12|
	v_max_f32_e64 v3, |v76|, |v76|
	v_max3_f32 v1, |v74|, |v10|, v1
	v_max_f32_e32 v2, v3, v2
	v_lshlrev_b32_e32 v77, 16, v13
	v_and_b32_e32 v13, 0xffff0000, v13
	v_max3_f32 v0, v0, v1, v2
	v_max_f32_e64 v1, |v13|, |v13|
	v_max_f32_e64 v2, |v77|, |v77|
	v_lshlrev_b32_e32 v79, 16, v15
	v_and_b32_e32 v15, 0xffff0000, v15
	v_max_f32_e32 v1, v2, v1
	v_max_f32_e64 v2, |v15|, |v15|
	v_max_f32_e64 v3, |v79|, |v79|
	v_lshlrev_b32_e32 v78, 16, v14
	v_and_b32_e32 v14, 0xffff0000, v14
	v_max_f32_e32 v2, v3, v2
	v_max3_f32 v2, |v78|, |v14|, v2
	v_max3_f32 v0, v0, v1, v2
	v_mov_b32_e32 v1, 0
	s_waitcnt vmcnt(2)
	v_add_f32_dpp v32, v33, v33 quad_perm:[1,0,3,2] row_mask:0xf bank_mask:0xf bound_ctrl:1
	v_mov_b32_dpp v1, v0 quad_perm:[1,0,3,2] row_mask:0xf bank_mask:0xf
	v_max_f32_e32 v1, v1, v1
	v_max_f32_e32 v0, v0, v1
	v_mov_b32_e32 v1, 0
	v_add_f32_dpp v32, v32, v32 quad_perm:[2,3,0,1] row_mask:0xf bank_mask:0xf bound_ctrl:1
	s_nop 0
	v_mov_b32_dpp v1, v0 quad_perm:[2,3,0,1] row_mask:0xf bank_mask:0xf
	v_max_f32_e32 v1, v1, v1
	v_max_f32_e32 v0, v0, v1
	v_mov_b32_e32 v1, 0
	v_add_f32_dpp v32, v32, v32 row_half_mirror row_mask:0xf bank_mask:0xf bound_ctrl:1
	s_nop 0
	v_mov_b32_dpp v1, v0 row_half_mirror row_mask:0xf bank_mask:0xf
	v_max_f32_e32 v1, v1, v1
	v_max_f32_e32 v0, v0, v1
	v_mov_b32_e32 v1, 0
	v_add_f32_dpp v32, v32, v32 row_mirror row_mask:0xf bank_mask:0xf bound_ctrl:1
	s_nop 0
	v_mov_b32_dpp v1, v0 row_mirror row_mask:0xf bank_mask:0xf
	v_max_f32_e32 v1, v1, v1
	v_max_f32_e32 v0, v0, v1
	v_readlane_b32 s37, v32, 16
	v_readlane_b32 s14, v0, 32
	v_readlane_b32 s15, v0, 48
	v_readlane_b32 s12, v0, 0
	v_readlane_b32 s13, v0, 16
	v_max_f32_e64 v0, s15, s15
	v_max_f32_e64 v1, s14, s14
	v_max_f32_e32 v0, v1, v0
	v_mov_b32_e32 v1, s13
	v_max3_f32 v162, s12, v1, v0
	v_div_scale_f32 v2, s[12:13], v162, v162, s29
	v_rcp_f32_e32 v3, v2
	v_lshl_add_u64 v[0:1], s[10:11], 0, v[18:19]
	s_lshl_b64 s[10:11], s[8:9], 8
	s_add_u32 s10, s22, s10
	v_fma_f32 v4, -v2, v3, 1.0
	v_fmac_f32_e32 v3, v4, v3
	v_div_scale_f32 v4, vcc, s29, v162, s29
	v_mul_f32_e32 v5, v4, v3
; #define LAS __attribute__((address_space(3)))
; __device__ __forceinline__ float bflo(unsigned w) { return __uint_as_float(w << 16); }
; __device__ __forceinline__ float bfhi(unsigned w) { return __uint_as_float(w & 0xffff0000u); }
; __device__ __forceinline__ float wave_sum(float v) { v = dpp_add16(v); return (rdlane(v, 0) + rdlane(v, 16)) + (rdlane(v, 32) + rdlane(v, 48)); }
; __device__ __forceinline__ float wave_max(float v) { v = dpp_max16(v); return fmaxf(fmaxf(rdlane(v, 0), rdlane(v, 16)), fmaxf(rdlane(v, 32), rdlane(v, 48))); }
; __device__ __forceinline__ void p12_peer(Frame& F) {
;     ...
;         for (int j = 0; j < 8; ++j) { xp[j] = ((const v4u*)(HN + (size_t)t * D_))[F.lane + 64 * j];
;             mxa = fmaxf(fmaxf(fmaxf(mxa, fmaxf(fabsf(bflo(xp[j].x)), fabsf(bfhi(xp[j].x)))), fmaxf(fabsf(bflo(xp[j].y)), fabsf(bfhi(xp[j].y)))), fmaxf(fmaxf(fabsf(bflo(xp[j].z)), fabsf(bfhi(xp[j].z))), fmaxf(fabsf(bflo(xp[j].w)), fabsf(bfhi(xp[j].w))))); }
;         mxa = wave_max(mxa); const float inv = mxa > 0.f ? 127.0f / mxa : 0.f;
;         const float rsn = 1.0f / sqrtf(wave_sum(PSQ[(size_t)t * 64 + F.lane]) * (1.f / D_) + 1e-6f);
;         sx[i] = mxa * rsn * (1.0f / 127.0f);
; #pragma unroll
;         for (int j = 0; j < 8; ++j) {
;             const int q0 = (int)rintf(bflo(xp[j].x) * inv), q1 = (int)rintf(bfhi(xp[j].x) * inv), q2 = (int)rintf(bflo(xp[j].y) * inv), q3 = (int)rintf(bfhi(xp[j].y) * inv);
;             const int q4 = (int)rintf(bflo(xp[j].z) * inv), q5 = (int)rintf(bfhi(xp[j].z) * inv), q6 = (int)rintf(bflo(xp[j].w) * inv), q7 = (int)rintf(bfhi(xp[j].w) * inv);
;             *(LAS v2u*)(XQ + i * 4096 + 8 * (F.lane + 64 * j)) = (v2u){(unsigned)((q0 & 0xff) | ((q1 & 0xff) << 8) | ((q2 & 0xff) << 16) | (q3 << 24)), (unsigned)((q4 & 0xff) | ((q5 & 0xff) << 8) | ((q6 & 0xff) << 16) | (q7 << 24))}; }
	v_fma_f32 v80, -v2, v5, v4
	v_fmac_f32_e32 v5, v80, v3
	v_fma_f32 v2, -v2, v5, v4
	v_div_fmas_f32 v2, v2, v3, v5
	v_div_fixup_f32 v2, v2, v162, s29
	v_cmp_lt_f32_e32 vcc, 0, v162
	s_addc_u32 s11, s23, s11
	s_lshl_b64 s[14:15], s[8:9], 9
	v_cndmask_b32_e32 v80, 0, v2, vcc
	v_mul_f32_e32 v3, v80, v26
	v_mul_f32_e32 v2, v80, v27
	v_rndne_f32_e32 v3, v3
	v_mul_f32_e32 v4, v80, v41
	v_mul_f32_e32 v5, v80, v38
	v_rndne_f32_e32 v2, v2
	v_cvt_i32_f32_e32 v3, v3
	v_rndne_f32_e32 v4, v4
	v_rndne_f32_e32 v5, v5
	v_mul_f32_e32 v27, v80, v39
	v_cvt_i32_f32_e32 v2, v2
	v_cvt_i32_f32_sdwa v4, v4 dst_sel:WORD_1 dst_unused:UNUSED_PAD src0_sel:DWORD
	v_cvt_i32_f32_e32 v5, v5
	v_mul_f32_e32 v26, v80, v42
	v_rndne_f32_e32 v27, v27
	v_mul_f32_e32 v36, v80, v36
	v_mul_f32_e32 v34, v80, v34
	v_rndne_f32_e32 v26, v26
	v_cvt_i32_f32_e32 v27, v27
	v_rndne_f32_e32 v36, v36
	v_rndne_f32_e32 v34, v34
	v_cvt_i32_f32_e32 v26, v26
	v_cvt_i32_f32_sdwa v36, v36 dst_sel:WORD_1 dst_unused:UNUSED_PAD src0_sel:DWORD
	v_cvt_i32_f32_e32 v34, v34
	v_lshlrev_b32_e32 v3, 8, v3
	v_and_b32_e32 v3, 0xff00, v3
	v_and_b32_e32 v4, 0xff0000, v4
	v_perm_b32 v2, v5, v2, s21
	v_or3_b32 v2, v2, v3, v4
	v_lshlrev_b32_e32 v3, 8, v27
	v_and_b32_e32 v3, 0xff00, v3
	v_and_b32_e32 v4, 0xff0000, v36
	v_perm_b32 v5, v34, v26, s21
	v_or3_b32 v3, v5, v3, v4
	v_mul_f32_e32 v5, v80, v28
	v_mul_f32_e32 v4, v80, v29
	v_rndne_f32_e32 v5, v5
	v_mul_f32_e32 v26, v80, v48
	v_mul_f32_e32 v27, v80, v45
	v_rndne_f32_e32 v4, v4
	v_cvt_i32_f32_e32 v5, v5
	v_rndne_f32_e32 v26, v26
	v_rndne_f32_e32 v27, v27
	v_mul_f32_e32 v29, v80, v44
	v_cvt_i32_f32_e32 v4, v4
	v_cvt_i32_f32_sdwa v26, v26 dst_sel:WORD_1 dst_unused:UNUSED_PAD src0_sel:DWORD
	v_cvt_i32_f32_e32 v27, v27
	v_mul_f32_e32 v28, v80, v46
	v_rndne_f32_e32 v29, v29
	v_mul_f32_e32 v34, v80, v43
	v_mul_f32_e32 v36, v80, v40
	v_rndne_f32_e32 v28, v28
	v_cvt_i32_f32_e32 v29, v29
	v_rndne_f32_e32 v34, v34
	v_rndne_f32_e32 v36, v36
	v_cvt_i32_f32_e32 v28, v28
	v_cvt_i32_f32_sdwa v34, v34 dst_sel:WORD_1 dst_unused:UNUSED_PAD src0_sel:DWORD
	v_cvt_i32_f32_e32 v36, v36
	v_lshlrev_b32_e32 v5, 8, v5
	v_and_b32_e32 v5, 0xff00, v5
	v_and_b32_e32 v26, 0xff0000, v26
	v_perm_b32 v4, v27, v4, s21
	v_or3_b32 v4, v4, v5, v26
	v_lshlrev_b32_e32 v5, 8, v29
	v_and_b32_e32 v5, 0xff00, v5
	v_and_b32_e32 v26, 0xff0000, v34
	v_perm_b32 v27, v36, v28, s21
	v_or3_b32 v5, v27, v5, v26
	ds_write2st64_b64 v25, v[2:3], v[4:5] offset0:8 offset1:9
	v_mul_f32_e32 v3, v80, v30
	v_mul_f32_e32 v2, v80, v31
	v_rndne_f32_e32 v3, v3
	v_mul_f32_e32 v4, v80, v53
	v_mul_f32_e32 v5, v80, v50
	v_rndne_f32_e32 v2, v2
	v_cvt_i32_f32_e32 v3, v3
	v_rndne_f32_e32 v4, v4
	v_rndne_f32_e32 v5, v5
	v_mul_f32_e32 v27, v80, v51
	v_cvt_i32_f32_e32 v2, v2
	v_cvt_i32_f32_sdwa v4, v4 dst_sel:WORD_1 dst_unused:UNUSED_PAD src0_sel:DWORD
	v_cvt_i32_f32_e32 v5, v5
	v_mul_f32_e32 v26, v80, v54
	v_rndne_f32_e32 v27, v27
	v_mul_f32_e32 v28, v80, v49
	v_mul_f32_e32 v29, v80, v47
	v_rndne_f32_e32 v26, v26
	v_cvt_i32_f32_e32 v27, v27
	v_rndne_f32_e32 v28, v28
	v_rndne_f32_e32 v29, v29
	v_cvt_i32_f32_e32 v26, v26
	v_cvt_i32_f32_sdwa v28, v28 dst_sel:WORD_1 dst_unused:UNUSED_PAD src0_sel:DWORD
	v_cvt_i32_f32_e32 v29, v29
	v_lshlrev_b32_e32 v3, 8, v3
	v_and_b32_e32 v3, 0xff00, v3
	v_and_b32_e32 v4, 0xff0000, v4
	v_perm_b32 v2, v5, v2, s21
	v_or3_b32 v2, v2, v3, v4
	v_lshlrev_b32_e32 v3, 8, v27
	v_and_b32_e32 v3, 0xff00, v3
	v_and_b32_e32 v4, 0xff0000, v28
	v_perm_b32 v5, v29, v26, s21
	v_or3_b32 v3, v5, v3, v4
	v_mul_f32_e32 v5, v80, v35
	v_mul_f32_e32 v4, v80, v37
	v_rndne_f32_e32 v5, v5
	v_mul_f32_e32 v26, v80, v59
	v_mul_f32_e32 v27, v80, v57
	v_rndne_f32_e32 v4, v4
	v_cvt_i32_f32_e32 v5, v5
	v_rndne_f32_e32 v26, v26
	v_rndne_f32_e32 v27, v27
	v_mul_f32_e32 v29, v80, v56
	v_cvt_i32_f32_e32 v4, v4
	v_cvt_i32_f32_sdwa v26, v26 dst_sel:WORD_1 dst_unused:UNUSED_PAD src0_sel:DWORD
	v_cvt_i32_f32_e32 v27, v27
	v_mul_f32_e32 v28, v80, v58
	v_rndne_f32_e32 v29, v29
	v_mul_f32_e32 v30, v80, v55
	v_mul_f32_e32 v31, v80, v52
	v_rndne_f32_e32 v28, v28
	v_cvt_i32_f32_e32 v29, v29
	v_rndne_f32_e32 v30, v30
	v_rndne_f32_e32 v31, v31
	v_cvt_i32_f32_e32 v28, v28
	v_cvt_i32_f32_sdwa v30, v30 dst_sel:WORD_1 dst_unused:UNUSED_PAD src0_sel:DWORD
	v_cvt_i32_f32_e32 v31, v31
	v_lshlrev_b32_e32 v5, 8, v5
	v_and_b32_e32 v5, 0xff00, v5
	v_and_b32_e32 v26, 0xff0000, v26
	v_perm_b32 v4, v27, v4, s21
	v_or3_b32 v4, v4, v5, v26
	v_lshlrev_b32_e32 v5, 8, v29
	v_and_b32_e32 v5, 0xff00, v5
	v_and_b32_e32 v26, 0xff0000, v30
	v_perm_b32 v27, v31, v28, s21
	v_or3_b32 v5, v27, v5, v26
	ds_write2st64_b64 v25, v[2:3], v[4:5] offset0:10 offset1:11
	v_mul_f32_e32 v3, v80, v21
	v_mul_f32_e32 v2, v80, v20
	v_rndne_f32_e32 v3, v3
	v_mul_f32_e32 v4, v80, v22
	v_mul_f32_e32 v5, v80, v23
	v_rndne_f32_e32 v2, v2
	v_cvt_i32_f32_e32 v3, v3
	v_rndne_f32_e32 v4, v4
	v_rndne_f32_e32 v5, v5
	v_mul_f32_e32 v21, v80, v63
	v_cvt_i32_f32_e32 v2, v2
	v_cvt_i32_f32_sdwa v4, v4 dst_sel:WORD_1 dst_unused:UNUSED_PAD src0_sel:DWORD
	v_cvt_i32_f32_e32 v5, v5
	v_mul_f32_e32 v20, v80, v60
	v_rndne_f32_e32 v21, v21
	v_mul_f32_e32 v22, v80, v64
	v_mul_f32_e32 v23, v80, v65
	v_rndne_f32_e32 v20, v20
	v_cvt_i32_f32_e32 v21, v21
	v_rndne_f32_e32 v22, v22
	v_rndne_f32_e32 v23, v23
	v_cvt_i32_f32_e32 v20, v20
	v_cvt_i32_f32_sdwa v22, v22 dst_sel:WORD_1 dst_unused:UNUSED_PAD src0_sel:DWORD
	v_cvt_i32_f32_e32 v23, v23
	v_lshlrev_b32_e32 v3, 8, v3
	v_and_b32_e32 v3, 0xff00, v3
	v_and_b32_e32 v4, 0xff0000, v4
	v_perm_b32 v2, v5, v2, s21
	v_or3_b32 v2, v2, v3, v4
	v_lshlrev_b32_e32 v3, 8, v21
	v_and_b32_e32 v3, 0xff00, v3
	v_and_b32_e32 v4, 0xff0000, v22
	v_perm_b32 v5, v23, v20, s21
	v_or3_b32 v3, v5, v3, v4
; #define LAS __attribute__((address_space(3)))
; __device__ __forceinline__ float bflo(unsigned w) { return __uint_as_float(w << 16); }
; __device__ __forceinline__ float bfhi(unsigned w) { return __uint_as_float(w & 0xffff0000u); }
; __device__ __forceinline__ float wave_sum(float v) { v = dpp_add16(v); return (rdlane(v, 0) + rdlane(v, 16)) + (rdlane(v, 32) + rdlane(v, 48)); }
; __device__ __forceinline__ float wave_max(float v) { v = dpp_max16(v); return fmaxf(fmaxf(rdlane(v, 0), rdlane(v, 16)), fmaxf(rdlane(v, 32), rdlane(v, 48))); }
; __device__ __forceinline__ void p12_peer(Frame& F) {
;     ...
;         for (int j = 0; j < 8; ++j) { xp[j] = ((const v4u*)(HN + (size_t)t * D_))[F.lane + 64 * j];
;             mxa = fmaxf(fmaxf(fmaxf(mxa, fmaxf(fabsf(bflo(xp[j].x)), fabsf(bfhi(xp[j].x)))), fmaxf(fabsf(bflo(xp[j].y)), fabsf(bfhi(xp[j].y)))), fmaxf(fmaxf(fabsf(bflo(xp[j].z)), fabsf(bfhi(xp[j].z))), fmaxf(fabsf(bflo(xp[j].w)), fabsf(bfhi(xp[j].w))))); }
;         mxa = wave_max(mxa); const float inv = mxa > 0.f ? 127.0f / mxa : 0.f;
;         const float rsn = 1.0f / sqrtf(wave_sum(PSQ[(size_t)t * 64 + F.lane]) * (1.f / D_) + 1e-6f);
;         sx[i] = mxa * rsn * (1.0f / 127.0f);
; #pragma unroll
;         for (int j = 0; j < 8; ++j) {
;             const int q0 = (int)rintf(bflo(xp[j].x) * inv), q1 = (int)rintf(bfhi(xp[j].x) * inv), q2 = (int)rintf(bflo(xp[j].y) * inv), q3 = (int)rintf(bfhi(xp[j].y) * inv);
;             const int q4 = (int)rintf(bflo(xp[j].z) * inv), q5 = (int)rintf(bfhi(xp[j].z) * inv), q6 = (int)rintf(bflo(xp[j].w) * inv), q7 = (int)rintf(bfhi(xp[j].w) * inv);
;             *(LAS v2u*)(XQ + i * 4096 + 8 * (F.lane + 64 * j)) = (v2u){(unsigned)((q0 & 0xff) | ((q1 & 0xff) << 8) | ((q2 & 0xff) << 16) | (q3 << 24)), (unsigned)((q4 & 0xff) | ((q5 & 0xff) << 8) | ((q6 & 0xff) << 16) | (q7 << 24))}; }
;         EL[i * 128 + F.lane] = (unsigned short)PIDX[(size_t)t * 128 + F.lane]; EL[i * 128 + 64 + F.lane] = (unsigned short)PIDX[(size_t)t * 128 + 64 + F.lane];
	v_mul_f32_e32 v5, v80, v67
	v_mul_f32_e32 v4, v80, v66
	v_rndne_f32_e32 v5, v5
	v_mul_f32_e32 v20, v80, v68
	v_mul_f32_e32 v21, v80, v69
	v_rndne_f32_e32 v4, v4
	v_cvt_i32_f32_e32 v5, v5
	v_rndne_f32_e32 v20, v20
	v_rndne_f32_e32 v21, v21
	v_mul_f32_e32 v6, v80, v6
	v_cvt_i32_f32_e32 v4, v4
	v_cvt_i32_f32_sdwa v20, v20 dst_sel:WORD_1 dst_unused:UNUSED_PAD src0_sel:DWORD
	v_cvt_i32_f32_e32 v21, v21
	v_mul_f32_e32 v22, v80, v70
	v_rndne_f32_e32 v6, v6
	v_mul_f32_e32 v23, v80, v71
	v_mul_f32_e32 v7, v80, v7
	v_rndne_f32_e32 v22, v22
	v_cvt_i32_f32_e32 v6, v6
	v_rndne_f32_e32 v23, v23
	v_rndne_f32_e32 v7, v7
	v_cvt_i32_f32_e32 v22, v22
	v_cvt_i32_f32_sdwa v23, v23 dst_sel:WORD_1 dst_unused:UNUSED_PAD src0_sel:DWORD
	v_cvt_i32_f32_e32 v7, v7
	v_lshlrev_b32_e32 v5, 8, v5
	v_and_b32_e32 v5, 0xff00, v5
	v_and_b32_e32 v20, 0xff0000, v20
	v_perm_b32 v4, v21, v4, s21
	v_or3_b32 v4, v4, v5, v20
	v_lshlrev_b32_e32 v5, 8, v6
	v_and_b32_e32 v5, 0xff00, v5
	v_and_b32_e32 v6, 0xff0000, v23
	v_perm_b32 v7, v7, v22, s21
	v_or3_b32 v5, v7, v5, v6
	ds_write2st64_b64 v25, v[2:3], v[4:5] offset0:12 offset1:13
	v_mul_f32_e32 v3, v80, v8
	v_mul_f32_e32 v2, v80, v72
	v_rndne_f32_e32 v3, v3
	v_mul_f32_e32 v4, v80, v73
	v_mul_f32_e32 v5, v80, v9
	v_rndne_f32_e32 v2, v2
	v_cvt_i32_f32_e32 v3, v3
	v_rndne_f32_e32 v4, v4
	v_rndne_f32_e32 v5, v5
	v_mul_f32_e32 v7, v80, v10
	v_cvt_i32_f32_e32 v2, v2
	v_cvt_i32_f32_sdwa v4, v4 dst_sel:WORD_1 dst_unused:UNUSED_PAD src0_sel:DWORD
	v_cvt_i32_f32_e32 v5, v5
	v_mul_f32_e32 v6, v80, v74
	v_rndne_f32_e32 v7, v7
	v_mul_f32_e32 v8, v80, v75
	v_mul_f32_e32 v9, v80, v11
	v_rndne_f32_e32 v6, v6
	v_cvt_i32_f32_e32 v7, v7
	v_rndne_f32_e32 v8, v8
	v_rndne_f32_e32 v9, v9
	v_cvt_i32_f32_e32 v6, v6
	v_cvt_i32_f32_sdwa v8, v8 dst_sel:WORD_1 dst_unused:UNUSED_PAD src0_sel:DWORD
	v_cvt_i32_f32_e32 v9, v9
	v_lshlrev_b32_e32 v3, 8, v3
	v_and_b32_e32 v3, 0xff00, v3
	v_and_b32_e32 v4, 0xff0000, v4
	v_perm_b32 v2, v5, v2, s21
	v_or3_b32 v2, v2, v3, v4
	v_lshlrev_b32_e32 v3, 8, v7
	v_and_b32_e32 v3, 0xff00, v3
	v_and_b32_e32 v4, 0xff0000, v8
	v_perm_b32 v5, v9, v6, s21
	v_or3_b32 v3, v5, v3, v4
	v_mul_f32_e32 v5, v80, v12
	v_mul_f32_e32 v4, v80, v76
	v_rndne_f32_e32 v5, v5
	v_mul_f32_e32 v6, v80, v77
	v_mul_f32_e32 v7, v80, v13
	v_rndne_f32_e32 v4, v4
	v_cvt_i32_f32_e32 v5, v5
	v_rndne_f32_e32 v6, v6
	v_rndne_f32_e32 v7, v7
	v_mul_f32_e32 v9, v80, v14
	v_cvt_i32_f32_e32 v4, v4
	v_cvt_i32_f32_sdwa v6, v6 dst_sel:WORD_1 dst_unused:UNUSED_PAD src0_sel:DWORD
	v_cvt_i32_f32_e32 v7, v7
	v_mul_f32_e32 v8, v80, v78
	v_rndne_f32_e32 v9, v9
	v_mul_f32_e32 v10, v80, v79
	v_mul_f32_e32 v11, v80, v15
	v_rndne_f32_e32 v8, v8
	v_cvt_i32_f32_e32 v9, v9
	v_rndne_f32_e32 v10, v10
	v_rndne_f32_e32 v11, v11
	v_cvt_i32_f32_e32 v8, v8
	v_cvt_i32_f32_sdwa v10, v10 dst_sel:WORD_1 dst_unused:UNUSED_PAD src0_sel:DWORD
	v_cvt_i32_f32_e32 v11, v11
	v_lshlrev_b32_e32 v5, 8, v5
	v_and_b32_e32 v5, 0xff00, v5
	v_and_b32_e32 v6, 0xff0000, v6
	v_perm_b32 v4, v7, v4, s21
	v_or3_b32 v4, v4, v5, v6
	v_lshlrev_b32_e32 v5, 8, v9
	v_and_b32_e32 v5, 0xff00, v5
	v_and_b32_e32 v6, 0xff0000, v10
	v_perm_b32 v7, v11, v8, s21
	v_or3_b32 v5, v7, v5, v6
	ds_write2st64_b64 v25, v[2:3], v[4:5] offset0:14 offset1:15
	s_waitcnt vmcnt(1)
	ds_write_b16 v24, v61 offset:16640
	s_waitcnt vmcnt(0)
	ds_write_b16 v24, v62 offset:16768
	global_load_dwordx4 v[4:7], v[0:1], off
	global_load_dwordx4 v[8:11], v[0:1], off offset:1024
	global_load_dwordx4 v[12:15], v[0:1], off offset:2048
	global_load_dwordx4 v[60:63], v[0:1], off offset:3072
	v_add_co_u32_e32 v56, vcc, s28, v0
	v_lshl_add_u64 v[20:21], s[10:11], 0, v[16:17]
	s_nop 0
	v_addc_co_u32_e32 v57, vcc, 0, v1, vcc
	s_add_u32 s10, s18, s14
	s_addc_u32 s11, s19, s15
	v_lshl_add_u64 v[22:23], s[10:11], 0, v[16:17]
	s_add_i32 s10, s8, s34
	s_ashr_i32 s11, s10, 31
	s_lshl_b64 s[12:13], s[10:11], 13
	s_add_u32 s12, s6, s12
	s_addc_u32 s13, s7, s13
	v_readlane_b32 s36, v32, 32
	v_readlane_b32 s38, v32, 48
	s_waitcnt vmcnt(3)
	v_lshlrev_b32_e32 v27, 16, v4
	v_and_b32_e32 v26, 0xffff0000, v4
	v_max_f32_e64 v2, |v26|, |v26|
	v_max_f32_e64 v3, |v27|, |v27|
	v_max_f32_e32 v4, v3, v2
	global_load_dwordx4 v[0:3], v[56:57], off
	v_lshlrev_b32_e32 v42, 16, v5
	v_and_b32_e32 v39, 0xffff0000, v5
	v_max_f32_e64 v5, |v39|, |v39|
	v_max_f32_e64 v28, |v42|, |v42|
	v_max_f32_e32 v5, v28, v5
	v_lshlrev_b32_e32 v37, 16, v7
	v_and_b32_e32 v35, 0xffff0000, v7
	v_max3_f32 v30, v4, 0, v5
	v_max_f32_e64 v4, |v35|, |v35|
	v_max_f32_e64 v5, |v37|, |v37|
	v_lshlrev_b32_e32 v43, 16, v6
	v_and_b32_e32 v40, 0xffff0000, v6
	v_max_f32_e32 v4, v5, v4
	v_max3_f32 v31, |v43|, |v40|, v4
	s_waitcnt vmcnt(3)
	v_lshlrev_b32_e32 v29, 16, v8
	v_and_b32_e32 v28, 0xffff0000, v8
	global_load_dwordx4 v[4:7], v[56:57], off offset:1024
	v_max_f32_e64 v8, |v28|, |v28|
	v_max_f32_e64 v34, |v29|, |v29|
	v_max_f32_e32 v8, v34, v8
	v_lshlrev_b32_e32 v49, 16, v9
	v_and_b32_e32 v46, 0xffff0000, v9
	v_lshlrev_b32_e32 v44, 16, v11
	v_and_b32_e32 v41, 0xffff0000, v11
	v_max3_f32 v8, v30, v31, v8
	v_max_f32_e64 v9, |v46|, |v46|
	v_max_f32_e64 v30, |v49|, |v49|
	v_lshlrev_b32_e32 v47, 16, v10
	v_and_b32_e32 v45, 0xffff0000, v10
	v_max_f32_e64 v10, |v41|, |v41|
	v_max_f32_e64 v11, |v44|, |v44|
	v_max_f32_e32 v9, v30, v9
	v_max_f32_e32 v10, v11, v10
	s_waitcnt vmcnt(3)
; #define LAS __attribute__((address_space(3)))
; __device__ __forceinline__ float bflo(unsigned w) { return __uint_as_float(w << 16); }
; __device__ __forceinline__ float bfhi(unsigned w) { return __uint_as_float(w & 0xffff0000u); }
; __device__ __forceinline__ float wave_sum(float v) { v = dpp_add16(v); return (rdlane(v, 0) + rdlane(v, 16)) + (rdlane(v, 32) + rdlane(v, 48)); }
; __device__ __forceinline__ float wave_max(float v) { v = dpp_max16(v); return fmaxf(fmaxf(rdlane(v, 0), rdlane(v, 16)), fmaxf(rdlane(v, 32), rdlane(v, 48))); }
; __device__ __forceinline__ void p12_peer(Frame& F) {
;     ...
;         for (int j = 0; j < 8; ++j) { xp[j] = ((const v4u*)(HN + (size_t)t * D_))[F.lane + 64 * j];
;             mxa = fmaxf(fmaxf(fmaxf(mxa, fmaxf(fabsf(bflo(xp[j].x)), fabsf(bfhi(xp[j].x)))), fmaxf(fabsf(bflo(xp[j].y)), fabsf(bfhi(xp[j].y)))), fmaxf(fmaxf(fabsf(bflo(xp[j].z)), fabsf(bfhi(xp[j].z))), fmaxf(fabsf(bflo(xp[j].w)), fabsf(bfhi(xp[j].w))))); }
;         mxa = wave_max(mxa); const float inv = mxa > 0.f ? 127.0f / mxa : 0.f;
;         const float rsn = 1.0f / sqrtf(wave_sum(PSQ[(size_t)t * 64 + F.lane]) * (1.f / D_) + 1e-6f);
;         sx[i] = mxa * rsn * (1.0f / 127.0f);
; #pragma unroll
;         for (int j = 0; j < 8; ++j) {
;             const int q0 = (int)rintf(bflo(xp[j].x) * inv), q1 = (int)rintf(bfhi(xp[j].x) * inv), q2 = (int)rintf(bflo(xp[j].y) * inv), q3 = (int)rintf(bfhi(xp[j].y) * inv);
;             const int q4 = (int)rintf(bflo(xp[j].z) * inv), q5 = (int)rintf(bfhi(xp[j].z) * inv), q6 = (int)rintf(bflo(xp[j].w) * inv), q7 = (int)rintf(bfhi(xp[j].w) * inv);
;             *(LAS v2u*)(XQ + i * 4096 + 8 * (F.lane + 64 * j)) = (v2u){(unsigned)((q0 & 0xff) | ((q1 & 0xff) << 8) | ((q2 & 0xff) << 16) | (q3 << 24)), (unsigned)((q4 & 0xff) | ((q5 & 0xff) << 8) | ((q6 & 0xff) << 16) | (q7 << 24))}; }
	v_lshlrev_b32_e32 v31, 16, v12
	v_and_b32_e32 v30, 0xffff0000, v12
	v_max3_f32 v10, |v47|, |v45|, v10
	v_max_f32_e64 v12, |v30|, |v30|
	v_max_f32_e64 v36, |v31|, |v31|
	v_lshlrev_b32_e32 v54, 16, v13
	v_and_b32_e32 v51, 0xffff0000, v13
	v_max3_f32 v34, v8, v9, v10
	global_load_dwordx4 v[8:11], v[56:57], off offset:2048
	v_max_f32_e32 v12, v36, v12
	v_max_f32_e64 v13, |v51|, |v51|
	v_max_f32_e64 v36, |v54|, |v54|
	v_max_f32_e32 v13, v36, v13
	v_lshlrev_b32_e32 v50, 16, v15
	v_and_b32_e32 v48, 0xffff0000, v15
	v_max3_f32 v34, v34, v12, v13
	v_max_f32_e64 v12, |v48|, |v48|
	v_max_f32_e64 v13, |v50|, |v50|
	v_lshlrev_b32_e32 v55, 16, v14
	v_and_b32_e32 v52, 0xffff0000, v14
	v_max_f32_e32 v12, v13, v12
	v_max3_f32 v53, |v55|, |v52|, v12
	global_load_dwordx4 v[12:15], v[56:57], off offset:3072
	s_waitcnt vmcnt(4)
	v_lshlrev_b32_e32 v38, 16, v60
	v_and_b32_e32 v36, 0xffff0000, v60
	v_max_f32_e64 v56, |v36|, |v36|
	v_max_f32_e64 v57, |v38|, |v38|
	v_max_f32_e32 v56, v57, v56
	v_lshlrev_b32_e32 v60, 16, v61
	v_and_b32_e32 v58, 0xffff0000, v61
	v_max3_f32 v34, v34, v53, v56
	v_max_f32_e64 v53, |v58|, |v58|
	v_max_f32_e64 v56, |v60|, |v60|
	v_max_f32_e32 v61, v56, v53
	v_lshlrev_b32_e32 v56, 16, v63
	v_and_b32_e32 v53, 0xffff0000, v63
	v_lshlrev_b32_e32 v59, 16, v62
	v_and_b32_e32 v57, 0xffff0000, v62
	v_max_f32_e64 v62, |v53|, |v53|
	v_max_f32_e64 v63, |v56|, |v56|
	v_max_f32_e32 v62, v63, v62
	v_max3_f32 v62, |v59|, |v57|, v62
	v_max3_f32 v61, v34, v61, v62
	global_load_dword v34, v[20:21], off
	global_load_dword v62, v[22:23], off
	global_load_dword v63, v[22:23], off offset:256
	s_waitcnt vmcnt(6)
	v_lshlrev_b32_e32 v20, 16, v0
	v_and_b32_e32 v21, 0xffff0000, v0
	v_max_f32_e64 v0, |v21|, |v21|
	v_max_f32_e64 v22, |v20|, |v20|
	v_max_f32_e32 v0, v22, v0
	v_lshlrev_b32_e32 v22, 16, v1
	v_and_b32_e32 v23, 0xffff0000, v1
	v_max_f32_e64 v1, |v23|, |v23|
	v_max_f32_e64 v64, |v22|, |v22|
	v_max_f32_e32 v1, v64, v1
	v_lshlrev_b32_e32 v65, 16, v3
	v_and_b32_e32 v66, 0xffff0000, v3
	v_max3_f32 v0, v61, v0, v1
	v_lshlrev_b32_e32 v61, 16, v2
	v_and_b32_e32 v64, 0xffff0000, v2
	v_max_f32_e64 v1, |v66|, |v66|
	v_max_f32_e64 v2, |v65|, |v65|
	s_waitcnt vmcnt(5)
	v_lshlrev_b32_e32 v67, 16, v4
	v_and_b32_e32 v68, 0xffff0000, v4
	v_max_f32_e32 v1, v2, v1
	v_max_f32_e64 v2, |v68|, |v68|
	v_max_f32_e64 v3, |v67|, |v67|
	v_max3_f32 v1, |v61|, |v64|, v1
	v_max_f32_e32 v2, v3, v2
	v_lshlrev_b32_e32 v69, 16, v5
	v_and_b32_e32 v70, 0xffff0000, v5
	v_max3_f32 v0, v0, v1, v2
	v_max_f32_e64 v1, |v70|, |v70|
	v_max_f32_e64 v2, |v69|, |v69|
	v_lshlrev_b32_e32 v72, 16, v7
	v_and_b32_e32 v7, 0xffff0000, v7
	v_max_f32_e32 v1, v2, v1
	v_max_f32_e64 v2, |v7|, |v7|
	v_max_f32_e64 v3, |v72|, |v72|
	v_lshlrev_b32_e32 v71, 16, v6
	v_and_b32_e32 v6, 0xffff0000, v6
	v_max_f32_e32 v2, v3, v2
	v_max3_f32 v2, |v71|, |v6|, v2
	v_max3_f32 v0, v0, v1, v2
	s_waitcnt vmcnt(4)
	v_lshlrev_b32_e32 v73, 16, v8
	v_and_b32_e32 v8, 0xffff0000, v8
	v_max_f32_e64 v1, |v8|, |v8|
	v_max_f32_e64 v2, |v73|, |v73|
	v_lshlrev_b32_e32 v74, 16, v9
	v_and_b32_e32 v9, 0xffff0000, v9
	v_max_f32_e32 v1, v2, v1
	v_max_f32_e64 v2, |v9|, |v9|
	v_max_f32_e64 v3, |v74|, |v74|
	v_max_f32_e32 v2, v3, v2
	v_lshlrev_b32_e32 v76, 16, v11
	v_and_b32_e32 v11, 0xffff0000, v11
	v_max3_f32 v0, v0, v1, v2
	v_max_f32_e64 v1, |v11|, |v11|
	v_max_f32_e64 v2, |v76|, |v76|
	s_waitcnt vmcnt(3)
	v_lshlrev_b32_e32 v77, 16, v12
	v_and_b32_e32 v12, 0xffff0000, v12
	v_lshlrev_b32_e32 v75, 16, v10
	v_and_b32_e32 v10, 0xffff0000, v10
	v_max_f32_e32 v1, v2, v1
	v_max_f32_e64 v2, |v12|, |v12|
	v_max_f32_e64 v3, |v77|, |v77|
	v_max3_f32 v1, |v75|, |v10|, v1
	v_max_f32_e32 v2, v3, v2
	v_lshlrev_b32_e32 v78, 16, v13
	v_and_b32_e32 v13, 0xffff0000, v13
	v_max3_f32 v0, v0, v1, v2
	v_max_f32_e64 v1, |v13|, |v13|
	v_max_f32_e64 v2, |v78|, |v78|
	v_lshlrev_b32_e32 v80, 16, v15
	v_and_b32_e32 v15, 0xffff0000, v15
	v_max_f32_e32 v1, v2, v1
	v_max_f32_e64 v2, |v15|, |v15|
	v_max_f32_e64 v3, |v80|, |v80|
	v_lshlrev_b32_e32 v79, 16, v14
	v_and_b32_e32 v14, 0xffff0000, v14
	v_max_f32_e32 v2, v3, v2
	v_max3_f32 v2, |v79|, |v14|, v2
	v_max3_f32 v0, v0, v1, v2
	v_mov_b32_e32 v1, 0
	s_nop 1
	v_mov_b32_dpp v1, v0 quad_perm:[1,0,3,2] row_mask:0xf bank_mask:0xf
	v_max_f32_e32 v1, v1, v1
	v_max_f32_e32 v0, v0, v1
	v_mov_b32_e32 v1, 0
	s_nop 1
	v_mov_b32_dpp v1, v0 quad_perm:[2,3,0,1] row_mask:0xf bank_mask:0xf
	v_max_f32_e32 v1, v1, v1
	v_max_f32_e32 v0, v0, v1
	v_mov_b32_e32 v1, 0
	s_nop 1
	v_mov_b32_dpp v1, v0 row_half_mirror row_mask:0xf bank_mask:0xf
	v_max_f32_e32 v1, v1, v1
	v_max_f32_e32 v0, v0, v1
	v_mov_b32_e32 v1, 0
	s_nop 1
	v_mov_b32_dpp v1, v0 row_mirror row_mask:0xf bank_mask:0xf
	v_max_f32_e32 v1, v1, v1
	v_max_f32_e32 v0, v0, v1
	s_nop 0
	v_readlane_b32 s33, v0, 32
	v_readlane_b32 s35, v0, 48
	v_readlane_b32 s30, v0, 0
	v_readlane_b32 s31, v0, 16
	v_max_f32_e64 v0, s35, s35
	v_max_f32_e64 v1, s33, s33
	v_max_f32_e32 v0, v1, v0
	v_mov_b32_e32 v1, s31
	v_max3_f32 v161, s30, v1, v0
	v_div_scale_f32 v2, s[30:31], v161, v161, s29
	v_rcp_f32_e32 v3, v2
	v_lshl_add_u64 v[0:1], s[12:13], 0, v[18:19]
	s_lshl_b64 s[12:13], s[10:11], 8
	s_add_u32 s12, s22, s12
	v_fma_f32 v4, -v2, v3, 1.0
	v_fmac_f32_e32 v3, v4, v3
	v_div_scale_f32 v4, vcc, s29, v161, s29
	v_mul_f32_e32 v5, v4, v3
	v_fma_f32 v18, -v2, v5, v4
	v_fmac_f32_e32 v5, v18, v3
	v_fma_f32 v2, -v2, v5, v4
	v_div_fmas_f32 v2, v2, v3, v5
	v_div_fixup_f32 v2, v2, v161, s29
	v_cmp_lt_f32_e32 vcc, 0, v161
	s_addc_u32 s13, s23, s13
	v_readlane_b32 s35, v32, 0
	v_cndmask_b32_e32 v18, 0, v2, vcc
	v_mul_f32_e32 v3, v18, v26
	v_mul_f32_e32 v2, v18, v27
	v_rndne_f32_e32 v3, v3
	v_mul_f32_e32 v4, v18, v42
; #define LAS __attribute__((address_space(3)))
; __device__ __forceinline__ float bflo(unsigned w) { return __uint_as_float(w << 16); }
; __device__ __forceinline__ float bfhi(unsigned w) { return __uint_as_float(w & 0xffff0000u); }
; __device__ __forceinline__ void p12_peer(Frame& F) {
;     ...
;         for (int j = 0; j < 8; ++j) {
;             const int q0 = (int)rintf(bflo(xp[j].x) * inv), q1 = (int)rintf(bfhi(xp[j].x) * inv), q2 = (int)rintf(bflo(xp[j].y) * inv), q3 = (int)rintf(bfhi(xp[j].y) * inv);
;             const int q4 = (int)rintf(bflo(xp[j].z) * inv), q5 = (int)rintf(bfhi(xp[j].z) * inv), q6 = (int)rintf(bflo(xp[j].w) * inv), q7 = (int)rintf(bfhi(xp[j].w) * inv);
;             *(LAS v2u*)(XQ + i * 4096 + 8 * (F.lane + 64 * j)) = (v2u){(unsigned)((q0 & 0xff) | ((q1 & 0xff) << 8) | ((q2 & 0xff) << 16) | (q3 << 24)), (unsigned)((q4 & 0xff) | ((q5 & 0xff) << 8) | ((q6 & 0xff) << 16) | (q7 << 24))}; }
	v_mul_f32_e32 v5, v18, v39
	v_rndne_f32_e32 v2, v2
	v_cvt_i32_f32_e32 v3, v3
	v_rndne_f32_e32 v4, v4
	v_rndne_f32_e32 v5, v5
	v_mul_f32_e32 v26, v18, v40
	v_cvt_i32_f32_e32 v2, v2
	v_cvt_i32_f32_sdwa v4, v4 dst_sel:WORD_1 dst_unused:UNUSED_PAD src0_sel:DWORD
	v_cvt_i32_f32_e32 v5, v5
	v_mul_f32_e32 v19, v18, v43
	v_rndne_f32_e32 v26, v26
	v_mul_f32_e32 v27, v18, v37
	v_mul_f32_e32 v35, v18, v35
	v_rndne_f32_e32 v19, v19
	v_cvt_i32_f32_e32 v26, v26
	v_rndne_f32_e32 v27, v27
	v_rndne_f32_e32 v35, v35
	v_cvt_i32_f32_e32 v19, v19
	v_cvt_i32_f32_sdwa v27, v27 dst_sel:WORD_1 dst_unused:UNUSED_PAD src0_sel:DWORD
	v_cvt_i32_f32_e32 v35, v35
	v_lshlrev_b32_e32 v3, 8, v3
	v_and_b32_e32 v3, 0xff00, v3
	v_and_b32_e32 v4, 0xff0000, v4
	v_perm_b32 v2, v5, v2, s21
	v_or3_b32 v2, v2, v3, v4
	v_lshlrev_b32_e32 v3, 8, v26
	v_and_b32_e32 v3, 0xff00, v3
	v_and_b32_e32 v4, 0xff0000, v27
	v_perm_b32 v5, v35, v19, s21
	v_or3_b32 v3, v5, v3, v4
	v_mul_f32_e32 v5, v18, v28
	v_mul_f32_e32 v4, v18, v29
	v_rndne_f32_e32 v5, v5
	v_mul_f32_e32 v19, v18, v49
	v_mul_f32_e32 v26, v18, v46
	v_rndne_f32_e32 v4, v4
	v_cvt_i32_f32_e32 v5, v5
	v_rndne_f32_e32 v19, v19
	v_rndne_f32_e32 v26, v26
	v_mul_f32_e32 v28, v18, v45
	v_cvt_i32_f32_e32 v4, v4
	v_cvt_i32_f32_sdwa v19, v19 dst_sel:WORD_1 dst_unused:UNUSED_PAD src0_sel:DWORD
	v_cvt_i32_f32_e32 v26, v26
	v_mul_f32_e32 v27, v18, v47
	v_rndne_f32_e32 v28, v28
	v_mul_f32_e32 v29, v18, v44
	v_mul_f32_e32 v35, v18, v41
	v_rndne_f32_e32 v27, v27
	v_cvt_i32_f32_e32 v28, v28
	v_rndne_f32_e32 v29, v29
	v_rndne_f32_e32 v35, v35
	v_cvt_i32_f32_e32 v27, v27
	v_cvt_i32_f32_sdwa v29, v29 dst_sel:WORD_1 dst_unused:UNUSED_PAD src0_sel:DWORD
	v_cvt_i32_f32_e32 v35, v35
	v_lshlrev_b32_e32 v5, 8, v5
	v_and_b32_e32 v5, 0xff00, v5
	v_and_b32_e32 v19, 0xff0000, v19
	v_perm_b32 v4, v26, v4, s21
	v_or3_b32 v4, v4, v5, v19
	v_lshlrev_b32_e32 v5, 8, v28
	v_and_b32_e32 v5, 0xff00, v5
	v_and_b32_e32 v19, 0xff0000, v29
	v_perm_b32 v26, v35, v27, s21
	v_or3_b32 v5, v26, v5, v19
	ds_write2st64_b64 v25, v[2:3], v[4:5] offset0:16 offset1:17
	v_mul_f32_e32 v3, v18, v30
	v_mul_f32_e32 v2, v18, v31
	v_rndne_f32_e32 v3, v3
	v_mul_f32_e32 v4, v18, v54
	v_mul_f32_e32 v5, v18, v51
	v_rndne_f32_e32 v2, v2
	v_cvt_i32_f32_e32 v3, v3
	v_rndne_f32_e32 v4, v4
	v_rndne_f32_e32 v5, v5
	v_mul_f32_e32 v26, v18, v52
	v_cvt_i32_f32_e32 v2, v2
	v_cvt_i32_f32_sdwa v4, v4 dst_sel:WORD_1 dst_unused:UNUSED_PAD src0_sel:DWORD
	v_cvt_i32_f32_e32 v5, v5
	v_mul_f32_e32 v19, v18, v55
	v_rndne_f32_e32 v26, v26
	v_mul_f32_e32 v27, v18, v50
	v_mul_f32_e32 v28, v18, v48
	v_rndne_f32_e32 v19, v19
	v_cvt_i32_f32_e32 v26, v26
	v_rndne_f32_e32 v27, v27
	v_rndne_f32_e32 v28, v28
	v_cvt_i32_f32_e32 v19, v19
	v_cvt_i32_f32_sdwa v27, v27 dst_sel:WORD_1 dst_unused:UNUSED_PAD src0_sel:DWORD
	v_cvt_i32_f32_e32 v28, v28
	v_lshlrev_b32_e32 v3, 8, v3
	v_and_b32_e32 v3, 0xff00, v3
	v_and_b32_e32 v4, 0xff0000, v4
	v_perm_b32 v2, v5, v2, s21
	v_or3_b32 v2, v2, v3, v4
	v_lshlrev_b32_e32 v3, 8, v26
	v_and_b32_e32 v3, 0xff00, v3
	v_and_b32_e32 v4, 0xff0000, v27
	v_perm_b32 v5, v28, v19, s21
	v_or3_b32 v3, v5, v3, v4
	v_mul_f32_e32 v5, v18, v36
	v_mul_f32_e32 v4, v18, v38
	v_rndne_f32_e32 v5, v5
	v_mul_f32_e32 v19, v18, v60
	v_mul_f32_e32 v26, v18, v58
	v_rndne_f32_e32 v4, v4
	v_cvt_i32_f32_e32 v5, v5
	v_rndne_f32_e32 v19, v19
	v_rndne_f32_e32 v26, v26
	v_mul_f32_e32 v28, v18, v57
	v_cvt_i32_f32_e32 v4, v4
	v_cvt_i32_f32_sdwa v19, v19 dst_sel:WORD_1 dst_unused:UNUSED_PAD src0_sel:DWORD
	v_cvt_i32_f32_e32 v26, v26
	v_mul_f32_e32 v27, v18, v59
	v_rndne_f32_e32 v28, v28
	v_mul_f32_e32 v29, v18, v56
	v_mul_f32_e32 v30, v18, v53
	v_rndne_f32_e32 v27, v27
	v_cvt_i32_f32_e32 v28, v28
	v_rndne_f32_e32 v29, v29
	v_rndne_f32_e32 v30, v30
	v_cvt_i32_f32_e32 v27, v27
	v_cvt_i32_f32_sdwa v29, v29 dst_sel:WORD_1 dst_unused:UNUSED_PAD src0_sel:DWORD
	v_cvt_i32_f32_e32 v30, v30
	v_lshlrev_b32_e32 v5, 8, v5
	v_and_b32_e32 v5, 0xff00, v5
	v_and_b32_e32 v19, 0xff0000, v19
	v_perm_b32 v4, v26, v4, s21
	v_or3_b32 v4, v4, v5, v19
	v_lshlrev_b32_e32 v5, 8, v28
	v_and_b32_e32 v5, 0xff00, v5
	v_and_b32_e32 v19, 0xff0000, v29
	v_perm_b32 v26, v30, v27, s21
	v_or3_b32 v5, v26, v5, v19
	ds_write2st64_b64 v25, v[2:3], v[4:5] offset0:18 offset1:19
	v_mul_f32_e32 v3, v18, v21
	v_mul_f32_e32 v2, v18, v20
	v_rndne_f32_e32 v3, v3
	v_mul_f32_e32 v4, v18, v22
	v_mul_f32_e32 v5, v18, v23
	v_rndne_f32_e32 v2, v2
	v_cvt_i32_f32_e32 v3, v3
	v_rndne_f32_e32 v4, v4
	v_rndne_f32_e32 v5, v5
	v_mul_f32_e32 v20, v18, v64
	v_cvt_i32_f32_e32 v2, v2
	v_cvt_i32_f32_sdwa v4, v4 dst_sel:WORD_1 dst_unused:UNUSED_PAD src0_sel:DWORD
	v_cvt_i32_f32_e32 v5, v5
	v_mul_f32_e32 v19, v18, v61
	v_rndne_f32_e32 v20, v20
	v_mul_f32_e32 v21, v18, v65
	v_mul_f32_e32 v22, v18, v66
	v_rndne_f32_e32 v19, v19
	v_cvt_i32_f32_e32 v20, v20
	v_rndne_f32_e32 v21, v21
	v_rndne_f32_e32 v22, v22
	v_cvt_i32_f32_e32 v19, v19
	v_cvt_i32_f32_sdwa v21, v21 dst_sel:WORD_1 dst_unused:UNUSED_PAD src0_sel:DWORD
	v_cvt_i32_f32_e32 v22, v22
	v_lshlrev_b32_e32 v3, 8, v3
	v_and_b32_e32 v3, 0xff00, v3
	v_and_b32_e32 v4, 0xff0000, v4
	v_perm_b32 v2, v5, v2, s21
	v_or3_b32 v2, v2, v3, v4
	v_lshlrev_b32_e32 v3, 8, v20
	v_and_b32_e32 v3, 0xff00, v3
	v_and_b32_e32 v4, 0xff0000, v21
	v_perm_b32 v5, v22, v19, s21
	v_or3_b32 v3, v5, v3, v4
	v_mul_f32_e32 v5, v18, v68
	v_mul_f32_e32 v4, v18, v67
	v_rndne_f32_e32 v5, v5
	v_mul_f32_e32 v19, v18, v69
	v_mul_f32_e32 v20, v18, v70
	v_rndne_f32_e32 v4, v4
	v_cvt_i32_f32_e32 v5, v5
	v_rndne_f32_e32 v19, v19
	v_rndne_f32_e32 v20, v20
	v_mul_f32_e32 v6, v18, v6
	v_cvt_i32_f32_e32 v4, v4
	v_cvt_i32_f32_sdwa v19, v19 dst_sel:WORD_1 dst_unused:UNUSED_PAD src0_sel:DWORD
; #define LAS __attribute__((address_space(3)))
; __device__ __forceinline__ float bflo(unsigned w) { return __uint_as_float(w << 16); }
; __device__ __forceinline__ float bfhi(unsigned w) { return __uint_as_float(w & 0xffff0000u); }
; __device__ __forceinline__ float wave_sum(float v) { v = dpp_add16(v); return (rdlane(v, 0) + rdlane(v, 16)) + (rdlane(v, 32) + rdlane(v, 48)); }
; __device__ __forceinline__ float wave_max(float v) { v = dpp_max16(v); return fmaxf(fmaxf(rdlane(v, 0), rdlane(v, 16)), fmaxf(rdlane(v, 32), rdlane(v, 48))); }
; __device__ __forceinline__ void p12_peer(Frame& F) {
;     ...
;     for (int i = 0; i < 4; ++i) {
;         const int t = F.gw + i * F.NGW; v4u xp[8]; float mxa = 0.f;
; #pragma unroll
;         for (int j = 0; j < 8; ++j) { xp[j] = ((const v4u*)(HN + (size_t)t * D_))[F.lane + 64 * j];
;             mxa = fmaxf(fmaxf(fmaxf(mxa, fmaxf(fabsf(bflo(xp[j].x)), fabsf(bfhi(xp[j].x)))), fmaxf(fabsf(bflo(xp[j].y)), fabsf(bfhi(xp[j].y)))), fmaxf(fmaxf(fabsf(bflo(xp[j].z)), fabsf(bfhi(xp[j].z))), fmaxf(fabsf(bflo(xp[j].w)), fabsf(bfhi(xp[j].w))))); }
;         mxa = wave_max(mxa); const float inv = mxa > 0.f ? 127.0f / mxa : 0.f;
;         const float rsn = 1.0f / sqrtf(wave_sum(PSQ[(size_t)t * 64 + F.lane]) * (1.f / D_) + 1e-6f);
;         sx[i] = mxa * rsn * (1.0f / 127.0f);
; #pragma unroll
;         for (int j = 0; j < 8; ++j) {
;             const int q0 = (int)rintf(bflo(xp[j].x) * inv), q1 = (int)rintf(bfhi(xp[j].x) * inv), q2 = (int)rintf(bflo(xp[j].y) * inv), q3 = (int)rintf(bfhi(xp[j].y) * inv);
;             const int q4 = (int)rintf(bflo(xp[j].z) * inv), q5 = (int)rintf(bfhi(xp[j].z) * inv), q6 = (int)rintf(bflo(xp[j].w) * inv), q7 = (int)rintf(bfhi(xp[j].w) * inv);
;             *(LAS v2u*)(XQ + i * 4096 + 8 * (F.lane + 64 * j)) = (v2u){(unsigned)((q0 & 0xff) | ((q1 & 0xff) << 8) | ((q2 & 0xff) << 16) | (q3 << 24)), (unsigned)((q4 & 0xff) | ((q5 & 0xff) << 8) | ((q6 & 0xff) << 16) | (q7 << 24))}; }
;         EL[i * 128 + F.lane] = (unsigned short)PIDX[(size_t)t * 128 + F.lane]; EL[i * 128 + 64 + F.lane] = (unsigned short)PIDX[(size_t)t * 128 + 64 + F.lane];
	v_cvt_i32_f32_e32 v20, v20
	v_mul_f32_e32 v21, v18, v71
	v_rndne_f32_e32 v6, v6
	v_mul_f32_e32 v22, v18, v72
	v_mul_f32_e32 v7, v18, v7
	v_rndne_f32_e32 v21, v21
	v_cvt_i32_f32_e32 v6, v6
	v_rndne_f32_e32 v22, v22
	v_rndne_f32_e32 v7, v7
	v_cvt_i32_f32_e32 v21, v21
	v_cvt_i32_f32_sdwa v22, v22 dst_sel:WORD_1 dst_unused:UNUSED_PAD src0_sel:DWORD
	v_cvt_i32_f32_e32 v7, v7
	v_lshlrev_b32_e32 v5, 8, v5
	v_and_b32_e32 v5, 0xff00, v5
	v_and_b32_e32 v19, 0xff0000, v19
	v_perm_b32 v4, v20, v4, s21
	v_or3_b32 v4, v4, v5, v19
	v_lshlrev_b32_e32 v5, 8, v6
	v_and_b32_e32 v5, 0xff00, v5
	v_and_b32_e32 v6, 0xff0000, v22
	v_perm_b32 v7, v7, v21, s21
	v_or3_b32 v5, v7, v5, v6
	ds_write2st64_b64 v25, v[2:3], v[4:5] offset0:20 offset1:21
	v_mul_f32_e32 v3, v18, v8
	v_mul_f32_e32 v2, v18, v73
	v_rndne_f32_e32 v3, v3
	v_mul_f32_e32 v4, v18, v74
	v_mul_f32_e32 v5, v18, v9
	v_rndne_f32_e32 v2, v2
	v_cvt_i32_f32_e32 v3, v3
	v_rndne_f32_e32 v4, v4
	v_rndne_f32_e32 v5, v5
	v_mul_f32_e32 v7, v18, v10
	v_cvt_i32_f32_e32 v2, v2
	v_cvt_i32_f32_sdwa v4, v4 dst_sel:WORD_1 dst_unused:UNUSED_PAD src0_sel:DWORD
	v_cvt_i32_f32_e32 v5, v5
	v_mul_f32_e32 v6, v18, v75
	v_rndne_f32_e32 v7, v7
	v_mul_f32_e32 v8, v18, v76
	v_mul_f32_e32 v9, v18, v11
	v_rndne_f32_e32 v6, v6
	v_cvt_i32_f32_e32 v7, v7
	v_rndne_f32_e32 v8, v8
	v_rndne_f32_e32 v9, v9
	v_cvt_i32_f32_e32 v6, v6
	v_cvt_i32_f32_sdwa v8, v8 dst_sel:WORD_1 dst_unused:UNUSED_PAD src0_sel:DWORD
	v_cvt_i32_f32_e32 v9, v9
	v_lshlrev_b32_e32 v3, 8, v3
	v_and_b32_e32 v3, 0xff00, v3
	v_and_b32_e32 v4, 0xff0000, v4
	v_perm_b32 v2, v5, v2, s21
	v_or3_b32 v2, v2, v3, v4
	v_lshlrev_b32_e32 v3, 8, v7
	v_and_b32_e32 v3, 0xff00, v3
	v_and_b32_e32 v4, 0xff0000, v8
	v_perm_b32 v5, v9, v6, s21
	v_or3_b32 v3, v5, v3, v4
	v_mul_f32_e32 v5, v18, v12
	v_mul_f32_e32 v4, v18, v77
	v_rndne_f32_e32 v5, v5
	v_mul_f32_e32 v6, v18, v78
	v_mul_f32_e32 v7, v18, v13
	v_rndne_f32_e32 v4, v4
	v_cvt_i32_f32_e32 v5, v5
	v_rndne_f32_e32 v6, v6
	v_rndne_f32_e32 v7, v7
	v_mul_f32_e32 v9, v18, v14
	v_cvt_i32_f32_e32 v4, v4
	v_cvt_i32_f32_sdwa v6, v6 dst_sel:WORD_1 dst_unused:UNUSED_PAD src0_sel:DWORD
	v_cvt_i32_f32_e32 v7, v7
	v_mul_f32_e32 v8, v18, v79
	v_rndne_f32_e32 v9, v9
	v_mul_f32_e32 v10, v18, v80
	v_mul_f32_e32 v11, v18, v15
	v_rndne_f32_e32 v8, v8
	v_cvt_i32_f32_e32 v9, v9
	v_rndne_f32_e32 v10, v10
	v_rndne_f32_e32 v11, v11
	v_cvt_i32_f32_e32 v8, v8
	v_cvt_i32_f32_sdwa v10, v10 dst_sel:WORD_1 dst_unused:UNUSED_PAD src0_sel:DWORD
	v_cvt_i32_f32_e32 v11, v11
	v_lshlrev_b32_e32 v5, 8, v5
	v_and_b32_e32 v5, 0xff00, v5
	v_and_b32_e32 v6, 0xff0000, v6
	v_perm_b32 v4, v7, v4, s21
	v_or3_b32 v4, v4, v5, v6
	v_lshlrev_b32_e32 v5, 8, v9
	v_and_b32_e32 v5, 0xff00, v5
	v_and_b32_e32 v6, 0xff0000, v10
	v_perm_b32 v7, v11, v8, s21
	v_or3_b32 v5, v7, v5, v6
	ds_write2st64_b64 v25, v[2:3], v[4:5] offset0:22 offset1:23
	s_waitcnt vmcnt(1)
	ds_write_b16 v24, v62 offset:16896
	s_waitcnt vmcnt(0)
	ds_write_b16 v24, v63 offset:17024
	global_load_dwordx4 v[4:7], v[0:1], off
	global_load_dwordx4 v[8:11], v[0:1], off offset:1024
	global_load_dwordx4 v[12:15], v[0:1], off offset:2048
	global_load_dwordx4 v[58:61], v[0:1], off offset:3072
	v_add_co_u32_e32 v54, vcc, s28, v0
	v_lshl_add_u64 v[18:19], s[12:13], 0, v[16:17]
	s_nop 0
	v_addc_co_u32_e32 v55, vcc, 0, v1, vcc
	s_lshl_b64 s[12:13], s[10:11], 9
	s_add_u32 s18, s18, s12
	s_addc_u32 s19, s19, s13
	v_lshl_add_u64 v[16:17], s[18:19], 0, v[16:17]
	s_add_u32 s18, s68, 0xf400000
	v_add_f32_dpp v32, v34, v34 quad_perm:[1,0,3,2] row_mask:0xf bank_mask:0xf bound_ctrl:1
	s_waitcnt vmcnt(3)
	v_lshlrev_b32_e32 v21, 16, v4
	v_and_b32_e32 v20, 0xffff0000, v4
	v_max_f32_e64 v2, |v20|, |v20|
	v_max_f32_e64 v3, |v21|, |v21|
	v_max_f32_e32 v4, v3, v2
	global_load_dwordx4 v[0:3], v[54:55], off
	v_lshlrev_b32_e32 v39, 16, v5
	v_and_b32_e32 v36, 0xffff0000, v5
	v_max_f32_e64 v5, |v36|, |v36|
	v_max_f32_e64 v22, |v39|, |v39|
	v_max_f32_e32 v5, v22, v5
	v_lshlrev_b32_e32 v30, 16, v7
	v_and_b32_e32 v28, 0xffff0000, v7
	v_max3_f32 v26, v4, 0, v5
	v_max_f32_e64 v4, |v28|, |v28|
	v_max_f32_e64 v5, |v30|, |v30|
	v_lshlrev_b32_e32 v40, 16, v6
	v_and_b32_e32 v37, 0xffff0000, v6
	v_max_f32_e32 v4, v5, v4
	v_max3_f32 v27, |v40|, |v37|, v4
	s_waitcnt vmcnt(3)
	v_lshlrev_b32_e32 v23, 16, v8
	v_and_b32_e32 v22, 0xffff0000, v8
	global_load_dwordx4 v[4:7], v[54:55], off offset:1024
	v_max_f32_e64 v8, |v22|, |v22|
	v_max_f32_e64 v29, |v23|, |v23|
	v_max_f32_e32 v8, v29, v8
	v_lshlrev_b32_e32 v46, 16, v9
	v_and_b32_e32 v43, 0xffff0000, v9
	v_lshlrev_b32_e32 v41, 16, v11
	v_and_b32_e32 v38, 0xffff0000, v11
	v_max3_f32 v8, v26, v27, v8
	v_max_f32_e64 v9, |v43|, |v43|
	v_max_f32_e64 v26, |v46|, |v46|
	v_lshlrev_b32_e32 v44, 16, v10
	v_and_b32_e32 v42, 0xffff0000, v10
	v_max_f32_e64 v10, |v38|, |v38|
	v_max_f32_e64 v11, |v41|, |v41|
	v_max_f32_e32 v9, v26, v9
	v_max_f32_e32 v10, v11, v10
	s_waitcnt vmcnt(3)
	v_lshlrev_b32_e32 v27, 16, v12
	v_and_b32_e32 v26, 0xffff0000, v12
	v_max3_f32 v10, |v44|, |v42|, v10
	v_max_f32_e64 v12, |v26|, |v26|
	v_max_f32_e64 v31, |v27|, |v27|
	v_lshlrev_b32_e32 v51, 16, v13
	v_and_b32_e32 v48, 0xffff0000, v13
	v_max3_f32 v29, v8, v9, v10
	global_load_dwordx4 v[8:11], v[54:55], off offset:2048
	v_max_f32_e32 v12, v31, v12
	v_max_f32_e64 v13, |v48|, |v48|
	v_max_f32_e64 v31, |v51|, |v51|
	v_max_f32_e32 v13, v31, v13
	v_lshlrev_b32_e32 v47, 16, v15
	v_and_b32_e32 v45, 0xffff0000, v15
	v_max3_f32 v35, v29, v12, v13
	v_max_f32_e64 v12, |v45|, |v45|
	v_max_f32_e64 v13, |v47|, |v47|
	v_lshlrev_b32_e32 v52, 16, v14
	v_and_b32_e32 v49, 0xffff0000, v14
	v_max_f32_e32 v12, v13, v12
	v_max3_f32 v50, |v52|, |v49|, v12
	global_load_dwordx4 v[12:15], v[54:55], off offset:3072
	s_waitcnt vmcnt(4)
; __device__ __forceinline__ float bflo(unsigned w) { return __uint_as_float(w << 16); }
; __device__ __forceinline__ float bfhi(unsigned w) { return __uint_as_float(w & 0xffff0000u); }
; __device__ __forceinline__ float wave_sum(float v) { v = dpp_add16(v); return (rdlane(v, 0) + rdlane(v, 16)) + (rdlane(v, 32) + rdlane(v, 48)); }
; __device__ __forceinline__ float wave_max(float v) { v = dpp_max16(v); return fmaxf(fmaxf(rdlane(v, 0), rdlane(v, 16)), fmaxf(rdlane(v, 32), rdlane(v, 48))); }
; __device__ __forceinline__ void p12_peer(Frame& F) {
;     ...
;         const int t = F.gw + i * F.NGW; v4u xp[8]; float mxa = 0.f;
; #pragma unroll
;         for (int j = 0; j < 8; ++j) { xp[j] = ((const v4u*)(HN + (size_t)t * D_))[F.lane + 64 * j];
;             mxa = fmaxf(fmaxf(fmaxf(mxa, fmaxf(fabsf(bflo(xp[j].x)), fabsf(bfhi(xp[j].x)))), fmaxf(fabsf(bflo(xp[j].y)), fabsf(bfhi(xp[j].y)))), fmaxf(fmaxf(fabsf(bflo(xp[j].z)), fabsf(bfhi(xp[j].z))), fmaxf(fabsf(bflo(xp[j].w)), fabsf(bfhi(xp[j].w))))); }
;         mxa = wave_max(mxa); const float inv = mxa > 0.f ? 127.0f / mxa : 0.f;
;         const float rsn = 1.0f / sqrtf(wave_sum(PSQ[(size_t)t * 64 + F.lane]) * (1.f / D_) + 1e-6f);
;         sx[i] = mxa * rsn * (1.0f / 127.0f);
	v_lshlrev_b32_e32 v31, 16, v58
	v_and_b32_e32 v29, 0xffff0000, v58
	v_max_f32_e64 v53, |v29|, |v29|
	v_max_f32_e64 v54, |v31|, |v31|
	v_max_f32_e32 v53, v54, v53
	v_lshlrev_b32_e32 v57, 16, v59
	v_and_b32_e32 v55, 0xffff0000, v59
	v_max3_f32 v35, v35, v50, v53
	v_max_f32_e64 v50, |v55|, |v55|
	v_max_f32_e64 v53, |v57|, |v57|
	v_max_f32_e32 v58, v53, v50
	v_lshlrev_b32_e32 v53, 16, v61
	v_and_b32_e32 v50, 0xffff0000, v61
	v_lshlrev_b32_e32 v56, 16, v60
	v_and_b32_e32 v54, 0xffff0000, v60
	v_max_f32_e64 v59, |v50|, |v50|
	v_max_f32_e64 v60, |v53|, |v53|
	v_max_f32_e32 v59, v60, v59
	v_max3_f32 v59, |v56|, |v54|, v59
	v_max3_f32 v58, v35, v58, v59
	global_load_dword v35, v[18:19], off
	global_load_dword v59, v[16:17], off
	global_load_dword v60, v[16:17], off offset:256
	v_add_f32_dpp v32, v32, v32 quad_perm:[2,3,0,1] row_mask:0xf bank_mask:0xf bound_ctrl:1
	s_waitcnt vmcnt(6)
	v_lshlrev_b32_e32 v16, 16, v0
	v_and_b32_e32 v17, 0xffff0000, v0
	v_max_f32_e64 v0, |v17|, |v17|
	v_max_f32_e64 v18, |v16|, |v16|
	v_max_f32_e32 v0, v18, v0
	v_lshlrev_b32_e32 v18, 16, v1
	v_and_b32_e32 v19, 0xffff0000, v1
	v_max_f32_e64 v1, |v19|, |v19|
	v_max_f32_e64 v61, |v18|, |v18|
	v_max_f32_e32 v1, v61, v1
	v_lshlrev_b32_e32 v62, 16, v3
	v_and_b32_e32 v63, 0xffff0000, v3
	v_max3_f32 v0, v58, v0, v1
	v_lshlrev_b32_e32 v58, 16, v2
	v_and_b32_e32 v61, 0xffff0000, v2
	v_max_f32_e64 v1, |v63|, |v63|
	v_max_f32_e64 v2, |v62|, |v62|
	s_waitcnt vmcnt(5)
	v_lshlrev_b32_e32 v64, 16, v4
	v_and_b32_e32 v4, 0xffff0000, v4
	v_max_f32_e32 v1, v2, v1
	v_max_f32_e64 v2, |v4|, |v4|
	v_max_f32_e64 v3, |v64|, |v64|
	v_max3_f32 v1, |v58|, |v61|, v1
	v_max_f32_e32 v2, v3, v2
	v_lshlrev_b32_e32 v65, 16, v5
	v_and_b32_e32 v5, 0xffff0000, v5
	v_max3_f32 v0, v0, v1, v2
	v_max_f32_e64 v1, |v5|, |v5|
	v_max_f32_e64 v2, |v65|, |v65|
	v_lshlrev_b32_e32 v67, 16, v7
	v_and_b32_e32 v7, 0xffff0000, v7
	v_max_f32_e32 v1, v2, v1
	v_max_f32_e64 v2, |v7|, |v7|
	v_max_f32_e64 v3, |v67|, |v67|
	v_lshlrev_b32_e32 v66, 16, v6
	v_and_b32_e32 v6, 0xffff0000, v6
	v_max_f32_e32 v2, v3, v2
	v_max3_f32 v2, |v66|, |v6|, v2
	v_max3_f32 v0, v0, v1, v2
	v_add_f32_dpp v32, v32, v32 row_half_mirror row_mask:0xf bank_mask:0xf bound_ctrl:1
	s_waitcnt vmcnt(4)
	v_lshlrev_b32_e32 v68, 16, v8
	v_and_b32_e32 v8, 0xffff0000, v8
	v_max_f32_e64 v1, |v8|, |v8|
	v_max_f32_e64 v2, |v68|, |v68|
	v_lshlrev_b32_e32 v69, 16, v9
	v_and_b32_e32 v9, 0xffff0000, v9
	v_max_f32_e32 v1, v2, v1
	v_max_f32_e64 v2, |v9|, |v9|
	v_max_f32_e64 v3, |v69|, |v69|
	v_max_f32_e32 v2, v3, v2
	v_lshlrev_b32_e32 v71, 16, v11
	v_and_b32_e32 v11, 0xffff0000, v11
	v_max3_f32 v0, v0, v1, v2
	v_max_f32_e64 v1, |v11|, |v11|
	v_max_f32_e64 v2, |v71|, |v71|
	s_waitcnt vmcnt(3)
	v_lshlrev_b32_e32 v72, 16, v12
	v_and_b32_e32 v12, 0xffff0000, v12
	v_lshlrev_b32_e32 v70, 16, v10
	v_and_b32_e32 v10, 0xffff0000, v10
	v_max_f32_e32 v1, v2, v1
	v_max_f32_e64 v2, |v12|, |v12|
	v_max_f32_e64 v3, |v72|, |v72|
	v_max3_f32 v1, |v70|, |v10|, v1
	v_max_f32_e32 v2, v3, v2
	v_lshlrev_b32_e32 v73, 16, v13
	v_and_b32_e32 v13, 0xffff0000, v13
	v_max3_f32 v0, v0, v1, v2
	v_max_f32_e64 v1, |v13|, |v13|
	v_max_f32_e64 v2, |v73|, |v73|
	v_lshlrev_b32_e32 v75, 16, v15
	v_and_b32_e32 v15, 0xffff0000, v15
	v_max_f32_e32 v1, v2, v1
	v_max_f32_e64 v2, |v15|, |v15|
	v_max_f32_e64 v3, |v75|, |v75|
	v_lshlrev_b32_e32 v74, 16, v14
	v_and_b32_e32 v14, 0xffff0000, v14
	v_max_f32_e32 v2, v3, v2
	v_max3_f32 v2, |v74|, |v14|, v2
	v_max3_f32 v0, v0, v1, v2
	v_mov_b32_e32 v1, 0
	v_add_f32_dpp v32, v32, v32 row_mirror row_mask:0xf bank_mask:0xf bound_ctrl:1
	s_nop 0
	v_mov_b32_dpp v1, v0 quad_perm:[1,0,3,2] row_mask:0xf bank_mask:0xf
	v_max_f32_e32 v1, v1, v1
	v_max_f32_e32 v0, v0, v1
	v_mov_b32_e32 v1, 0
	v_readlane_b32 s31, v32, 16
	v_readlane_b32 s30, v32, 32
	v_mov_b32_dpp v1, v0 quad_perm:[2,3,0,1] row_mask:0xf bank_mask:0xf
	v_max_f32_e32 v1, v1, v1
	v_max_f32_e32 v0, v0, v1
	v_mov_b32_e32 v1, 0
	v_readlane_b32 s33, v32, 48
	s_nop 0
	v_mov_b32_dpp v1, v0 row_half_mirror row_mask:0xf bank_mask:0xf
	v_max_f32_e32 v1, v1, v1
	v_max_f32_e32 v0, v0, v1
	v_mov_b32_e32 v1, 0
	s_nop 1
	v_mov_b32_dpp v1, v0 row_mirror row_mask:0xf bank_mask:0xf
	v_max_f32_e32 v1, v1, v1
	v_max_f32_e32 v0, v0, v1
	s_nop 0
	v_readlane_b32 s23, v0, 32
	v_readlane_b32 s28, v0, 48
	v_readlane_b32 s19, v0, 0
	v_readlane_b32 s22, v0, 16
	v_max_f32_e64 v0, s28, s28
	v_max_f32_e64 v1, s23, s23
	v_max_f32_e32 v0, v1, v0
	v_mov_b32_e32 v1, s22
	v_max3_f32 v160, s19, v1, v0
	v_div_scale_f32 v0, s[22:23], v160, v160, s29
	v_rcp_f32_e32 v1, v0
	s_addc_u32 s19, s69, 0
	v_fma_f32 v2, -v0, v1, 1.0
	v_fmac_f32_e32 v1, v2, v1
	v_div_scale_f32 v2, vcc, s29, v160, s29
	v_mul_f32_e32 v3, v2, v1
	v_fma_f32 v76, -v0, v3, v2
	v_fmac_f32_e32 v3, v76, v1
	v_fma_f32 v0, -v0, v3, v2
	v_div_fmas_f32 v0, v0, v1, v3
	v_div_fixup_f32 v0, v0, v160, s29
	v_cmp_lt_f32_e32 vcc, 0, v160
	v_readlane_b32 s29, v32, 0
	s_waitcnt vmcnt(2)
; #define LAS __attribute__((address_space(3)))
; __device__ __forceinline__ float bflo(unsigned w) { return __uint_as_float(w << 16); }
; __device__ __forceinline__ float bfhi(unsigned w) { return __uint_as_float(w & 0xffff0000u); }
; __device__ __forceinline__ void p12_peer(Frame& F) {
;     ...
;         sx[i] = mxa * rsn * (1.0f / 127.0f);
; #pragma unroll
;         for (int j = 0; j < 8; ++j) {
;             const int q0 = (int)rintf(bflo(xp[j].x) * inv), q1 = (int)rintf(bfhi(xp[j].x) * inv), q2 = (int)rintf(bflo(xp[j].y) * inv), q3 = (int)rintf(bfhi(xp[j].y) * inv);
;             const int q4 = (int)rintf(bflo(xp[j].z) * inv), q5 = (int)rintf(bfhi(xp[j].z) * inv), q6 = (int)rintf(bflo(xp[j].w) * inv), q7 = (int)rintf(bfhi(xp[j].w) * inv);
;             *(LAS v2u*)(XQ + i * 4096 + 8 * (F.lane + 64 * j)) = (v2u){(unsigned)((q0 & 0xff) | ((q1 & 0xff) << 8) | ((q2 & 0xff) << 16) | (q3 << 24)), (unsigned)((q4 & 0xff) | ((q5 & 0xff) << 8) | ((q6 & 0xff) << 16) | (q7 << 24))}; }
	v_add_f32_dpp v32, v35, v35 quad_perm:[1,0,3,2] row_mask:0xf bank_mask:0xf bound_ctrl:1
	v_cndmask_b32_e32 v76, 0, v0, vcc
	v_mul_f32_e32 v1, v76, v20
	v_mul_f32_e32 v0, v76, v21
	v_rndne_f32_e32 v1, v1
	v_mul_f32_e32 v2, v76, v39
	v_mul_f32_e32 v3, v76, v36
	v_rndne_f32_e32 v0, v0
	v_cvt_i32_f32_e32 v1, v1
	v_rndne_f32_e32 v2, v2
	v_rndne_f32_e32 v3, v3
	v_mul_f32_e32 v21, v76, v37
	v_cvt_i32_f32_e32 v0, v0
	v_cvt_i32_f32_sdwa v2, v2 dst_sel:WORD_1 dst_unused:UNUSED_PAD src0_sel:DWORD
	v_cvt_i32_f32_e32 v3, v3
	v_mul_f32_e32 v20, v76, v40
	v_rndne_f32_e32 v21, v21
	v_mul_f32_e32 v30, v76, v30
	v_mul_f32_e32 v28, v76, v28
	v_rndne_f32_e32 v20, v20
	v_cvt_i32_f32_e32 v21, v21
	v_rndne_f32_e32 v30, v30
	v_rndne_f32_e32 v28, v28
	v_cvt_i32_f32_e32 v20, v20
	v_cvt_i32_f32_sdwa v30, v30 dst_sel:WORD_1 dst_unused:UNUSED_PAD src0_sel:DWORD
	v_cvt_i32_f32_e32 v28, v28
	v_lshlrev_b32_e32 v1, 8, v1
	v_and_b32_e32 v1, 0xff00, v1
	v_and_b32_e32 v2, 0xff0000, v2
	v_perm_b32 v0, v3, v0, s21
	v_or3_b32 v0, v0, v1, v2
	v_lshlrev_b32_e32 v1, 8, v21
	v_and_b32_e32 v1, 0xff00, v1
	v_and_b32_e32 v2, 0xff0000, v30
	v_perm_b32 v3, v28, v20, s21
	v_or3_b32 v1, v3, v1, v2
	v_mul_f32_e32 v3, v76, v22
	v_mul_f32_e32 v2, v76, v23
	v_rndne_f32_e32 v3, v3
	v_mul_f32_e32 v20, v76, v46
	v_mul_f32_e32 v21, v76, v43
	v_rndne_f32_e32 v2, v2
	v_cvt_i32_f32_e32 v3, v3
	v_rndne_f32_e32 v20, v20
	v_rndne_f32_e32 v21, v21
	v_mul_f32_e32 v23, v76, v42
	v_cvt_i32_f32_e32 v2, v2
	v_cvt_i32_f32_sdwa v20, v20 dst_sel:WORD_1 dst_unused:UNUSED_PAD src0_sel:DWORD
	v_cvt_i32_f32_e32 v21, v21
	v_mul_f32_e32 v22, v76, v44
	v_rndne_f32_e32 v23, v23
	v_mul_f32_e32 v28, v76, v41
	v_mul_f32_e32 v30, v76, v38
	v_rndne_f32_e32 v22, v22
	v_cvt_i32_f32_e32 v23, v23
	v_rndne_f32_e32 v28, v28
	v_rndne_f32_e32 v30, v30
	v_cvt_i32_f32_e32 v22, v22
	v_cvt_i32_f32_sdwa v28, v28 dst_sel:WORD_1 dst_unused:UNUSED_PAD src0_sel:DWORD
	v_cvt_i32_f32_e32 v30, v30
	v_lshlrev_b32_e32 v3, 8, v3
	v_and_b32_e32 v3, 0xff00, v3
	v_and_b32_e32 v20, 0xff0000, v20
	v_perm_b32 v2, v21, v2, s21
	v_or3_b32 v2, v2, v3, v20
	v_lshlrev_b32_e32 v3, 8, v23
	v_and_b32_e32 v3, 0xff00, v3
	v_and_b32_e32 v20, 0xff0000, v28
	v_perm_b32 v21, v30, v22, s21
	v_or3_b32 v3, v21, v3, v20
	ds_write2st64_b64 v25, v[0:1], v[2:3] offset0:24 offset1:25
	v_mul_f32_e32 v1, v76, v26
	v_mul_f32_e32 v0, v76, v27
	v_rndne_f32_e32 v1, v1
	v_mul_f32_e32 v2, v76, v51
	v_mul_f32_e32 v3, v76, v48
	v_rndne_f32_e32 v0, v0
	v_cvt_i32_f32_e32 v1, v1
	v_rndne_f32_e32 v2, v2
	v_rndne_f32_e32 v3, v3
	v_mul_f32_e32 v21, v76, v49
	v_cvt_i32_f32_e32 v0, v0
	v_cvt_i32_f32_sdwa v2, v2 dst_sel:WORD_1 dst_unused:UNUSED_PAD src0_sel:DWORD
	v_cvt_i32_f32_e32 v3, v3
	v_mul_f32_e32 v20, v76, v52
	v_rndne_f32_e32 v21, v21
	v_mul_f32_e32 v22, v76, v47
	v_mul_f32_e32 v23, v76, v45
	v_rndne_f32_e32 v20, v20
	v_cvt_i32_f32_e32 v21, v21
	v_rndne_f32_e32 v22, v22
	v_rndne_f32_e32 v23, v23
	v_cvt_i32_f32_e32 v20, v20
	v_cvt_i32_f32_sdwa v22, v22 dst_sel:WORD_1 dst_unused:UNUSED_PAD src0_sel:DWORD
	v_cvt_i32_f32_e32 v23, v23
	v_lshlrev_b32_e32 v1, 8, v1
	v_and_b32_e32 v1, 0xff00, v1
	v_and_b32_e32 v2, 0xff0000, v2
	v_perm_b32 v0, v3, v0, s21
	v_or3_b32 v0, v0, v1, v2
	v_lshlrev_b32_e32 v1, 8, v21
	v_and_b32_e32 v1, 0xff00, v1
	v_and_b32_e32 v2, 0xff0000, v22
	v_perm_b32 v3, v23, v20, s21
	v_or3_b32 v1, v3, v1, v2
	v_mul_f32_e32 v3, v76, v29
	v_mul_f32_e32 v2, v76, v31
	v_rndne_f32_e32 v3, v3
	v_mul_f32_e32 v20, v76, v57
	v_mul_f32_e32 v21, v76, v55
	v_rndne_f32_e32 v2, v2
	v_cvt_i32_f32_e32 v3, v3
	v_rndne_f32_e32 v20, v20
	v_rndne_f32_e32 v21, v21
	v_mul_f32_e32 v23, v76, v54
	v_cvt_i32_f32_e32 v2, v2
	v_cvt_i32_f32_sdwa v20, v20 dst_sel:WORD_1 dst_unused:UNUSED_PAD src0_sel:DWORD
	v_cvt_i32_f32_e32 v21, v21
	v_mul_f32_e32 v22, v76, v56
	v_rndne_f32_e32 v23, v23
	v_mul_f32_e32 v26, v76, v53
	v_mul_f32_e32 v27, v76, v50
	v_rndne_f32_e32 v22, v22
	v_cvt_i32_f32_e32 v23, v23
	v_rndne_f32_e32 v26, v26
	v_rndne_f32_e32 v27, v27
	v_cvt_i32_f32_e32 v22, v22
	v_cvt_i32_f32_sdwa v26, v26 dst_sel:WORD_1 dst_unused:UNUSED_PAD src0_sel:DWORD
	v_cvt_i32_f32_e32 v27, v27
	v_lshlrev_b32_e32 v3, 8, v3
	v_and_b32_e32 v3, 0xff00, v3
	v_and_b32_e32 v20, 0xff0000, v20
	v_perm_b32 v2, v21, v2, s21
	v_or3_b32 v2, v2, v3, v20
	v_lshlrev_b32_e32 v3, 8, v23
	v_and_b32_e32 v3, 0xff00, v3
	v_and_b32_e32 v20, 0xff0000, v26
	v_perm_b32 v21, v27, v22, s21
	v_or3_b32 v3, v21, v3, v20
	ds_write2st64_b64 v25, v[0:1], v[2:3] offset0:26 offset1:27
	v_mul_f32_e32 v1, v76, v17
	v_mul_f32_e32 v0, v76, v16
	v_rndne_f32_e32 v1, v1
	v_mul_f32_e32 v2, v76, v18
	v_mul_f32_e32 v3, v76, v19
	v_rndne_f32_e32 v0, v0
	v_cvt_i32_f32_e32 v1, v1
	v_rndne_f32_e32 v2, v2
	v_rndne_f32_e32 v3, v3
	v_mul_f32_e32 v17, v76, v61
	v_cvt_i32_f32_e32 v0, v0
	v_cvt_i32_f32_sdwa v2, v2 dst_sel:WORD_1 dst_unused:UNUSED_PAD src0_sel:DWORD
	v_cvt_i32_f32_e32 v3, v3
	v_mul_f32_e32 v16, v76, v58
	v_rndne_f32_e32 v17, v17
	v_mul_f32_e32 v18, v76, v62
	v_mul_f32_e32 v19, v76, v63
	v_rndne_f32_e32 v16, v16
	v_cvt_i32_f32_e32 v17, v17
	v_rndne_f32_e32 v18, v18
	v_rndne_f32_e32 v19, v19
	v_cvt_i32_f32_e32 v16, v16
	v_cvt_i32_f32_sdwa v18, v18 dst_sel:WORD_1 dst_unused:UNUSED_PAD src0_sel:DWORD
	v_cvt_i32_f32_e32 v19, v19
	v_lshlrev_b32_e32 v1, 8, v1
	v_and_b32_e32 v1, 0xff00, v1
	v_and_b32_e32 v2, 0xff0000, v2
	v_perm_b32 v0, v3, v0, s21
	v_or3_b32 v0, v0, v1, v2
	v_lshlrev_b32_e32 v1, 8, v17
	v_and_b32_e32 v1, 0xff00, v1
	v_and_b32_e32 v2, 0xff0000, v18
	v_perm_b32 v3, v19, v16, s21
	v_or3_b32 v1, v3, v1, v2
; #define LAS __attribute__((address_space(3)))
; __device__ __forceinline__ float bflo(unsigned w) { return __uint_as_float(w << 16); }
; __device__ __forceinline__ float bfhi(unsigned w) { return __uint_as_float(w & 0xffff0000u); }
; #define P12_ISSUE(c_, i_, h_, CW_, SC_) do { _Pragma("unroll") for (int bb = 0; bb < 8; ++bb) { const unsigned ro = (unsigned)(c_) * 16384u + (unsigned)EL[(i_) * 128 + ((h_) * 8 + bb) * 8 + g8]; \
;         CW_[bb] = *(const v4u*)(U4 + (size_t)(ro * 128u + 16u * (unsigned)k8)); SC_[bb] = USS[(size_t)(ro * 8u + (unsigned)k8)]; } } while (0)
; #define P12_COMP(i_, h_, CW_, SC_) do { _Pragma("unroll") for (int bb = 0; bb < 8; ++bb) { int a0 = 0, a1 = 0; P12_U4(CW_[bb].x, xa.x, xa.y, a0); P12_U4(CW_[bb].y, xa.z, xa.w, a1); P12_U4(CW_[bb].z, xb.x, xb.y, a0); P12_U4(CW_[bb].w, xb.z, xb.w, a1); \
;         psum[(i_)][(h_) * 8 + bb] += __uint_as_float(SC_[bb] << 16) * (float)((a0 + a1) - xo); } } while (0)
; #define P12_BAR() asm volatile("" ::: "memory")
; __device__ __forceinline__ void p12_peer(Frame& F) {
;     ...
;         for (int j = 0; j < 8; ++j) {
;             const int q0 = (int)rintf(bflo(xp[j].x) * inv), q1 = (int)rintf(bfhi(xp[j].x) * inv), q2 = (int)rintf(bflo(xp[j].y) * inv), q3 = (int)rintf(bfhi(xp[j].y) * inv);
;             const int q4 = (int)rintf(bflo(xp[j].z) * inv), q5 = (int)rintf(bfhi(xp[j].z) * inv), q6 = (int)rintf(bflo(xp[j].w) * inv), q7 = (int)rintf(bfhi(xp[j].w) * inv);
;             *(LAS v2u*)(XQ + i * 4096 + 8 * (F.lane + 64 * j)) = (v2u){(unsigned)((q0 & 0xff) | ((q1 & 0xff) << 8) | ((q2 & 0xff) << 16) | (q3 << 24)), (unsigned)((q4 & 0xff) | ((q5 & 0xff) << 8) | ((q6 & 0xff) << 16) | (q7 << 24))}; }
;         EL[i * 128 + F.lane] = (unsigned short)PIDX[(size_t)t * 128 + F.lane]; EL[i * 128 + 64 + F.lane] = (unsigned short)PIDX[(size_t)t * 128 + 64 + F.lane];
;     ...
;     { v4u cwA[8], cwB[8]; unsigned scA[8], scB[8]; v4u xa, xb; int xo;
;       P12_ISSUE(0, 0, 0, cwA, scA);
; _Pragma("nounroll")
;       for (int c = 0; c < 16; ++c) { const int cn = c + 1 < 16 ? c + 1 : 15;
;           P12_XQ(c, 0); P12_ISSUE(c, 0, 1, cwB, scB); P12_BAR(); P12_COMP(0, 0, cwA, scA); P12_ISSUE(c, 1, 0, cwA, scA); P12_BAR(); P12_COMP(0, 1, cwB, scB);
	v_mul_f32_e32 v3, v76, v4
	v_mul_f32_e32 v2, v76, v64
	v_rndne_f32_e32 v3, v3
	v_mul_f32_e32 v4, v76, v65
	v_mul_f32_e32 v5, v76, v5
	v_rndne_f32_e32 v2, v2
	v_cvt_i32_f32_e32 v3, v3
	v_rndne_f32_e32 v4, v4
	v_rndne_f32_e32 v5, v5
	v_mul_f32_e32 v6, v76, v6
	v_cvt_i32_f32_e32 v2, v2
	v_cvt_i32_f32_sdwa v4, v4 dst_sel:WORD_1 dst_unused:UNUSED_PAD src0_sel:DWORD
	v_cvt_i32_f32_e32 v5, v5
	v_mul_f32_e32 v16, v76, v66
	v_rndne_f32_e32 v6, v6
	v_mul_f32_e32 v17, v76, v67
	v_mul_f32_e32 v7, v76, v7
	v_rndne_f32_e32 v16, v16
	v_cvt_i32_f32_e32 v6, v6
	v_rndne_f32_e32 v17, v17
	v_rndne_f32_e32 v7, v7
	v_cvt_i32_f32_e32 v16, v16
	v_cvt_i32_f32_sdwa v17, v17 dst_sel:WORD_1 dst_unused:UNUSED_PAD src0_sel:DWORD
	v_cvt_i32_f32_e32 v7, v7
	v_lshlrev_b32_e32 v3, 8, v3
	v_and_b32_e32 v3, 0xff00, v3
	v_and_b32_e32 v4, 0xff0000, v4
	v_perm_b32 v2, v5, v2, s21
	v_or3_b32 v2, v2, v3, v4
	v_lshlrev_b32_e32 v3, 8, v6
	v_and_b32_e32 v3, 0xff00, v3
	v_and_b32_e32 v4, 0xff0000, v17
	v_perm_b32 v5, v7, v16, s21
	v_or3_b32 v3, v5, v3, v4
	ds_write2st64_b64 v25, v[0:1], v[2:3] offset0:28 offset1:29
	v_mul_f32_e32 v1, v76, v8
	v_mul_f32_e32 v0, v76, v68
	v_rndne_f32_e32 v1, v1
	v_mul_f32_e32 v2, v76, v69
	v_mul_f32_e32 v3, v76, v9
	v_rndne_f32_e32 v0, v0
	v_cvt_i32_f32_e32 v1, v1
	v_rndne_f32_e32 v2, v2
	v_rndne_f32_e32 v3, v3
	v_mul_f32_e32 v5, v76, v10
	v_cvt_i32_f32_e32 v0, v0
	v_cvt_i32_f32_sdwa v2, v2 dst_sel:WORD_1 dst_unused:UNUSED_PAD src0_sel:DWORD
	v_cvt_i32_f32_e32 v3, v3
	v_mul_f32_e32 v4, v76, v70
	v_rndne_f32_e32 v5, v5
	v_mul_f32_e32 v6, v76, v71
	v_mul_f32_e32 v7, v76, v11
	v_rndne_f32_e32 v4, v4
	v_cvt_i32_f32_e32 v5, v5
	v_rndne_f32_e32 v6, v6
	v_rndne_f32_e32 v7, v7
	v_cvt_i32_f32_e32 v4, v4
	v_cvt_i32_f32_sdwa v6, v6 dst_sel:WORD_1 dst_unused:UNUSED_PAD src0_sel:DWORD
	v_cvt_i32_f32_e32 v7, v7
	v_lshlrev_b32_e32 v1, 8, v1
	v_and_b32_e32 v1, 0xff00, v1
	v_and_b32_e32 v2, 0xff0000, v2
	v_perm_b32 v0, v3, v0, s21
	v_or3_b32 v0, v0, v1, v2
	v_lshlrev_b32_e32 v1, 8, v5
	v_and_b32_e32 v1, 0xff00, v1
	v_and_b32_e32 v2, 0xff0000, v6
	v_perm_b32 v3, v7, v4, s21
	v_or3_b32 v1, v3, v1, v2
	v_mul_f32_e32 v3, v76, v12
	v_mul_f32_e32 v2, v76, v72
	v_rndne_f32_e32 v3, v3
	v_mul_f32_e32 v4, v76, v73
	v_mul_f32_e32 v5, v76, v13
	v_rndne_f32_e32 v2, v2
	v_cvt_i32_f32_e32 v3, v3
	v_rndne_f32_e32 v4, v4
	v_rndne_f32_e32 v5, v5
	v_mul_f32_e32 v7, v76, v14
	v_cvt_i32_f32_e32 v2, v2
	v_cvt_i32_f32_sdwa v4, v4 dst_sel:WORD_1 dst_unused:UNUSED_PAD src0_sel:DWORD
	v_cvt_i32_f32_e32 v5, v5
	v_mul_f32_e32 v6, v76, v74
	v_rndne_f32_e32 v7, v7
	v_mul_f32_e32 v8, v76, v75
	v_mul_f32_e32 v9, v76, v15
	v_rndne_f32_e32 v6, v6
	v_cvt_i32_f32_e32 v7, v7
	v_rndne_f32_e32 v8, v8
	v_rndne_f32_e32 v9, v9
	v_cvt_i32_f32_e32 v6, v6
	v_cvt_i32_f32_sdwa v8, v8 dst_sel:WORD_1 dst_unused:UNUSED_PAD src0_sel:DWORD
	v_cvt_i32_f32_e32 v9, v9
	v_lshlrev_b32_e32 v3, 8, v3
	v_and_b32_e32 v3, 0xff00, v3
	v_and_b32_e32 v4, 0xff0000, v4
	v_perm_b32 v2, v5, v2, s21
	v_or3_b32 v2, v2, v3, v4
	v_lshlrev_b32_e32 v3, 8, v7
	v_and_b32_e32 v3, 0xff00, v3
	v_and_b32_e32 v4, 0xff0000, v8
	v_perm_b32 v5, v9, v6, s21
	v_or3_b32 v3, v5, v3, v4
	ds_write2st64_b64 v25, v[0:1], v[2:3] offset0:30 offset1:31
	s_waitcnt vmcnt(1)
	ds_write_b16 v24, v59 offset:17152
	s_waitcnt vmcnt(0)
	ds_write_b16 v24, v60 offset:17280
	s_waitcnt lgkmcnt(0)
	v_lshlrev_b32_e32 v248, 1, v95
	s_mov_b32 s48, 0x7060302
	ds_read_u16 v0, v93 offset:16384
	ds_read_u16 v1, v93 offset:16400
	ds_read_u16 v2, v93 offset:16416
	ds_read_u16 v3, v93 offset:16432
	ds_read_u16 v4, v93 offset:16448
	ds_read_u16 v5, v93 offset:16464
	ds_read_u16 v6, v93 offset:16480
	ds_read_u16 v36, v93 offset:16496
	s_waitcnt lgkmcnt(7)
	v_lshl_or_b32 v7, v0, 5, v248
	s_waitcnt lgkmcnt(5)
	v_lshl_or_b32 v8, v2, 5, v248
	s_waitcnt lgkmcnt(3)
	v_lshl_or_b32 v9, v4, 5, v248
	s_waitcnt lgkmcnt(1)
	v_lshl_or_b32 v10, v6, 5, v248
	global_load_dword v184, v7, s[18:19]
	global_load_dword v186, v8, s[18:19]
	global_load_dword v188, v9, s[18:19]
	global_load_dword v190, v10, s[18:19]
	s_waitcnt lgkmcnt(0)
	v_lshl_or_b32 v10, v36, 5, v248
	v_lshl_or_b32 v0, v0, 7, v165
	v_lshl_or_b32 v7, v1, 5, v248
	v_lshl_or_b32 v8, v3, 5, v248
	v_lshl_or_b32 v9, v5, 5, v248
	global_load_dword v191, v10, s[18:19]
	global_load_dword v189, v9, s[18:19]
	global_load_dword v187, v8, s[18:19]
	global_load_dword v185, v7, s[18:19]
	global_load_dwordx4 v[28:31], v0, s[0:1]
	v_lshl_or_b32 v0, v1, 7, v165
	global_load_dwordx4 v[24:27], v0, s[0:1]
	v_lshl_or_b32 v0, v2, 7, v165
	global_load_dwordx4 v[20:23], v0, s[0:1]
	v_lshl_or_b32 v0, v3, 7, v165
	global_load_dwordx4 v[16:19], v0, s[0:1]
	v_lshl_or_b32 v0, v4, 7, v165
	global_load_dwordx4 v[12:15], v0, s[0:1]
	v_lshl_or_b32 v0, v5, 7, v165
	global_load_dwordx4 v[8:11], v0, s[0:1]
	v_lshl_or_b32 v0, v6, 7, v165
	global_load_dwordx4 v[4:7], v0, s[0:1]
	v_lshl_or_b32 v0, v36, 7, v165
	global_load_dwordx4 v[0:3], v0, s[0:1]
	v_add_f32_dpp v32, v32, v32 quad_perm:[2,3,0,1] row_mask:0xf bank_mask:0xf bound_ctrl:1
	s_waitcnt vmcnt(11)
	v_perm_b32 v40, v190, v191, s43
	v_add_f32_dpp v32, v32, v32 row_half_mirror row_mask:0xf bank_mask:0xf bound_ctrl:1
	s_waitcnt vmcnt(10)
	v_perm_b32 v41, v188, v189, s43
	s_waitcnt vmcnt(9)
	v_perm_b32 v42, v186, v187, s43
	v_add_f32_dpp v32, v32, v32 row_mirror row_mask:0xf bank_mask:0xf bound_ctrl:1
	s_waitcnt vmcnt(8)
	v_perm_b32 v43, v184, v185, s43
	v_readlane_b32 s21, v32, 0
	v_readlane_b32 s23, v32, 16
	v_readlane_b32 s22, v32, 32
	v_readlane_b32 s28, v32, 48

; __global__ void __launch_bounds__(NWAVES * 64, 2) mk_fwd(Args args) {
	.amdhsa_kernel _Z6mk_fwd4Args
		.amdhsa_group_segment_fixed_size 0
		.amdhsa_private_segment_fixed_size 0
		.amdhsa_kernarg_size 472
		.amdhsa_user_sgpr_count 2
		.amdhsa_user_sgpr_dispatch_ptr 0
		.amdhsa_user_sgpr_queue_ptr 0
		.amdhsa_user_sgpr_kernarg_segment_ptr 1
		.amdhsa_user_sgpr_dispatch_id 0
		.amdhsa_user_sgpr_kernarg_preload_length 0
		.amdhsa_user_sgpr_kernarg_preload_offset 0
		.amdhsa_user_sgpr_private_segment_size 0
		.amdhsa_uses_dynamic_stack 0
		.amdhsa_enable_private_segment 0
		.amdhsa_system_sgpr_workgroup_id_x 1
		.amdhsa_system_sgpr_workgroup_id_y 0
		.amdhsa_system_sgpr_workgroup_id_z 0
		.amdhsa_system_sgpr_workgroup_info 0
		.amdhsa_system_vgpr_workitem_id 0
		.amdhsa_next_free_vgpr 256
		.amdhsa_next_free_sgpr 98
		.amdhsa_accum_offset 256
		.amdhsa_reserve_vcc 1
		.amdhsa_float_round_mode_32 0
		.amdhsa_float_round_mode_16_64 0
		.amdhsa_float_denorm_mode_32 3
		.amdhsa_float_denorm_mode_16_64 3
		.amdhsa_dx10_clamp 1
		.amdhsa_ieee_mode 1
		.amdhsa_fp16_overflow 0
		.amdhsa_tg_split 0
		.amdhsa_exception_fp_ieee_invalid_op 0
		.amdhsa_exception_fp_denorm_src 0
		.amdhsa_exception_fp_ieee_div_zero 0
		.amdhsa_exception_fp_ieee_overflow 0
		.amdhsa_exception_fp_ieee_underflow 0
		.amdhsa_exception_fp_ieee_inexact 0
		.amdhsa_exception_int_div_zero 0
	.end_amdhsa_kernel

; __global__ void __launch_bounds__(NWAVES * 64, 2) mk_fwd(Args args) {
amdhsa.kernels:
  - .agpr_count:     0
    .args:
      - .offset:         0
        .size:           216
        .value_kind:     by_value
      - .offset:         216
        .size:           4
        .value_kind:     hidden_block_count_x
      - .offset:         220
        .size:           4
        .value_kind:     hidden_block_count_y
      - .offset:         224
        .size:           4
        .value_kind:     hidden_block_count_z
      - .offset:         228
        .size:           2
        .value_kind:     hidden_group_size_x
      - .offset:         230
        .size:           2
        .value_kind:     hidden_group_size_y
      - .offset:         232
        .size:           2
        .value_kind:     hidden_group_size_z
      - .offset:         234
        .size:           2
        .value_kind:     hidden_remainder_x
      - .offset:         236
        .size:           2
        .value_kind:     hidden_remainder_y
      - .offset:         238
        .size:           2
        .value_kind:     hidden_remainder_z
      - .offset:         256
        .size:           8
        .value_kind:     hidden_global_offset_x
      - .offset:         264
        .size:           8
        .value_kind:     hidden_global_offset_y
      - .offset:         272
        .size:           8
        .value_kind:     hidden_global_offset_z
      - .offset:         280
        .size:           2
        .value_kind:     hidden_grid_dims
      - .offset:         336
        .size:           4
        .value_kind:     hidden_dynamic_lds_size
    .group_segment_fixed_size: 0
    .kernarg_segment_align: 8
    .kernarg_segment_size: 472
    .language:       OpenCL C
    .language_version:
      - 2
      - 0
    .max_flat_workgroup_size: 512
    .name:           _Z6mk_fwd4Args
    .private_segment_fixed_size: 0
    .sgpr_count:     104
    .sgpr_spill_count: 50
    .symbol:         _Z6mk_fwd4Args.kd
    .uniform_work_group_size: 1
    .uses_dynamic_stack: false
    .vgpr_count:     256
    .vgpr_spill_count: 0
    .wavefront_size: 64
